# P1 GEMM K-loop: last 2 of 6 LDS-DMA issues of each 6-load staging segment moved into the following MFMA block (vmcnt 8->6); saddr-form DMA
# speedup vs baseline: 1.0032x; 1.0032x over previous
.LBB0_293:
	s_lshl_b32 s8, s8, 5
	s_and_b32 s14, s8, 0x60
	s_mov_b64 s[8:9], 0x80
	s_add_i32 m0, s21, 0x18000
	v_lshl_add_u64 v[8:9], v[8:9], 0, s[8:9]
	s_lshl_b32 s11, s10, 13
	s_lshl_b32 s15, s14, 7
	s_waitcnt vmcnt(2)
	s_barrier
	global_load_lds_dwordx4 v[8:9], off
	v_lshl_add_u64 v[6:7], v[6:7], 0, s[8:9]
	s_add_i32 m0, s21, 0x1a000
	s_add_i32 s41, s21, 0x8000
	s_add_i32 s42, s21, 0xa000
	global_load_lds_dwordx4 v[6:7], off
	v_lshl_add_u64 v[2:3], v[2:3], 0, s[8:9]
	s_mov_b32 m0, s41
	s_add_u32 s12, s24, 0x40080
	global_load_lds_dwordx4 v[2:3], off
	v_lshl_add_u64 v[2:3], v[4:5], 0, s[8:9]
	s_mov_b32 m0, s42
	s_addc_u32 s13, s25, 0
	global_load_lds_dwordx4 v[2:3], off
	s_add_i32 m0, s21, 0x1c000
	global_load_lds_dwordx4 v134, s[12:13]
	v_lshl_add_u64 v[2:3], s[12:13], 0, v[130:131]
	s_add_i32 m0, s21, 0x1e000
	v_lshlrev_b32_e32 v4, 2, v222
	global_load_lds_dwordx4 v[2:3], off
	v_lshlrev_b32_e32 v2, 1, v13
	v_lshl_or_b32 v3, v222, 6, v2
	v_and_b32_e32 v4, 32, v4
	s_sext_i32_i8 s47, s4
	v_bitop3_b32 v3, v3, s11, v4 bitop3:0xde
	v_lshlrev_b32_e32 v4, 6, v0
	s_movk_i32 s4, 0x3c0
	v_and_or_b32 v2, v4, s4, v2
	v_and_b32_e32 v4, 32, v252
	v_bitop3_b32 v147, s15, v2, v4 bitop3:0xf6
	v_lshlrev_b32_e32 v2, 8, v0
	v_and_b32_e32 v2, 0x18000, v2
	v_lshlrev_b32_e32 v4, 11, v14
	v_or3_b32 v2, v11, v2, v4
	v_add_u32_e32 v138, v2, v12
	v_lshlrev_b32_e32 v2, 4, v10
	s_waitcnt vmcnt(6)
	s_cmpk_lt_u32 s5, 0x100
	v_and_b32_e32 v2, 0x38000, v2
	v_lshl_or_b32 v1, s10, 6, v222
	s_cselect_b64 s[10:11], -1, 0
	v_or3_b32 v2, v11, v2, v4
	s_add_i32 s44, 0, 0x10000
	s_add_i32 s45, 0, 0x14000
	s_ashr_i32 s43, s33, 31
	v_or_b32_e32 v150, s14, v13
	v_mov_b32_e32 v139, v135
	v_add_u32_e32 v140, v2, v12
	v_mov_b32_e32 v141, v135
	v_mov_b64_e32 v[142:143], 0x300
	v_mov_b64_e32 v[144:145], 0x2ff
	v_add_u32_e32 v151, s44, v147
	v_add_u32_e32 v152, s45, v147
	v_add_u32_e32 v153, 0, v3
	s_movk_i32 s46, 0x1800
	v_mov_b32_e32 v154, 0x3db504f3
	s_barrier
	s_waitcnt vmcnt(0)
	s_branch .LBB0_296

.LBB0_299:
	ds_read_b128 v[156:159], v151
	ds_read_b128 v[160:163], v151 offset:1024
	ds_read_b128 v[164:167], v151 offset:2048
	ds_read_b128 v[168:171], v151 offset:3072
	ds_read_b128 v[172:175], v152
	ds_read_b128 v[176:179], v152 offset:1024
	ds_read_b128 v[180:183], v152 offset:2048
	ds_read_b128 v[184:187], v152 offset:3072
	s_add_u32 s24, s22, 0xfffc0080
	s_addc_u32 s25, s23, -1
	s_cmp_eq_u32 s52, 12
	s_cselect_b32 s27, s15, s25
	s_cselect_b32 s26, s48, s24
	s_cselect_b32 s25, s13, s51
	s_cselect_b32 s24, s49, s50
	s_add_i32 m0, s21, 0xc000
	ds_read_b128 v[192:195], v153
	ds_read_b128 v[196:199], v153 offset:1024
	ds_read_b128 v[200:203], v153 offset:2048
	ds_read_b128 v[204:207], v153 offset:3072
	ds_read_b128 v[208:211], v153 offset:4096
	ds_read_b128 v[212:215], v153 offset:5120
	ds_read_b128 v[216:219], v153 offset:6144
	ds_read_b128 v[224:227], v153 offset:7168
	global_load_lds_dwordx4 v138, s[22:23]
	s_add_i32 m0, s21, 0xe000
	s_nop 0
	global_load_lds_dwordx4 v140, s[22:23]
	s_waitcnt vmcnt(8)
	s_waitcnt lgkmcnt(0)
	s_barrier
	s_setprio 1
	s_waitcnt lgkmcnt(0)
	v_mfma_f32_16x16x32_bf16 v[126:129], v[156:159], v[192:195], v[126:129]
	v_mfma_f32_16x16x32_bf16 v[122:125], v[164:167], v[192:195], v[122:125]
	v_mfma_f32_16x16x32_bf16 v[114:117], v[156:159], v[200:203], v[114:117]
	v_mfma_f32_16x16x32_bf16 v[106:109], v[164:167], v[200:203], v[106:109]
	v_mfma_f32_16x16x32_bf16 v[98:101], v[156:159], v[208:211], v[98:101]
	v_mfma_f32_16x16x32_bf16 v[90:93], v[164:167], v[208:211], v[90:93]
	v_mfma_f32_16x16x32_bf16 v[82:85], v[156:159], v[216:219], v[82:85]
	v_mfma_f32_16x16x32_bf16 v[74:77], v[164:167], v[216:219], v[74:77]
	v_mfma_f32_16x16x32_bf16 v[126:129], v[160:163], v[196:199], v[126:129]
	v_mfma_f32_16x16x32_bf16 v[122:125], v[168:171], v[196:199], v[122:125]
	v_mfma_f32_16x16x32_bf16 v[114:117], v[160:163], v[204:207], v[114:117]
	v_mfma_f32_16x16x32_bf16 v[106:109], v[168:171], v[204:207], v[106:109]
	v_mfma_f32_16x16x32_bf16 v[98:101], v[160:163], v[212:215], v[98:101]
	v_mfma_f32_16x16x32_bf16 v[90:93], v[168:171], v[212:215], v[90:93]
	v_mfma_f32_16x16x32_bf16 v[82:85], v[160:163], v[224:227], v[82:85]
	v_mfma_f32_16x16x32_bf16 v[74:77], v[168:171], v[224:227], v[74:77]
	s_setprio 0
	s_setprio 1
	v_mfma_f32_16x16x32_bf16 v[118:121], v[172:175], v[192:195], v[118:121]
	v_mfma_f32_16x16x32_bf16 v[110:113], v[180:183], v[192:195], v[110:113]
	v_mfma_f32_16x16x32_bf16 v[102:105], v[172:175], v[200:203], v[102:105]
	v_mfma_f32_16x16x32_bf16 v[94:97], v[180:183], v[200:203], v[94:97]
	v_mfma_f32_16x16x32_bf16 v[86:89], v[172:175], v[208:211], v[86:89]
	v_mfma_f32_16x16x32_bf16 v[78:81], v[180:183], v[208:211], v[78:81]
	v_mfma_f32_16x16x32_bf16 v[70:73], v[172:175], v[216:219], v[70:73]
	v_mfma_f32_16x16x32_bf16 v[66:69], v[180:183], v[216:219], v[66:69]
	v_mfma_f32_16x16x32_bf16 v[118:121], v[176:179], v[196:199], v[118:121]
	v_mfma_f32_16x16x32_bf16 v[110:113], v[184:187], v[196:199], v[110:113]
	v_mfma_f32_16x16x32_bf16 v[102:105], v[176:179], v[204:207], v[102:105]
	v_mfma_f32_16x16x32_bf16 v[94:97], v[184:187], v[204:207], v[94:97]
	v_mfma_f32_16x16x32_bf16 v[86:89], v[176:179], v[212:215], v[86:89]
	v_mfma_f32_16x16x32_bf16 v[78:81], v[184:187], v[212:215], v[78:81]
	v_mfma_f32_16x16x32_bf16 v[70:73], v[176:179], v[224:227], v[70:73]
	v_mfma_f32_16x16x32_bf16 v[66:69], v[184:187], v[224:227], v[66:69]
	s_setprio 0
	s_barrier
	s_add_i32 s53, s44, s34
	v_lshl_add_u64 v[148:149], s[24:25], 0, v[134:135]
	s_mov_b32 m0, s53
	ds_read_b128 v[192:195], v153 offset:16384
	ds_read_b128 v[196:199], v153 offset:17408
	ds_read_b128 v[200:203], v153 offset:18432
	ds_read_b128 v[204:207], v153 offset:19456
	ds_read_b128 v[208:211], v153 offset:20480
	ds_read_b128 v[212:215], v153 offset:21504
	ds_read_b128 v[216:219], v153 offset:22528
	ds_read_b128 v[224:227], v153 offset:23552
	global_load_lds_dwordx4 v[148:149], off
	s_add_i32 m0, s53, 0x2000
	s_add_u32 s54, s24, 0x40000
	v_lshl_add_u64 v[188:189], s[24:25], 0, v[130:131]
	s_addc_u32 s55, s25, 0
	s_add_i32 s53, s45, s34
	global_load_lds_dwordx4 v[188:189], off
	s_mov_b32 m0, s53
	v_lshl_add_u64 v[220:221], s[26:27], 0, v[132:133]
	global_load_lds_dwordx4 v134, s[54:55]
	s_add_i32 m0, s53, 0x2000
	s_nop 0
	global_load_lds_dwordx4 v130, s[54:55]
	v_lshl_add_u64 v[190:191], s[26:27], 0, v[136:137]
	s_waitcnt vmcnt(6)
	s_waitcnt lgkmcnt(0)
	s_barrier
	s_setprio 1
	s_waitcnt lgkmcnt(0)
	v_mfma_f32_16x16x32_bf16 v[62:65], v[156:159], v[192:195], v[62:65]
	v_mfma_f32_16x16x32_bf16 v[58:61], v[164:167], v[192:195], v[58:61]
	v_mfma_f32_16x16x32_bf16 v[50:53], v[156:159], v[200:203], v[50:53]
	v_mfma_f32_16x16x32_bf16 v[42:45], v[164:167], v[200:203], v[42:45]
	v_mfma_f32_16x16x32_bf16 v[34:37], v[156:159], v[208:211], v[34:37]
	v_mfma_f32_16x16x32_bf16 v[26:29], v[164:167], v[208:211], v[26:29]
	v_mfma_f32_16x16x32_bf16 v[18:21], v[156:159], v[216:219], v[18:21]
	v_mfma_f32_16x16x32_bf16 v[10:13], v[164:167], v[216:219], v[10:13]
	s_mov_b32 m0, s21
	s_nop 0
	global_load_lds_dwordx4 v[190:191], off
	v_mfma_f32_16x16x32_bf16 v[62:65], v[160:163], v[196:199], v[62:65]
	v_mfma_f32_16x16x32_bf16 v[58:61], v[168:171], v[196:199], v[58:61]
	v_mfma_f32_16x16x32_bf16 v[50:53], v[160:163], v[204:207], v[50:53]
	v_mfma_f32_16x16x32_bf16 v[42:45], v[168:171], v[204:207], v[42:45]
	v_mfma_f32_16x16x32_bf16 v[34:37], v[160:163], v[212:215], v[34:37]
	v_mfma_f32_16x16x32_bf16 v[26:29], v[168:171], v[212:215], v[26:29]
	v_mfma_f32_16x16x32_bf16 v[18:21], v[160:163], v[224:227], v[18:21]
	v_mfma_f32_16x16x32_bf16 v[10:13], v[168:171], v[224:227], v[10:13]
	s_setprio 0
	s_setprio 1
	v_mfma_f32_16x16x32_bf16 v[54:57], v[172:175], v[192:195], v[54:57]
	v_mfma_f32_16x16x32_bf16 v[46:49], v[180:183], v[192:195], v[46:49]
	v_mfma_f32_16x16x32_bf16 v[38:41], v[172:175], v[200:203], v[38:41]
	v_mfma_f32_16x16x32_bf16 v[30:33], v[180:183], v[200:203], v[30:33]
	v_mfma_f32_16x16x32_bf16 v[22:25], v[172:175], v[208:211], v[22:25]
	v_mfma_f32_16x16x32_bf16 v[14:17], v[180:183], v[208:211], v[14:17]
	v_mfma_f32_16x16x32_bf16 v[6:9], v[172:175], v[216:219], v[6:9]
	v_mfma_f32_16x16x32_bf16 v[2:5], v[180:183], v[216:219], v[2:5]
	s_mov_b32 m0, s37
	s_nop 0
	global_load_lds_dwordx4 v[220:221], off
	v_mfma_f32_16x16x32_bf16 v[54:57], v[176:179], v[196:199], v[54:57]
	v_mfma_f32_16x16x32_bf16 v[46:49], v[184:187], v[196:199], v[46:49]
	v_mfma_f32_16x16x32_bf16 v[38:41], v[176:179], v[204:207], v[38:41]
	v_mfma_f32_16x16x32_bf16 v[30:33], v[184:187], v[204:207], v[30:33]
	v_mfma_f32_16x16x32_bf16 v[22:25], v[176:179], v[212:215], v[22:25]
	v_mfma_f32_16x16x32_bf16 v[14:17], v[184:187], v[212:215], v[14:17]
	v_mfma_f32_16x16x32_bf16 v[6:9], v[176:179], v[224:227], v[6:9]
	v_mfma_f32_16x16x32_bf16 v[2:5], v[184:187], v[224:227], v[2:5]
	s_setprio 0
	s_barrier
	s_add_i32 s53, 0, 0x18000
	v_add_u32_e32 v146, s53, v147
	s_add_i32 s54, 0, 0x1c000
	ds_read_b128 v[156:159], v146
	ds_read_b128 v[160:163], v146 offset:1024
	ds_read_b128 v[164:167], v146 offset:2048
	ds_read_b128 v[168:171], v146 offset:3072
	v_add_u32_e32 v146, s54, v147
	ds_read_b128 v[172:175], v146
	ds_read_b128 v[176:179], v146 offset:1024
	ds_read_b128 v[180:183], v146 offset:2048
	ds_read_b128 v[184:187], v146 offset:3072
	s_add_u32 s26, s26, 0x40000
	s_addc_u32 s27, s27, 0
	s_mov_b32 m0, s38
	ds_read_b128 v[192:195], v153 offset:32768
	ds_read_b128 v[196:199], v153 offset:33792
	ds_read_b128 v[200:203], v153 offset:34816
	ds_read_b128 v[204:207], v153 offset:35840
	ds_read_b128 v[208:211], v153 offset:36864
	ds_read_b128 v[212:215], v153 offset:37888
	ds_read_b128 v[216:219], v153 offset:38912
	ds_read_b128 v[224:227], v153 offset:39936
	global_load_lds_dwordx4 v136, s[26:27]
	v_lshl_add_u64 v[228:229], s[26:27], 0, v[132:133]
	s_mov_b32 m0, s39
	s_nop 0
	global_load_lds_dwordx4 v[228:229], off
	s_waitcnt vmcnt(8)
	s_waitcnt lgkmcnt(0)
	s_barrier
	s_setprio 1
	s_waitcnt lgkmcnt(0)
	v_mfma_f32_16x16x32_bf16 v[126:129], v[156:159], v[192:195], v[126:129]
	v_mfma_f32_16x16x32_bf16 v[122:125], v[164:167], v[192:195], v[122:125]
	v_mfma_f32_16x16x32_bf16 v[114:117], v[156:159], v[200:203], v[114:117]
	v_mfma_f32_16x16x32_bf16 v[106:109], v[164:167], v[200:203], v[106:109]
	v_mfma_f32_16x16x32_bf16 v[98:101], v[156:159], v[208:211], v[98:101]
	v_mfma_f32_16x16x32_bf16 v[90:93], v[164:167], v[208:211], v[90:93]
	v_mfma_f32_16x16x32_bf16 v[82:85], v[156:159], v[216:219], v[82:85]
	v_mfma_f32_16x16x32_bf16 v[74:77], v[164:167], v[216:219], v[74:77]
	v_mfma_f32_16x16x32_bf16 v[126:129], v[160:163], v[196:199], v[126:129]
	v_mfma_f32_16x16x32_bf16 v[122:125], v[168:171], v[196:199], v[122:125]
	v_mfma_f32_16x16x32_bf16 v[114:117], v[160:163], v[204:207], v[114:117]
	v_mfma_f32_16x16x32_bf16 v[106:109], v[168:171], v[204:207], v[106:109]
	v_mfma_f32_16x16x32_bf16 v[98:101], v[160:163], v[212:215], v[98:101]
	v_mfma_f32_16x16x32_bf16 v[90:93], v[168:171], v[212:215], v[90:93]
	v_mfma_f32_16x16x32_bf16 v[82:85], v[160:163], v[224:227], v[82:85]
	v_mfma_f32_16x16x32_bf16 v[74:77], v[168:171], v[224:227], v[74:77]
	s_setprio 0
	s_setprio 1
	v_mfma_f32_16x16x32_bf16 v[118:121], v[172:175], v[192:195], v[118:121]
	v_mfma_f32_16x16x32_bf16 v[110:113], v[180:183], v[192:195], v[110:113]
	v_mfma_f32_16x16x32_bf16 v[102:105], v[172:175], v[200:203], v[102:105]
	v_mfma_f32_16x16x32_bf16 v[94:97], v[180:183], v[200:203], v[94:97]
	v_mfma_f32_16x16x32_bf16 v[86:89], v[172:175], v[208:211], v[86:89]
	v_mfma_f32_16x16x32_bf16 v[78:81], v[180:183], v[208:211], v[78:81]
	v_mfma_f32_16x16x32_bf16 v[70:73], v[172:175], v[216:219], v[70:73]
	v_mfma_f32_16x16x32_bf16 v[66:69], v[180:183], v[216:219], v[66:69]
	v_mfma_f32_16x16x32_bf16 v[118:121], v[176:179], v[196:199], v[118:121]
	v_mfma_f32_16x16x32_bf16 v[110:113], v[184:187], v[196:199], v[110:113]
	v_mfma_f32_16x16x32_bf16 v[102:105], v[176:179], v[204:207], v[102:105]
	v_mfma_f32_16x16x32_bf16 v[94:97], v[184:187], v[204:207], v[94:97]
	v_mfma_f32_16x16x32_bf16 v[86:89], v[176:179], v[212:215], v[86:89]
	v_mfma_f32_16x16x32_bf16 v[78:81], v[184:187], v[212:215], v[78:81]
	v_mfma_f32_16x16x32_bf16 v[70:73], v[176:179], v[224:227], v[70:73]
	v_mfma_f32_16x16x32_bf16 v[66:69], v[184:187], v[224:227], v[66:69]
	s_setprio 0
	s_barrier
	s_add_i32 s26, s53, s34
	v_lshl_add_u64 v[148:149], v[148:149], 0, s[8:9]
	s_mov_b32 m0, s26
	ds_read_b128 v[192:195], v153 offset:49152
	ds_read_b128 v[196:199], v153 offset:50176
	ds_read_b128 v[200:203], v153 offset:51200
	ds_read_b128 v[204:207], v153 offset:52224
	ds_read_b128 v[208:211], v153 offset:53248
	ds_read_b128 v[212:215], v153 offset:54272
	ds_read_b128 v[216:219], v153 offset:55296
	ds_read_b128 v[224:227], v153 offset:56320
	global_load_lds_dwordx4 v[148:149], off
	s_add_i32 m0, s26, 0x2000
	s_add_u32 s24, s24, 0x40080
	v_lshl_add_u64 v[148:149], v[188:189], 0, s[8:9]
	s_addc_u32 s25, s25, 0
	s_add_i32 s26, s54, s34
	global_load_lds_dwordx4 v[148:149], off
	s_mov_b32 m0, s26
	s_nop 0
	global_load_lds_dwordx4 v134, s[24:25]
	s_add_i32 m0, s26, 0x2000
	s_nop 0
	global_load_lds_dwordx4 v130, s[24:25]
	v_lshl_add_u64 v[148:149], v[190:191], 0, s[8:9]
	v_lshl_add_u64 v[228:229], v[220:221], 0, s[8:9]
	s_waitcnt vmcnt(6)
	s_waitcnt lgkmcnt(0)
	s_barrier
	s_setprio 1
	s_waitcnt lgkmcnt(0)
	v_mfma_f32_16x16x32_bf16 v[62:65], v[156:159], v[192:195], v[62:65]
	v_mfma_f32_16x16x32_bf16 v[58:61], v[164:167], v[192:195], v[58:61]
	v_mfma_f32_16x16x32_bf16 v[50:53], v[156:159], v[200:203], v[50:53]
	v_mfma_f32_16x16x32_bf16 v[42:45], v[164:167], v[200:203], v[42:45]
	v_mfma_f32_16x16x32_bf16 v[34:37], v[156:159], v[208:211], v[34:37]
	v_mfma_f32_16x16x32_bf16 v[26:29], v[164:167], v[208:211], v[26:29]
	v_mfma_f32_16x16x32_bf16 v[18:21], v[156:159], v[216:219], v[18:21]
	v_mfma_f32_16x16x32_bf16 v[10:13], v[164:167], v[216:219], v[10:13]
	s_mov_b32 m0, s41
	s_nop 0
	global_load_lds_dwordx4 v[148:149], off
	v_mfma_f32_16x16x32_bf16 v[62:65], v[160:163], v[196:199], v[62:65]
	v_mfma_f32_16x16x32_bf16 v[58:61], v[168:171], v[196:199], v[58:61]
	v_mfma_f32_16x16x32_bf16 v[50:53], v[160:163], v[204:207], v[50:53]
	v_mfma_f32_16x16x32_bf16 v[42:45], v[168:171], v[204:207], v[42:45]
	v_mfma_f32_16x16x32_bf16 v[34:37], v[160:163], v[212:215], v[34:37]
	v_mfma_f32_16x16x32_bf16 v[26:29], v[168:171], v[212:215], v[26:29]
	v_mfma_f32_16x16x32_bf16 v[18:21], v[160:163], v[224:227], v[18:21]
	v_mfma_f32_16x16x32_bf16 v[10:13], v[168:171], v[224:227], v[10:13]
	s_setprio 0
	s_setprio 1
	v_mfma_f32_16x16x32_bf16 v[54:57], v[172:175], v[192:195], v[54:57]
	v_mfma_f32_16x16x32_bf16 v[46:49], v[180:183], v[192:195], v[46:49]
	v_mfma_f32_16x16x32_bf16 v[38:41], v[172:175], v[200:203], v[38:41]
	v_mfma_f32_16x16x32_bf16 v[30:33], v[180:183], v[200:203], v[30:33]
	v_mfma_f32_16x16x32_bf16 v[22:25], v[172:175], v[208:211], v[22:25]
	v_mfma_f32_16x16x32_bf16 v[14:17], v[180:183], v[208:211], v[14:17]
	v_mfma_f32_16x16x32_bf16 v[6:9], v[172:175], v[216:219], v[6:9]
	v_mfma_f32_16x16x32_bf16 v[2:5], v[180:183], v[216:219], v[2:5]
	s_mov_b32 m0, s42
	s_nop 0
	global_load_lds_dwordx4 v[228:229], off
	v_mfma_f32_16x16x32_bf16 v[54:57], v[176:179], v[196:199], v[54:57]
	v_mfma_f32_16x16x32_bf16 v[46:49], v[184:187], v[196:199], v[46:49]
	v_mfma_f32_16x16x32_bf16 v[38:41], v[176:179], v[204:207], v[38:41]
	v_mfma_f32_16x16x32_bf16 v[30:33], v[184:187], v[204:207], v[30:33]
	v_mfma_f32_16x16x32_bf16 v[22:25], v[176:179], v[212:215], v[22:25]
	v_mfma_f32_16x16x32_bf16 v[14:17], v[184:187], v[212:215], v[14:17]
	v_mfma_f32_16x16x32_bf16 v[6:9], v[176:179], v[224:227], v[6:9]
	v_mfma_f32_16x16x32_bf16 v[2:5], v[184:187], v[224:227], v[2:5]
	s_setprio 0
	s_barrier
	s_add_i32 s52, s52, 2
	s_add_u32 s22, s22, 0x100
	s_addc_u32 s23, s23, 0
	s_add_u32 s50, s50, 0x100
	s_addc_u32 s51, s51, 0
	s_cmp_gt_u32 s52, 13
	s_cbranch_scc0 .LBB0_299
	s_and_b64 vcc, exec, s[10:11]
	s_cbranch_vccz .LBB0_302
	s_barrier

.LBB0_826:
	s_lshl_b32 s8, s8, 5
	s_and_b32 s14, s8, 0x60
	s_mov_b64 s[8:9], 0x80
	s_add_i32 m0, s21, 0x18000
	v_lshl_add_u64 v[8:9], v[8:9], 0, s[8:9]
	s_lshl_b32 s11, s5, 13
	s_lshl_b32 s15, s14, 7
	s_waitcnt vmcnt(2)
	s_barrier
	global_load_lds_dwordx4 v[8:9], off
	v_lshl_add_u64 v[6:7], v[6:7], 0, s[8:9]
	s_add_i32 m0, s21, 0x1a000
	s_add_i32 s36, s21, 0x8000
	s_add_i32 s37, s21, 0xa000
	global_load_lds_dwordx4 v[6:7], off
	v_lshl_add_u64 v[2:3], v[2:3], 0, s[8:9]
	s_mov_b32 m0, s36
	s_add_u32 s12, s24, 0x40080
	global_load_lds_dwordx4 v[2:3], off
	v_lshl_add_u64 v[2:3], v[4:5], 0, s[8:9]
	s_mov_b32 m0, s37
	s_addc_u32 s13, s25, 0
	global_load_lds_dwordx4 v[2:3], off
	s_add_i32 m0, s21, 0x1c000
	global_load_lds_dwordx4 v132, s[12:13]
	v_lshl_add_u64 v[2:3], s[12:13], 0, v[136:137]
	s_add_i32 m0, s21, 0x1e000
	v_lshlrev_b32_e32 v4, 2, v222
	global_load_lds_dwordx4 v[2:3], off
	v_lshlrev_b32_e32 v2, 1, v13
	v_lshl_or_b32 v3, v222, 6, v2
	v_and_b32_e32 v4, 32, v4
	s_sext_i32_i8 s41, s4
	v_bitop3_b32 v3, v3, s11, v4 bitop3:0xde
	v_lshlrev_b32_e32 v4, 6, v0
	s_movk_i32 s4, 0x3c0
	v_and_or_b32 v2, v4, s4, v2
	v_and_b32_e32 v4, 32, v252
	v_bitop3_b32 v152, s15, v2, v4 bitop3:0xf6
	v_lshlrev_b32_e32 v2, 8, v0
	v_and_b32_e32 v2, 0x18000, v2
	v_lshlrev_b32_e32 v4, 11, v12
	v_or3_b32 v2, v10, v2, v4
	v_add_u32_e32 v138, v2, v11
	v_lshlrev_b32_e32 v2, 4, v14
	s_waitcnt vmcnt(6)
	s_cmpk_lt_u32 s10, 0x100
	v_and_b32_e32 v2, 0x38000, v2
	s_cselect_b64 s[10:11], -1, 0
	v_or3_b32 v2, v10, v2, v4
	s_add_i32 s39, 0, 0x10000
	s_add_i32 s40, 0, 0x14000
	v_lshl_or_b32 v1, s5, 6, v222
	s_ashr_i32 s38, s33, 31
	v_or_b32_e32 v153, s14, v13
	v_mov_b32_e32 v139, v133
	v_add_u32_e32 v140, v2, v11
	v_mov_b32_e32 v141, v133
	v_mov_b64_e32 v[142:143], 0x100
	v_mov_b64_e32 v[144:145], 0xff
	v_add_u32_e32 v154, s39, v152
	v_add_u32_e32 v155, s40, v152
	v_add_u32_e32 v156, 0, v3
	s_barrier
	s_branch .LBB0_829

.LBB0_836:
	ds_read_b128 v[146:149], v154
	ds_read_b128 v[160:163], v154 offset:1024
	ds_read_b128 v[164:167], v154 offset:2048
	ds_read_b128 v[168:171], v154 offset:3072
	ds_read_b128 v[172:175], v155
	ds_read_b128 v[176:179], v155 offset:1024
	ds_read_b128 v[180:183], v155 offset:2048
	ds_read_b128 v[184:187], v155 offset:3072
	s_add_u32 s24, s22, 0xfffc0080
	s_addc_u32 s25, s23, -1
	s_cmp_eq_u32 s46, 12
	s_cselect_b32 s27, s15, s25
	s_cselect_b32 s26, s42, s24
	s_cselect_b32 s25, s13, s45
	s_cselect_b32 s24, s43, s44
	s_add_i32 m0, s21, 0xc000
	ds_read_b128 v[194:197], v156
	ds_read_b128 v[198:201], v156 offset:1024
	ds_read_b128 v[202:205], v156 offset:2048
	ds_read_b128 v[210:213], v156 offset:3072
	ds_read_b128 v[214:217], v156 offset:4096
	ds_read_b128 v[218:221], v156 offset:5120
	ds_read_b128 v[230:233], v156 offset:6144
	ds_read_b128 v[234:237], v156 offset:7168
	global_load_lds_dwordx4 v138, s[22:23]
	s_add_i32 m0, s21, 0xe000
	s_nop 0
	global_load_lds_dwordx4 v140, s[22:23]
	s_waitcnt vmcnt(8)
	s_waitcnt lgkmcnt(0)
	s_barrier
	s_setprio 1
	s_waitcnt lgkmcnt(0)
	v_mfma_f32_16x16x32_bf16 v[126:129], v[146:149], v[194:197], v[126:129]
	v_mfma_f32_16x16x32_bf16 v[122:125], v[164:167], v[194:197], v[122:125]
	v_mfma_f32_16x16x32_bf16 v[118:121], v[146:149], v[202:205], v[118:121]
	v_mfma_f32_16x16x32_bf16 v[114:117], v[164:167], v[202:205], v[114:117]
	v_mfma_f32_16x16x32_bf16 v[94:97], v[146:149], v[214:217], v[94:97]
	v_mfma_f32_16x16x32_bf16 v[90:93], v[164:167], v[214:217], v[90:93]
	v_mfma_f32_16x16x32_bf16 v[86:89], v[146:149], v[230:233], v[86:89]
	v_mfma_f32_16x16x32_bf16 v[82:85], v[164:167], v[230:233], v[82:85]
	v_mfma_f32_16x16x32_bf16 v[126:129], v[160:163], v[198:201], v[126:129]
	v_mfma_f32_16x16x32_bf16 v[122:125], v[168:171], v[198:201], v[122:125]
	v_mfma_f32_16x16x32_bf16 v[118:121], v[160:163], v[210:213], v[118:121]
	v_mfma_f32_16x16x32_bf16 v[114:117], v[168:171], v[210:213], v[114:117]
	v_mfma_f32_16x16x32_bf16 v[94:97], v[160:163], v[218:221], v[94:97]
	v_mfma_f32_16x16x32_bf16 v[90:93], v[168:171], v[218:221], v[90:93]
	v_mfma_f32_16x16x32_bf16 v[86:89], v[160:163], v[234:237], v[86:89]
	v_mfma_f32_16x16x32_bf16 v[82:85], v[168:171], v[234:237], v[82:85]
	s_setprio 0
	s_setprio 1
	v_mfma_f32_16x16x32_bf16 v[110:113], v[172:175], v[194:197], v[110:113]
	v_mfma_f32_16x16x32_bf16 v[106:109], v[180:183], v[194:197], v[106:109]
	v_mfma_f32_16x16x32_bf16 v[102:105], v[172:175], v[202:205], v[102:105]
	v_mfma_f32_16x16x32_bf16 v[98:101], v[180:183], v[202:205], v[98:101]
	v_mfma_f32_16x16x32_bf16 v[78:81], v[172:175], v[214:217], v[78:81]
	v_mfma_f32_16x16x32_bf16 v[74:77], v[180:183], v[214:217], v[74:77]
	v_mfma_f32_16x16x32_bf16 v[70:73], v[172:175], v[230:233], v[70:73]
	v_mfma_f32_16x16x32_bf16 v[66:69], v[180:183], v[230:233], v[66:69]
	v_mfma_f32_16x16x32_bf16 v[110:113], v[176:179], v[198:201], v[110:113]
	v_mfma_f32_16x16x32_bf16 v[106:109], v[184:187], v[198:201], v[106:109]
	v_mfma_f32_16x16x32_bf16 v[102:105], v[176:179], v[210:213], v[102:105]
	v_mfma_f32_16x16x32_bf16 v[98:101], v[184:187], v[210:213], v[98:101]
	v_mfma_f32_16x16x32_bf16 v[78:81], v[176:179], v[218:221], v[78:81]
	v_mfma_f32_16x16x32_bf16 v[74:77], v[184:187], v[218:221], v[74:77]
	v_mfma_f32_16x16x32_bf16 v[70:73], v[176:179], v[234:237], v[70:73]
	v_mfma_f32_16x16x32_bf16 v[66:69], v[184:187], v[234:237], v[66:69]
	s_setprio 0
	s_barrier
	s_add_i32 s47, s39, s29
	v_lshl_add_u64 v[150:151], s[24:25], 0, v[132:133]
	s_mov_b32 m0, s47
	ds_read_b128 v[194:197], v156 offset:16384
	ds_read_b128 v[198:201], v156 offset:17408
	ds_read_b128 v[202:205], v156 offset:18432
	ds_read_b128 v[210:213], v156 offset:19456
	ds_read_b128 v[214:217], v156 offset:20480
	ds_read_b128 v[218:221], v156 offset:21504
	ds_read_b128 v[230:233], v156 offset:22528
	ds_read_b128 v[234:237], v156 offset:23552
	global_load_lds_dwordx4 v[150:151], off
	s_add_i32 m0, s47, 0x2000
	s_add_u32 s48, s24, 0x40000
	v_lshl_add_u64 v[188:189], s[24:25], 0, v[136:137]
	s_addc_u32 s49, s25, 0
	s_add_i32 s47, s40, s29
	global_load_lds_dwordx4 v[188:189], off
	s_mov_b32 m0, s47
	v_lshl_add_u64 v[206:207], s[26:27], 0, v[134:135]
	global_load_lds_dwordx4 v132, s[48:49]
	s_add_i32 m0, s47, 0x2000
	s_nop 0
	global_load_lds_dwordx4 v136, s[48:49]
	v_lshl_add_u64 v[190:191], s[26:27], 0, v[130:131]
	s_mov_b32 m0, s21
	s_nop 0
	global_load_lds_dwordx4 v[190:191], off
	s_mov_b32 m0, s30
	s_nop 0
	global_load_lds_dwordx4 v[206:207], off
	s_waitcnt vmcnt(8)
	s_waitcnt lgkmcnt(0)
	s_barrier
	s_setprio 1
	s_waitcnt lgkmcnt(0)
	v_mfma_f32_16x16x32_bf16 v[62:65], v[146:149], v[194:197], v[62:65]
	v_mfma_f32_16x16x32_bf16 v[58:61], v[164:167], v[194:197], v[58:61]
	v_mfma_f32_16x16x32_bf16 v[54:57], v[146:149], v[202:205], v[54:57]
	v_mfma_f32_16x16x32_bf16 v[50:53], v[164:167], v[202:205], v[50:53]
	v_mfma_f32_16x16x32_bf16 v[30:33], v[146:149], v[214:217], v[30:33]
	v_mfma_f32_16x16x32_bf16 v[26:29], v[164:167], v[214:217], v[26:29]
	v_mfma_f32_16x16x32_bf16 v[22:25], v[146:149], v[230:233], v[22:25]
	v_mfma_f32_16x16x32_bf16 v[18:21], v[164:167], v[230:233], v[18:21]
	v_mfma_f32_16x16x32_bf16 v[62:65], v[160:163], v[198:201], v[62:65]
	v_mfma_f32_16x16x32_bf16 v[58:61], v[168:171], v[198:201], v[58:61]
	v_mfma_f32_16x16x32_bf16 v[54:57], v[160:163], v[210:213], v[54:57]
	v_mfma_f32_16x16x32_bf16 v[50:53], v[168:171], v[210:213], v[50:53]
	v_mfma_f32_16x16x32_bf16 v[30:33], v[160:163], v[218:221], v[30:33]
	v_mfma_f32_16x16x32_bf16 v[26:29], v[168:171], v[218:221], v[26:29]
	v_mfma_f32_16x16x32_bf16 v[22:25], v[160:163], v[234:237], v[22:25]
	v_mfma_f32_16x16x32_bf16 v[18:21], v[168:171], v[234:237], v[18:21]
	s_setprio 0
	s_setprio 1
	v_mfma_f32_16x16x32_bf16 v[46:49], v[172:175], v[194:197], v[46:49]
	v_mfma_f32_16x16x32_bf16 v[42:45], v[180:183], v[194:197], v[42:45]
	v_mfma_f32_16x16x32_bf16 v[38:41], v[172:175], v[202:205], v[38:41]
	v_mfma_f32_16x16x32_bf16 v[34:37], v[180:183], v[202:205], v[34:37]
	v_mfma_f32_16x16x32_bf16 v[14:17], v[172:175], v[214:217], v[14:17]
	v_mfma_f32_16x16x32_bf16 v[10:13], v[180:183], v[214:217], v[10:13]
	v_mfma_f32_16x16x32_bf16 v[6:9], v[172:175], v[230:233], v[6:9]
	v_mfma_f32_16x16x32_bf16 v[2:5], v[180:183], v[230:233], v[2:5]
	v_mfma_f32_16x16x32_bf16 v[46:49], v[176:179], v[198:201], v[46:49]
	v_mfma_f32_16x16x32_bf16 v[42:45], v[184:187], v[198:201], v[42:45]
	v_mfma_f32_16x16x32_bf16 v[38:41], v[176:179], v[210:213], v[38:41]
	v_mfma_f32_16x16x32_bf16 v[34:37], v[184:187], v[210:213], v[34:37]
	v_mfma_f32_16x16x32_bf16 v[14:17], v[176:179], v[218:221], v[14:17]
	v_mfma_f32_16x16x32_bf16 v[10:13], v[184:187], v[218:221], v[10:13]
	v_mfma_f32_16x16x32_bf16 v[6:9], v[176:179], v[234:237], v[6:9]
	v_mfma_f32_16x16x32_bf16 v[2:5], v[184:187], v[234:237], v[2:5]
	s_setprio 0
	s_barrier
	s_add_i32 s47, 0, 0x18000
	v_add_u32_e32 v157, s47, v152
	s_add_i32 s48, 0, 0x1c000
	ds_read_b128 v[146:149], v157
	ds_read_b128 v[160:163], v157 offset:1024
	ds_read_b128 v[164:167], v157 offset:2048
	ds_read_b128 v[168:171], v157 offset:3072
	v_add_u32_e32 v157, s48, v152
	ds_read_b128 v[172:175], v157
	ds_read_b128 v[176:179], v157 offset:1024
	ds_read_b128 v[180:183], v157 offset:2048
	ds_read_b128 v[184:187], v157 offset:3072
	s_add_u32 s26, s26, 0x40000
	s_addc_u32 s27, s27, 0
	s_mov_b32 m0, s31
	ds_read_b128 v[194:197], v156 offset:32768
	ds_read_b128 v[198:201], v156 offset:33792
	ds_read_b128 v[202:205], v156 offset:34816
	ds_read_b128 v[210:213], v156 offset:35840
	ds_read_b128 v[214:217], v156 offset:36864
	ds_read_b128 v[218:221], v156 offset:37888
	ds_read_b128 v[230:233], v156 offset:38912
	ds_read_b128 v[234:237], v156 offset:39936
	global_load_lds_dwordx4 v130, s[26:27]
	s_mov_b32 m0, s34
	s_nop 0
	global_load_lds_dwordx4 v134, s[26:27]
	s_waitcnt vmcnt(8)
	s_waitcnt lgkmcnt(0)
	s_barrier
	s_setprio 1
	s_waitcnt lgkmcnt(0)
	v_mfma_f32_16x16x32_bf16 v[126:129], v[146:149], v[194:197], v[126:129]
	v_mfma_f32_16x16x32_bf16 v[122:125], v[164:167], v[194:197], v[122:125]
	v_mfma_f32_16x16x32_bf16 v[118:121], v[146:149], v[202:205], v[118:121]
	v_mfma_f32_16x16x32_bf16 v[114:117], v[164:167], v[202:205], v[114:117]
	v_mfma_f32_16x16x32_bf16 v[94:97], v[146:149], v[214:217], v[94:97]
	v_mfma_f32_16x16x32_bf16 v[90:93], v[164:167], v[214:217], v[90:93]
	v_mfma_f32_16x16x32_bf16 v[86:89], v[146:149], v[230:233], v[86:89]
	v_mfma_f32_16x16x32_bf16 v[82:85], v[164:167], v[230:233], v[82:85]
	v_mfma_f32_16x16x32_bf16 v[126:129], v[160:163], v[198:201], v[126:129]
	v_mfma_f32_16x16x32_bf16 v[122:125], v[168:171], v[198:201], v[122:125]
	v_mfma_f32_16x16x32_bf16 v[118:121], v[160:163], v[210:213], v[118:121]
	v_mfma_f32_16x16x32_bf16 v[114:117], v[168:171], v[210:213], v[114:117]
	v_mfma_f32_16x16x32_bf16 v[94:97], v[160:163], v[218:221], v[94:97]
	v_mfma_f32_16x16x32_bf16 v[90:93], v[168:171], v[218:221], v[90:93]
	v_mfma_f32_16x16x32_bf16 v[86:89], v[160:163], v[234:237], v[86:89]
	v_mfma_f32_16x16x32_bf16 v[82:85], v[168:171], v[234:237], v[82:85]
	s_setprio 0
	s_setprio 1
	v_mfma_f32_16x16x32_bf16 v[110:113], v[172:175], v[194:197], v[110:113]
	v_mfma_f32_16x16x32_bf16 v[106:109], v[180:183], v[194:197], v[106:109]
	v_mfma_f32_16x16x32_bf16 v[102:105], v[172:175], v[202:205], v[102:105]
	v_mfma_f32_16x16x32_bf16 v[98:101], v[180:183], v[202:205], v[98:101]
	v_mfma_f32_16x16x32_bf16 v[78:81], v[172:175], v[214:217], v[78:81]
	v_mfma_f32_16x16x32_bf16 v[74:77], v[180:183], v[214:217], v[74:77]
	v_mfma_f32_16x16x32_bf16 v[70:73], v[172:175], v[230:233], v[70:73]
	v_mfma_f32_16x16x32_bf16 v[66:69], v[180:183], v[230:233], v[66:69]
	v_mfma_f32_16x16x32_bf16 v[110:113], v[176:179], v[198:201], v[110:113]
	v_mfma_f32_16x16x32_bf16 v[106:109], v[184:187], v[198:201], v[106:109]
	v_mfma_f32_16x16x32_bf16 v[102:105], v[176:179], v[210:213], v[102:105]
	v_mfma_f32_16x16x32_bf16 v[98:101], v[184:187], v[210:213], v[98:101]
	v_mfma_f32_16x16x32_bf16 v[78:81], v[176:179], v[218:221], v[78:81]
	v_mfma_f32_16x16x32_bf16 v[74:77], v[184:187], v[218:221], v[74:77]
	v_mfma_f32_16x16x32_bf16 v[70:73], v[176:179], v[234:237], v[70:73]
	v_mfma_f32_16x16x32_bf16 v[66:69], v[184:187], v[234:237], v[66:69]
	s_setprio 0
	s_barrier
	s_add_i32 s26, s47, s29
	v_lshl_add_u64 v[150:151], v[150:151], 0, s[8:9]
	s_mov_b32 m0, s26
	ds_read_b128 v[194:197], v156 offset:49152
	ds_read_b128 v[198:201], v156 offset:50176
	ds_read_b128 v[202:205], v156 offset:51200
	ds_read_b128 v[210:213], v156 offset:52224
	ds_read_b128 v[214:217], v156 offset:53248
	ds_read_b128 v[218:221], v156 offset:54272
	ds_read_b128 v[230:233], v156 offset:55296
	ds_read_b128 v[234:237], v156 offset:56320
	global_load_lds_dwordx4 v[150:151], off
	s_add_i32 m0, s26, 0x2000
	s_add_u32 s24, s24, 0x40080
	v_lshl_add_u64 v[150:151], v[188:189], 0, s[8:9]
	s_addc_u32 s25, s25, 0
	s_add_i32 s26, s48, s29
	global_load_lds_dwordx4 v[150:151], off
	s_mov_b32 m0, s26
	s_nop 0
	global_load_lds_dwordx4 v132, s[24:25]
	s_add_i32 m0, s26, 0x2000
	s_nop 0
	global_load_lds_dwordx4 v136, s[24:25]
	v_lshl_add_u64 v[150:151], v[190:191], 0, s[8:9]
	s_mov_b32 m0, s36
	s_nop 0
	global_load_lds_dwordx4 v[150:151], off
	v_lshl_add_u64 v[150:151], v[206:207], 0, s[8:9]
	s_mov_b32 m0, s37
	s_nop 0
	global_load_lds_dwordx4 v[150:151], off
	s_waitcnt vmcnt(8)
	s_waitcnt lgkmcnt(0)
	s_barrier
	s_setprio 1
	s_waitcnt lgkmcnt(0)
	v_mfma_f32_16x16x32_bf16 v[62:65], v[146:149], v[194:197], v[62:65]
	v_mfma_f32_16x16x32_bf16 v[58:61], v[164:167], v[194:197], v[58:61]
	v_mfma_f32_16x16x32_bf16 v[54:57], v[146:149], v[202:205], v[54:57]
	v_mfma_f32_16x16x32_bf16 v[50:53], v[164:167], v[202:205], v[50:53]
	v_mfma_f32_16x16x32_bf16 v[30:33], v[146:149], v[214:217], v[30:33]
	v_mfma_f32_16x16x32_bf16 v[26:29], v[164:167], v[214:217], v[26:29]
	v_mfma_f32_16x16x32_bf16 v[22:25], v[146:149], v[230:233], v[22:25]
	v_mfma_f32_16x16x32_bf16 v[18:21], v[164:167], v[230:233], v[18:21]
	v_mfma_f32_16x16x32_bf16 v[62:65], v[160:163], v[198:201], v[62:65]
	v_mfma_f32_16x16x32_bf16 v[58:61], v[168:171], v[198:201], v[58:61]
	v_mfma_f32_16x16x32_bf16 v[54:57], v[160:163], v[210:213], v[54:57]
	v_mfma_f32_16x16x32_bf16 v[50:53], v[168:171], v[210:213], v[50:53]
	v_mfma_f32_16x16x32_bf16 v[30:33], v[160:163], v[218:221], v[30:33]
	v_mfma_f32_16x16x32_bf16 v[26:29], v[168:171], v[218:221], v[26:29]
	v_mfma_f32_16x16x32_bf16 v[22:25], v[160:163], v[234:237], v[22:25]
	v_mfma_f32_16x16x32_bf16 v[18:21], v[168:171], v[234:237], v[18:21]
	s_setprio 0
	s_setprio 1
	v_mfma_f32_16x16x32_bf16 v[46:49], v[172:175], v[194:197], v[46:49]
	v_mfma_f32_16x16x32_bf16 v[42:45], v[180:183], v[194:197], v[42:45]
	v_mfma_f32_16x16x32_bf16 v[38:41], v[172:175], v[202:205], v[38:41]
	v_mfma_f32_16x16x32_bf16 v[34:37], v[180:183], v[202:205], v[34:37]
	v_mfma_f32_16x16x32_bf16 v[14:17], v[172:175], v[214:217], v[14:17]
	v_mfma_f32_16x16x32_bf16 v[10:13], v[180:183], v[214:217], v[10:13]
	v_mfma_f32_16x16x32_bf16 v[6:9], v[172:175], v[230:233], v[6:9]
	v_mfma_f32_16x16x32_bf16 v[2:5], v[180:183], v[230:233], v[2:5]
	v_mfma_f32_16x16x32_bf16 v[46:49], v[176:179], v[198:201], v[46:49]
	v_mfma_f32_16x16x32_bf16 v[42:45], v[184:187], v[198:201], v[42:45]
	v_mfma_f32_16x16x32_bf16 v[38:41], v[176:179], v[210:213], v[38:41]
	v_mfma_f32_16x16x32_bf16 v[34:37], v[184:187], v[210:213], v[34:37]
	v_mfma_f32_16x16x32_bf16 v[14:17], v[176:179], v[218:221], v[14:17]
	v_mfma_f32_16x16x32_bf16 v[10:13], v[184:187], v[218:221], v[10:13]
	v_mfma_f32_16x16x32_bf16 v[6:9], v[176:179], v[234:237], v[6:9]
	v_mfma_f32_16x16x32_bf16 v[2:5], v[184:187], v[234:237], v[2:5]
	s_setprio 0
	s_barrier
	s_add_i32 s46, s46, 2
	s_add_u32 s22, s22, 0x100
	s_addc_u32 s23, s23, 0
	s_add_u32 s44, s44, 0x100
	s_addc_u32 s45, s45, 0
	s_cmp_gt_u32 s46, 13
	s_cbranch_scc0 .LBB0_836
	s_and_b64 vcc, exec, s[10:11]
	s_cbranch_vccz .LBB0_839
	s_barrier

.LBB0_1012:
	s_mov_b64 s[10:11], 0x80
	s_add_i32 m0, s37, 0x18000
	v_lshl_add_u64 v[2:3], v[2:3], 0, s[10:11]
	s_waitcnt vmcnt(2)
	s_barrier
	global_load_lds_dwordx4 v[2:3], off
	v_lshl_add_u64 v[2:3], v[4:5], 0, s[10:11]
	s_add_i32 m0, s37, 0x1a000
	s_lshl_b32 s4, s4, 5
	global_load_lds_dwordx4 v[2:3], off
	v_readlane_b32 s60, v253, 46
	ds_read_b64 v[2:3], v153
	s_and_b32 s55, s95, 3
	s_lshl_b32 s6, s1, 13
	s_and_b32 s7, s4, 0x60
	v_readlane_b32 s74, v253, 60
	v_readlane_b32 s75, v253, 61
	s_add_u32 s12, s74, 0x3b00080
	s_addc_u32 s13, s75, 0
	s_add_i32 s41, s37, 0x8000
	s_add_i32 s42, s37, 0xa000
	s_mov_b32 m0, s41
	s_add_u32 s4, s20, 0x40080
	s_waitcnt lgkmcnt(0)
	global_load_lds_dwordx4 v2, s[12:13]
	s_mov_b32 m0, s42
	s_addc_u32 s5, s21, 0
	global_load_lds_dwordx4 v3, s[12:13]
	s_add_i32 m0, s37, 0x1c000
	global_load_lds_dwordx4 v134, s[4:5]
	v_lshl_add_u64 v[2:3], s[4:5], 0, v[132:133]
	s_add_i32 m0, s37, 0x1e000
	s_cmpk_lt_u32 s0, 0x100
	global_load_lds_dwordx4 v[2:3], off
	v_lshlrev_b32_e32 v3, 2, v222
	v_lshl_or_b32 v2, v222, 6, v143
	v_and_b32_e32 v3, 32, v3
	s_waitcnt vmcnt(6)
	v_lshl_or_b32 v155, s1, 6, v222
	v_bitop3_b32 v2, v2, s6, v3 bitop3:0xde
	v_lshl_or_b32 v156, s7, 7, v144
	s_cselect_b64 s[14:15], -1, 0
	s_add_i32 s0, 0, 0x224f0
	s_add_i32 s43, 0, 0x10000
	s_add_i32 s44, 0, 0x14000
	v_lshrrev_b32_e32 v148, 2, v0
	v_or_b32_e32 v157, s7, v142
	v_add_u32_e32 v159, 0x80, v155
	v_add_u32_e32 v160, 0x90, v155
	v_add_u32_e32 v161, 0xa0, v155
	v_add_u32_e32 v162, 0xb0, v155
	v_or_b32_e32 v163, 48, v155
	v_or_b32_e32 v164, 32, v155
	v_or_b32_e32 v165, 16, v155
	v_cmp_eq_u32_e64 s[4:5], 0, v208
	v_mov_b32_e32 v166, s0
	v_add_u32_e32 v167, s43, v156
	v_add_u32_e32 v168, s44, v156
	v_add_u32_e32 v169, 0, v2
	s_mov_b32 s45, 0
	v_readlane_b32 s61, v253, 47
	v_readlane_b32 s62, v253, 48
	v_readlane_b32 s63, v253, 49
	v_readlane_b32 s64, v253, 50
	v_readlane_b32 s65, v253, 51
	v_readlane_b32 s66, v253, 52
	v_readlane_b32 s67, v253, 53
	v_readlane_b32 s68, v253, 54
	v_readlane_b32 s69, v253, 55
	v_readlane_b32 s70, v253, 56
	v_readlane_b32 s71, v253, 57
	v_readlane_b32 s72, v253, 58
	v_readlane_b32 s73, v253, 59
	s_barrier
	s_branch .LBB0_1015

.LBB0_1023:
	ds_read_b128 v[2:5], v167
	ds_read_b128 v[6:9], v167 offset:1024
	ds_read_b128 v[10:13], v167 offset:2048
	ds_read_b128 v[14:17], v167 offset:3072
	ds_read_b128 v[18:21], v168
	ds_read_b128 v[22:25], v168 offset:1024
	ds_read_b128 v[26:29], v168 offset:2048
	ds_read_b128 v[30:33], v168 offset:3072
	s_add_u32 s22, s20, 0x80
	s_addc_u32 s23, s21, 0
	s_cmp_eq_u32 s60, 12
	s_cselect_b32 s23, s83, s23
	s_cselect_b32 s22, s82, s22
	s_cselect_b32 s31, s17, s1
	s_cselect_b32 s30, s16, s0
	s_cselect_b32 s61, s57, s56
	ds_read_b128 v[42:45], v169 offset:1024
	ds_read_b128 v[50:53], v169 offset:2048
	ds_read_b128 v[54:57], v169 offset:3072
	ds_read_b128 v[58:61], v169 offset:4096
	ds_read_b128 v[70:73], v169
	ds_read2_b32 v[140:141], v138 offset0:2 offset1:3
	ds_read_b128 v[78:81], v169 offset:5120
	ds_read_b128 v[86:89], v169 offset:6144
	ds_read_b128 v[90:93], v169 offset:7168
	s_add_i32 m0, s37, 0xc000
	s_waitcnt lgkmcnt(0)
	global_load_lds_dwordx4 v140, s[20:21]
	s_add_i32 m0, s37, 0xe000
	s_nop 0
	global_load_lds_dwordx4 v141, s[20:21]
	s_waitcnt vmcnt(8)
	s_waitcnt lgkmcnt(0)
	s_barrier
	s_setprio 1
	v_mfma_f32_16x16x32_bf16 v[126:129], v[2:5], v[70:73], v[126:129]
	v_mfma_f32_16x16x32_bf16 v[122:125], v[10:13], v[70:73], v[122:125]
	v_mfma_f32_16x16x32_bf16 v[110:113], v[2:5], v[50:53], v[110:113]
	v_mfma_f32_16x16x32_bf16 v[106:109], v[10:13], v[50:53], v[106:109]
	v_mfma_f32_16x16x32_bf16 v[94:97], v[2:5], v[58:61], v[94:97]
	v_mfma_f32_16x16x32_bf16 v[82:85], v[10:13], v[58:61], v[82:85]
	v_mfma_f32_16x16x32_bf16 v[2:5], v[2:5], v[86:89], v[62:65]
	v_mfma_f32_16x16x32_bf16 v[126:129], v[6:9], v[42:45], v[126:129]
	v_mfma_f32_16x16x32_bf16 v[122:125], v[14:17], v[42:45], v[122:125]
	v_mfma_f32_16x16x32_bf16 v[110:113], v[6:9], v[54:57], v[110:113]
	v_mfma_f32_16x16x32_bf16 v[106:109], v[14:17], v[54:57], v[106:109]
	v_mfma_f32_16x16x32_bf16 v[94:97], v[6:9], v[78:81], v[94:97]
	v_mfma_f32_16x16x32_bf16 v[82:85], v[14:17], v[78:81], v[82:85]
	v_mfma_f32_16x16x32_bf16 v[2:5], v[6:9], v[90:93], v[2:5]
	v_mfma_f32_16x16x32_bf16 v[6:9], v[10:13], v[86:89], v[46:49]
	v_mfma_f32_16x16x32_bf16 v[6:9], v[14:17], v[90:93], v[6:9]
	s_setprio 0
	s_setprio 1
	v_mfma_f32_16x16x32_bf16 v[10:13], v[18:21], v[70:73], v[118:121]
	v_mfma_f32_16x16x32_bf16 v[14:17], v[26:29], v[70:73], v[114:117]
	v_mfma_f32_16x16x32_bf16 v[46:49], v[26:29], v[50:53], v[98:101]
	v_mfma_f32_16x16x32_bf16 v[10:13], v[22:25], v[42:45], v[10:13]
	v_mfma_f32_16x16x32_bf16 v[14:17], v[30:33], v[42:45], v[14:17]
	v_mfma_f32_16x16x32_bf16 v[42:45], v[18:21], v[50:53], v[102:105]
	v_mfma_f32_16x16x32_bf16 v[50:53], v[30:33], v[54:57], v[46:49]
	v_mfma_f32_16x16x32_bf16 v[46:49], v[18:21], v[58:61], v[74:77]
	v_mfma_f32_16x16x32_bf16 v[18:21], v[18:21], v[86:89], v[38:41]
	v_mfma_f32_16x16x32_bf16 v[42:45], v[22:25], v[54:57], v[42:45]
	v_mfma_f32_16x16x32_bf16 v[54:57], v[22:25], v[78:81], v[46:49]
	v_mfma_f32_16x16x32_bf16 v[46:49], v[26:29], v[58:61], v[66:69]
	v_mfma_f32_16x16x32_bf16 v[18:21], v[22:25], v[90:93], v[18:21]
	v_mfma_f32_16x16x32_bf16 v[22:25], v[26:29], v[86:89], v[34:37]
	v_mfma_f32_16x16x32_bf16 v[58:61], v[30:33], v[78:81], v[46:49]
	v_mfma_f32_16x16x32_bf16 v[22:25], v[30:33], v[90:93], v[22:25]
	s_setprio 0
	s_barrier
	s_add_i32 s62, s43, s36
	v_lshl_add_u64 v[140:141], s[30:31], 0, v[134:135]
	s_mov_b32 m0, s62
	v_lshl_add_u64 v[190:191], s[30:31], 0, v[132:133]
	global_load_lds_dwordx4 v[140:141], off
	s_add_i32 m0, s62, 0x2000
	s_add_u32 s62, s30, 0x40000
	s_addc_u32 s63, s31, 0
	s_add_i32 s64, s44, s36
	global_load_lds_dwordx4 v[190:191], off
	s_mov_b32 m0, s64
	v_lshl_add_u32 v136, s61, 2, v153
	global_load_lds_dwordx4 v134, s[62:63]
	s_add_i32 m0, s64, 0x2000
	s_nop 0
	global_load_lds_dwordx4 v132, s[62:63]
	ds_read2_b32 v[26:27], v136 offset1:1
	s_mov_b32 m0, s37
	s_waitcnt lgkmcnt(0)
	global_load_lds_dwordx4 v26, s[22:23]
	s_mov_b32 m0, s38
	s_nop 0
	global_load_lds_dwordx4 v27, s[22:23]
	s_waitcnt vmcnt(8)
	s_waitcnt lgkmcnt(0)
	s_barrier
	s_barrier
	s_add_i32 s61, 0, 0x18000
	s_add_i32 s62, 0, 0x1c000
	v_add_u32_e32 v38, s61, v156
	v_add_u32_e32 v46, s62, v156
	ds_read_b128 v[26:29], v38
	ds_read_b128 v[30:33], v38 offset:1024
	ds_read_b128 v[34:37], v38 offset:2048
	ds_read_b128 v[38:41], v38 offset:3072
	ds_read_b128 v[70:73], v46
	ds_read_b128 v[78:81], v46 offset:1024
	ds_read_b128 v[86:89], v46 offset:2048
	ds_read_b128 v[90:93], v46 offset:3072
	ds_read_b128 v[66:69], v169 offset:32768
	ds_read_b128 v[74:77], v169 offset:33792
	ds_read_b128 v[98:101], v169 offset:34816
	ds_read_b128 v[170:173], v169 offset:35840
	ds_read_b128 v[174:177], v169 offset:36864
	ds_read_b128 v[178:181], v169 offset:37888
	ds_read2_b32 v[46:47], v136 offset0:2 offset1:3
	ds_read_b128 v[182:185], v169 offset:38912
	ds_read_b128 v[186:189], v169 offset:39936
	s_mov_b32 m0, s39
	s_waitcnt lgkmcnt(0)
	global_load_lds_dwordx4 v46, s[22:23]
	s_mov_b32 m0, s40
	s_nop 0
	global_load_lds_dwordx4 v47, s[22:23]
	s_waitcnt vmcnt(8)
	s_waitcnt lgkmcnt(0)
	s_barrier
	s_setprio 1
	v_mfma_f32_16x16x32_bf16 v[46:49], v[26:29], v[66:69], v[126:129]
	v_mfma_f32_16x16x32_bf16 v[126:129], v[30:33], v[74:77], v[46:49]
	v_mfma_f32_16x16x32_bf16 v[46:49], v[34:37], v[66:69], v[122:125]
	v_mfma_f32_16x16x32_bf16 v[122:125], v[38:41], v[74:77], v[46:49]
	v_mfma_f32_16x16x32_bf16 v[46:49], v[26:29], v[98:101], v[110:113]
	v_mfma_f32_16x16x32_bf16 v[110:113], v[30:33], v[170:173], v[46:49]
	v_mfma_f32_16x16x32_bf16 v[46:49], v[34:37], v[98:101], v[106:109]
	v_mfma_f32_16x16x32_bf16 v[106:109], v[38:41], v[170:173], v[46:49]
	v_mfma_f32_16x16x32_bf16 v[46:49], v[26:29], v[174:177], v[94:97]
	v_mfma_f32_16x16x32_bf16 v[2:5], v[26:29], v[182:185], v[2:5]
	v_mfma_f32_16x16x32_bf16 v[94:97], v[30:33], v[178:181], v[46:49]
	v_mfma_f32_16x16x32_bf16 v[46:49], v[34:37], v[174:177], v[82:85]
	v_mfma_f32_16x16x32_bf16 v[62:65], v[30:33], v[186:189], v[2:5]
	v_mfma_f32_16x16x32_bf16 v[2:5], v[34:37], v[182:185], v[6:9]
	v_mfma_f32_16x16x32_bf16 v[82:85], v[38:41], v[178:181], v[46:49]
	v_mfma_f32_16x16x32_bf16 v[46:49], v[38:41], v[186:189], v[2:5]
	s_setprio 0
	s_setprio 1
	v_mfma_f32_16x16x32_bf16 v[2:5], v[70:73], v[66:69], v[10:13]
	v_mfma_f32_16x16x32_bf16 v[118:121], v[78:81], v[74:77], v[2:5]
	v_mfma_f32_16x16x32_bf16 v[2:5], v[86:89], v[66:69], v[14:17]
	v_mfma_f32_16x16x32_bf16 v[114:117], v[90:93], v[74:77], v[2:5]
	v_mfma_f32_16x16x32_bf16 v[2:5], v[70:73], v[98:101], v[42:45]
	v_mfma_f32_16x16x32_bf16 v[102:105], v[78:81], v[170:173], v[2:5]
	v_mfma_f32_16x16x32_bf16 v[2:5], v[86:89], v[98:101], v[50:53]
	v_mfma_f32_16x16x32_bf16 v[98:101], v[90:93], v[170:173], v[2:5]
	v_mfma_f32_16x16x32_bf16 v[2:5], v[70:73], v[174:177], v[54:57]
	v_mfma_f32_16x16x32_bf16 v[74:77], v[78:81], v[178:181], v[2:5]
	v_mfma_f32_16x16x32_bf16 v[2:5], v[86:89], v[174:177], v[58:61]
	v_mfma_f32_16x16x32_bf16 v[66:69], v[90:93], v[178:181], v[2:5]
	v_mfma_f32_16x16x32_bf16 v[2:5], v[70:73], v[182:185], v[18:21]
	v_mfma_f32_16x16x32_bf16 v[38:41], v[78:81], v[186:189], v[2:5]
	v_mfma_f32_16x16x32_bf16 v[2:5], v[86:89], v[182:185], v[22:25]
	v_mfma_f32_16x16x32_bf16 v[34:37], v[90:93], v[186:189], v[2:5]
	s_setprio 0
	s_barrier
	s_add_i32 s61, s61, s36
	s_nop 3
	v_lshl_add_u64 v[2:3], v[140:141], 0, s[10:11]
	s_mov_b32 m0, s61
	s_nop 0
	global_load_lds_dwordx4 v[2:3], off
	s_add_i32 m0, s61, 0x2000
	s_add_u32 s30, s30, 0x40080
	v_lshl_add_u64 v[2:3], v[190:191], 0, s[10:11]
	s_addc_u32 s31, s31, 0
	s_add_i32 s61, s62, s36
	global_load_lds_dwordx4 v[2:3], off
	s_mov_b32 m0, s61
	s_nop 0
	global_load_lds_dwordx4 v134, s[30:31]
	s_add_i32 m0, s61, 0x2000
	s_nop 0
	global_load_lds_dwordx4 v132, s[30:31]
	ds_read2_b32 v[2:3], v136 offset1:1
	s_mov_b32 m0, s41
	s_waitcnt lgkmcnt(0)
	v_mov_b32_e32 v136, v2
	v_lshl_add_u64 v[4:5], s[22:23], 0, v[136:137]
	v_mov_b32_e32 v136, v3
	v_lshl_add_u64 v[4:5], v[4:5], 0, s[10:11]
	v_lshl_add_u64 v[2:3], s[22:23], 0, v[136:137]
	global_load_lds_dwordx4 v[4:5], off
	v_lshl_add_u64 v[2:3], v[2:3], 0, s[10:11]
	s_mov_b32 m0, s42
	s_nop 0
	global_load_lds_dwordx4 v[2:3], off
	s_waitcnt vmcnt(8)
	s_waitcnt lgkmcnt(0)
	s_barrier
	s_barrier
	s_add_i32 s60, s60, 2
	s_add_u32 s20, s20, 0x100
	s_addc_u32 s21, s21, 0
	s_add_u32 s0, s0, 0x100
	s_addc_u32 s1, s1, 0
	s_cmp_lt_u32 s60, 14
	s_cbranch_scc1 .LBB0_1023
	s_mov_b64 s[22:23], 0

.LBB0_1027:
	ds_read_b128 v[170:173], v167
	ds_read_b128 v[174:177], v167 offset:1024
	ds_read_b128 v[178:181], v167 offset:2048
	ds_read_b128 v[182:185], v167 offset:3072
	ds_read_b128 v[186:189], v168
	ds_read_b128 v[196:199], v168 offset:1024
	ds_read_b128 v[200:203], v168 offset:2048
	ds_read_b128 v[204:207], v168 offset:3072
	s_add_u32 s0, s20, 0x80
	s_addc_u32 s1, s21, 0
	s_cmp_eq_u32 s60, 12
	s_cselect_b32 s23, s83, s1
	s_cselect_b32 s22, s82, s0
	s_cselect_b32 s31, s17, s59
	s_cselect_b32 s30, s16, s58
	s_cselect_b32 s61, s57, s56
	ds_read_b128 v[210:213], v169 offset:1024
	ds_read_b128 v[214:217], v169 offset:2048
	ds_read_b128 v[218:221], v169 offset:3072
	ds_read_b128 v[230:233], v169 offset:4096
	ds_read_b128 v[234:237], v169
	ds_read2_b32 v[140:141], v138 offset0:2 offset1:3
	ds_read_b128 v[238:241], v169 offset:5120
	ds_read_b128 v[242:245], v169 offset:6144
	ds_read_b128 v[246:249], v169 offset:7168
	s_add_i32 m0, s37, 0xc000
	s_waitcnt lgkmcnt(0)
	global_load_lds_dwordx4 v140, s[20:21]
	s_add_i32 m0, s37, 0xe000
	s_nop 0
	global_load_lds_dwordx4 v141, s[20:21]
	s_waitcnt vmcnt(8)
	s_waitcnt lgkmcnt(0)
	s_barrier
	s_setprio 1
	v_mfma_f32_16x16x32_bf16 v[126:129], v[170:173], v[234:237], v[126:129]
	v_mfma_f32_16x16x32_bf16 v[122:125], v[178:181], v[234:237], v[122:125]
	v_mfma_f32_16x16x32_bf16 v[110:113], v[170:173], v[214:217], v[110:113]
	v_mfma_f32_16x16x32_bf16 v[106:109], v[178:181], v[214:217], v[106:109]
	v_mfma_f32_16x16x32_bf16 v[94:97], v[170:173], v[230:233], v[94:97]
	v_mfma_f32_16x16x32_bf16 v[82:85], v[178:181], v[230:233], v[82:85]
	v_mfma_f32_16x16x32_bf16 v[62:65], v[170:173], v[242:245], v[62:65]
	v_mfma_f32_16x16x32_bf16 v[46:49], v[178:181], v[242:245], v[46:49]
	v_mfma_f32_16x16x32_bf16 v[126:129], v[174:177], v[210:213], v[126:129]
	v_mfma_f32_16x16x32_bf16 v[122:125], v[182:185], v[210:213], v[122:125]
	v_mfma_f32_16x16x32_bf16 v[110:113], v[174:177], v[218:221], v[110:113]
	v_mfma_f32_16x16x32_bf16 v[106:109], v[182:185], v[218:221], v[106:109]
	v_mfma_f32_16x16x32_bf16 v[94:97], v[174:177], v[238:241], v[94:97]
	v_mfma_f32_16x16x32_bf16 v[82:85], v[182:185], v[238:241], v[82:85]
	v_mfma_f32_16x16x32_bf16 v[62:65], v[174:177], v[246:249], v[62:65]
	v_mfma_f32_16x16x32_bf16 v[46:49], v[182:185], v[246:249], v[46:49]
	s_setprio 0
	s_setprio 1
	v_mfma_f32_16x16x32_bf16 v[118:121], v[186:189], v[234:237], v[118:121]
	v_mfma_f32_16x16x32_bf16 v[114:117], v[200:203], v[234:237], v[114:117]
	v_mfma_f32_16x16x32_bf16 v[102:105], v[186:189], v[214:217], v[102:105]
	v_mfma_f32_16x16x32_bf16 v[98:101], v[200:203], v[214:217], v[98:101]
	v_mfma_f32_16x16x32_bf16 v[74:77], v[186:189], v[230:233], v[74:77]
	v_mfma_f32_16x16x32_bf16 v[66:69], v[200:203], v[230:233], v[66:69]
	v_mfma_f32_16x16x32_bf16 v[38:41], v[186:189], v[242:245], v[38:41]
	v_mfma_f32_16x16x32_bf16 v[34:37], v[200:203], v[242:245], v[34:37]
	v_mfma_f32_16x16x32_bf16 v[118:121], v[196:199], v[210:213], v[118:121]
	v_mfma_f32_16x16x32_bf16 v[114:117], v[204:207], v[210:213], v[114:117]
	v_mfma_f32_16x16x32_bf16 v[102:105], v[196:199], v[218:221], v[102:105]
	v_mfma_f32_16x16x32_bf16 v[98:101], v[204:207], v[218:221], v[98:101]
	v_mfma_f32_16x16x32_bf16 v[74:77], v[196:199], v[238:241], v[74:77]
	v_mfma_f32_16x16x32_bf16 v[66:69], v[204:207], v[238:241], v[66:69]
	v_mfma_f32_16x16x32_bf16 v[38:41], v[196:199], v[246:249], v[38:41]
	v_mfma_f32_16x16x32_bf16 v[34:37], v[204:207], v[246:249], v[34:37]
	s_setprio 0
	s_barrier
	s_add_i32 s0, s43, s36
	v_lshl_add_u64 v[140:141], s[30:31], 0, v[134:135]
	s_mov_b32 m0, s0
	ds_read_b128 v[210:213], v169 offset:16384
	ds_read_b128 v[214:217], v169 offset:17408
	ds_read_b128 v[218:221], v169 offset:18432
	ds_read_b128 v[230:233], v169 offset:19456
	ds_read_b128 v[234:237], v169 offset:20480
	ds_read_b128 v[238:241], v169 offset:21504
	ds_read_b128 v[242:245], v169 offset:22528
	ds_read_b128 v[246:249], v169 offset:23552
	global_load_lds_dwordx4 v[140:141], off
	s_add_i32 m0, s0, 0x2000
	s_add_u32 s0, s30, 0x40000
	v_lshl_add_u64 v[190:191], s[30:31], 0, v[132:133]
	s_addc_u32 s1, s31, 0
	s_add_i32 s62, s44, s36
	global_load_lds_dwordx4 v[190:191], off
	s_mov_b32 m0, s62
	v_lshl_add_u32 v136, s61, 2, v153
	global_load_lds_dwordx4 v134, s[0:1]
	s_add_i32 m0, s62, 0x2000
	s_nop 0
	global_load_lds_dwordx4 v132, s[0:1]
	ds_read2_b32 v[208:209], v136 offset1:1
	s_mov_b32 m0, s37
	s_waitcnt lgkmcnt(0)
	global_load_lds_dwordx4 v208, s[22:23]
	s_mov_b32 m0, s38
	s_nop 0
	global_load_lds_dwordx4 v209, s[22:23]
	s_waitcnt vmcnt(8)
	s_waitcnt lgkmcnt(0)
	s_barrier
	s_setprio 1
	v_mfma_f32_16x16x32_bf16 v[90:93], v[170:173], v[210:213], v[90:93]
	v_mfma_f32_16x16x32_bf16 v[78:81], v[178:181], v[210:213], v[78:81]
	v_mfma_f32_16x16x32_bf16 v[58:61], v[170:173], v[218:221], v[58:61]
	v_mfma_f32_16x16x32_bf16 v[50:53], v[178:181], v[218:221], v[50:53]
	v_mfma_f32_16x16x32_bf16 v[30:33], v[170:173], v[234:237], v[30:33]
	v_mfma_f32_16x16x32_bf16 v[22:25], v[178:181], v[234:237], v[22:25]
	v_mfma_f32_16x16x32_bf16 v[14:17], v[170:173], v[242:245], v[14:17]
	v_mfma_f32_16x16x32_bf16 v[6:9], v[178:181], v[242:245], v[6:9]
	v_mfma_f32_16x16x32_bf16 v[90:93], v[174:177], v[214:217], v[90:93]
	v_mfma_f32_16x16x32_bf16 v[78:81], v[182:185], v[214:217], v[78:81]
	v_mfma_f32_16x16x32_bf16 v[58:61], v[174:177], v[230:233], v[58:61]
	v_mfma_f32_16x16x32_bf16 v[50:53], v[182:185], v[230:233], v[50:53]
	v_mfma_f32_16x16x32_bf16 v[30:33], v[174:177], v[238:241], v[30:33]
	v_mfma_f32_16x16x32_bf16 v[22:25], v[182:185], v[238:241], v[22:25]
	v_mfma_f32_16x16x32_bf16 v[14:17], v[174:177], v[246:249], v[14:17]
	v_mfma_f32_16x16x32_bf16 v[6:9], v[182:185], v[246:249], v[6:9]
	s_setprio 0
	s_setprio 1
	v_mfma_f32_16x16x32_bf16 v[86:89], v[186:189], v[210:213], v[86:89]
	v_mfma_f32_16x16x32_bf16 v[70:73], v[200:203], v[210:213], v[70:73]
	v_mfma_f32_16x16x32_bf16 v[54:57], v[186:189], v[218:221], v[54:57]
	v_mfma_f32_16x16x32_bf16 v[42:45], v[200:203], v[218:221], v[42:45]
	v_mfma_f32_16x16x32_bf16 v[26:29], v[186:189], v[234:237], v[26:29]
	v_mfma_f32_16x16x32_bf16 v[18:21], v[200:203], v[234:237], v[18:21]
	v_mfma_f32_16x16x32_bf16 v[10:13], v[186:189], v[242:245], v[10:13]
	v_mfma_f32_16x16x32_bf16 v[2:5], v[200:203], v[242:245], v[2:5]
	v_mfma_f32_16x16x32_bf16 v[86:89], v[196:199], v[214:217], v[86:89]
	v_mfma_f32_16x16x32_bf16 v[70:73], v[204:207], v[214:217], v[70:73]
	v_mfma_f32_16x16x32_bf16 v[54:57], v[196:199], v[230:233], v[54:57]
	v_mfma_f32_16x16x32_bf16 v[42:45], v[204:207], v[230:233], v[42:45]
	v_mfma_f32_16x16x32_bf16 v[26:29], v[196:199], v[238:241], v[26:29]
	v_mfma_f32_16x16x32_bf16 v[18:21], v[204:207], v[238:241], v[18:21]
	v_mfma_f32_16x16x32_bf16 v[10:13], v[196:199], v[246:249], v[10:13]
	v_mfma_f32_16x16x32_bf16 v[2:5], v[204:207], v[246:249], v[2:5]
	s_setprio 0
	s_barrier
	s_add_i32 s0, 0, 0x18000
	v_add_u32_e32 v139, s0, v156
	s_add_i32 s61, 0, 0x1c000
	ds_read_b128 v[170:173], v139
	ds_read_b128 v[174:177], v139 offset:1024
	ds_read_b128 v[178:181], v139 offset:2048
	ds_read_b128 v[182:185], v139 offset:3072
	v_add_u32_e32 v139, s61, v156
	ds_read_b128 v[186:189], v139
	ds_read_b128 v[196:199], v139 offset:1024
	ds_read_b128 v[200:203], v139 offset:2048
	ds_read_b128 v[204:207], v139 offset:3072
	ds_read_b128 v[210:213], v169 offset:32768
	ds_read_b128 v[214:217], v169 offset:33792
	ds_read_b128 v[218:221], v169 offset:34816
	ds_read_b128 v[230:233], v169 offset:35840
	ds_read_b128 v[234:237], v169 offset:36864
	ds_read_b128 v[238:241], v169 offset:37888
	ds_read2_b32 v[208:209], v136 offset0:2 offset1:3
	ds_read_b128 v[242:245], v169 offset:38912
	ds_read_b128 v[246:249], v169 offset:39936
	s_mov_b32 m0, s39
	s_waitcnt lgkmcnt(0)
	global_load_lds_dwordx4 v208, s[22:23]
	s_mov_b32 m0, s40
	s_nop 0
	global_load_lds_dwordx4 v209, s[22:23]
	s_waitcnt vmcnt(8)
	s_waitcnt lgkmcnt(0)
	s_barrier
	s_setprio 1
	v_mfma_f32_16x16x32_bf16 v[126:129], v[170:173], v[210:213], v[126:129]
	v_mfma_f32_16x16x32_bf16 v[122:125], v[178:181], v[210:213], v[122:125]
	v_mfma_f32_16x16x32_bf16 v[110:113], v[170:173], v[218:221], v[110:113]
	v_mfma_f32_16x16x32_bf16 v[106:109], v[178:181], v[218:221], v[106:109]
	v_mfma_f32_16x16x32_bf16 v[94:97], v[170:173], v[234:237], v[94:97]
	v_mfma_f32_16x16x32_bf16 v[82:85], v[178:181], v[234:237], v[82:85]
	v_mfma_f32_16x16x32_bf16 v[62:65], v[170:173], v[242:245], v[62:65]
	v_mfma_f32_16x16x32_bf16 v[46:49], v[178:181], v[242:245], v[46:49]
	v_mfma_f32_16x16x32_bf16 v[126:129], v[174:177], v[214:217], v[126:129]
	v_mfma_f32_16x16x32_bf16 v[122:125], v[182:185], v[214:217], v[122:125]
	v_mfma_f32_16x16x32_bf16 v[110:113], v[174:177], v[230:233], v[110:113]
	v_mfma_f32_16x16x32_bf16 v[106:109], v[182:185], v[230:233], v[106:109]
	v_mfma_f32_16x16x32_bf16 v[94:97], v[174:177], v[238:241], v[94:97]
	v_mfma_f32_16x16x32_bf16 v[82:85], v[182:185], v[238:241], v[82:85]
	v_mfma_f32_16x16x32_bf16 v[62:65], v[174:177], v[246:249], v[62:65]
	v_mfma_f32_16x16x32_bf16 v[46:49], v[182:185], v[246:249], v[46:49]
	s_setprio 0
	s_setprio 1
	v_mfma_f32_16x16x32_bf16 v[118:121], v[186:189], v[210:213], v[118:121]
	v_mfma_f32_16x16x32_bf16 v[114:117], v[200:203], v[210:213], v[114:117]
	v_mfma_f32_16x16x32_bf16 v[102:105], v[186:189], v[218:221], v[102:105]
	v_mfma_f32_16x16x32_bf16 v[98:101], v[200:203], v[218:221], v[98:101]
	v_mfma_f32_16x16x32_bf16 v[74:77], v[186:189], v[234:237], v[74:77]
	v_mfma_f32_16x16x32_bf16 v[66:69], v[200:203], v[234:237], v[66:69]
	v_mfma_f32_16x16x32_bf16 v[38:41], v[186:189], v[242:245], v[38:41]
	v_mfma_f32_16x16x32_bf16 v[34:37], v[200:203], v[242:245], v[34:37]
	v_mfma_f32_16x16x32_bf16 v[118:121], v[196:199], v[214:217], v[118:121]
	v_mfma_f32_16x16x32_bf16 v[114:117], v[204:207], v[214:217], v[114:117]
	v_mfma_f32_16x16x32_bf16 v[102:105], v[196:199], v[230:233], v[102:105]
	v_mfma_f32_16x16x32_bf16 v[98:101], v[204:207], v[230:233], v[98:101]
	v_mfma_f32_16x16x32_bf16 v[74:77], v[196:199], v[238:241], v[74:77]
	v_mfma_f32_16x16x32_bf16 v[66:69], v[204:207], v[238:241], v[66:69]
	v_mfma_f32_16x16x32_bf16 v[38:41], v[196:199], v[246:249], v[38:41]
	v_mfma_f32_16x16x32_bf16 v[34:37], v[204:207], v[246:249], v[34:37]
	s_setprio 0
	s_barrier
	s_add_i32 s0, s0, s36
	v_lshl_add_u64 v[140:141], v[140:141], 0, s[10:11]
	s_mov_b32 m0, s0
	ds_read_b128 v[210:213], v169 offset:49152
	ds_read_b128 v[214:217], v169 offset:50176
	ds_read_b128 v[218:221], v169 offset:51200
	ds_read_b128 v[230:233], v169 offset:52224
	ds_read_b128 v[234:237], v169 offset:53248
	ds_read_b128 v[238:241], v169 offset:54272
	ds_read_b128 v[242:245], v169 offset:55296
	ds_read_b128 v[246:249], v169 offset:56320
	global_load_lds_dwordx4 v[140:141], off
	s_add_i32 m0, s0, 0x2000
	s_add_u32 s0, s30, 0x40080
	v_lshl_add_u64 v[140:141], v[190:191], 0, s[10:11]
	s_addc_u32 s1, s31, 0
	s_add_i32 s30, s61, s36
	global_load_lds_dwordx4 v[140:141], off
	s_mov_b32 m0, s30
	s_nop 0
	global_load_lds_dwordx4 v134, s[0:1]
	s_add_i32 m0, s30, 0x2000
	s_nop 0
	global_load_lds_dwordx4 v132, s[0:1]
	ds_read2_b32 v[140:141], v136 offset1:1
	s_mov_b32 m0, s41
	s_waitcnt lgkmcnt(0)
	v_mov_b32_e32 v136, v140
	v_lshl_add_u64 v[190:191], s[22:23], 0, v[136:137]
	v_mov_b32_e32 v136, v141
	v_lshl_add_u64 v[190:191], v[190:191], 0, s[10:11]
	v_lshl_add_u64 v[140:141], s[22:23], 0, v[136:137]
	global_load_lds_dwordx4 v[190:191], off
	v_lshl_add_u64 v[140:141], v[140:141], 0, s[10:11]
	s_mov_b32 m0, s42
	s_nop 0
	global_load_lds_dwordx4 v[140:141], off
	s_waitcnt vmcnt(8)
	s_waitcnt lgkmcnt(0)
	s_barrier
	s_setprio 1
	v_mfma_f32_16x16x32_bf16 v[90:93], v[170:173], v[210:213], v[90:93]
	v_mfma_f32_16x16x32_bf16 v[78:81], v[178:181], v[210:213], v[78:81]
	v_mfma_f32_16x16x32_bf16 v[58:61], v[170:173], v[218:221], v[58:61]
	v_mfma_f32_16x16x32_bf16 v[50:53], v[178:181], v[218:221], v[50:53]
	v_mfma_f32_16x16x32_bf16 v[30:33], v[170:173], v[234:237], v[30:33]
	v_mfma_f32_16x16x32_bf16 v[22:25], v[178:181], v[234:237], v[22:25]
	v_mfma_f32_16x16x32_bf16 v[14:17], v[170:173], v[242:245], v[14:17]
	v_mfma_f32_16x16x32_bf16 v[6:9], v[178:181], v[242:245], v[6:9]
	v_mfma_f32_16x16x32_bf16 v[90:93], v[174:177], v[214:217], v[90:93]
	v_mfma_f32_16x16x32_bf16 v[78:81], v[182:185], v[214:217], v[78:81]
	v_mfma_f32_16x16x32_bf16 v[58:61], v[174:177], v[230:233], v[58:61]
	v_mfma_f32_16x16x32_bf16 v[50:53], v[182:185], v[230:233], v[50:53]
	v_mfma_f32_16x16x32_bf16 v[30:33], v[174:177], v[238:241], v[30:33]
	v_mfma_f32_16x16x32_bf16 v[22:25], v[182:185], v[238:241], v[22:25]
	v_mfma_f32_16x16x32_bf16 v[14:17], v[174:177], v[246:249], v[14:17]
	v_mfma_f32_16x16x32_bf16 v[6:9], v[182:185], v[246:249], v[6:9]
	s_setprio 0
	s_setprio 1
	v_mfma_f32_16x16x32_bf16 v[86:89], v[186:189], v[210:213], v[86:89]
	v_mfma_f32_16x16x32_bf16 v[70:73], v[200:203], v[210:213], v[70:73]
	v_mfma_f32_16x16x32_bf16 v[54:57], v[186:189], v[218:221], v[54:57]
	v_mfma_f32_16x16x32_bf16 v[42:45], v[200:203], v[218:221], v[42:45]
	v_mfma_f32_16x16x32_bf16 v[26:29], v[186:189], v[234:237], v[26:29]
	v_mfma_f32_16x16x32_bf16 v[18:21], v[200:203], v[234:237], v[18:21]
	v_mfma_f32_16x16x32_bf16 v[10:13], v[186:189], v[242:245], v[10:13]
	v_mfma_f32_16x16x32_bf16 v[2:5], v[200:203], v[242:245], v[2:5]
	v_mfma_f32_16x16x32_bf16 v[86:89], v[196:199], v[214:217], v[86:89]
	v_mfma_f32_16x16x32_bf16 v[70:73], v[204:207], v[214:217], v[70:73]
	v_mfma_f32_16x16x32_bf16 v[54:57], v[196:199], v[230:233], v[54:57]
	v_mfma_f32_16x16x32_bf16 v[42:45], v[204:207], v[230:233], v[42:45]
	v_mfma_f32_16x16x32_bf16 v[26:29], v[196:199], v[238:241], v[26:29]
	v_mfma_f32_16x16x32_bf16 v[18:21], v[204:207], v[238:241], v[18:21]
	v_mfma_f32_16x16x32_bf16 v[10:13], v[196:199], v[246:249], v[10:13]
	v_mfma_f32_16x16x32_bf16 v[2:5], v[204:207], v[246:249], v[2:5]
	s_setprio 0
	s_barrier
	s_add_i32 s60, s60, 2
	s_add_u32 s20, s20, 0x100
	s_addc_u32 s21, s21, 0
	s_add_u32 s58, s58, 0x100
	s_addc_u32 s59, s59, 0
	s_cmp_gt_u32 s60, 13
	s_cbranch_scc0 .LBB0_1027
	v_and_b32_e32 v208, 63, v0

.LBB0_1072:
	s_mov_b64 s[30:31], 0x80
	s_add_i32 m0, s71, 0x18000
	v_lshl_add_u64 v[2:3], v[2:3], 0, s[30:31]
	s_waitcnt vmcnt(2)
	s_barrier
	global_load_lds_dwordx4 v[2:3], off
	v_lshl_add_u64 v[2:3], v[4:5], 0, s[30:31]
	s_add_i32 m0, s71, 0x1a000
	s_lshl_b32 s7, s7, 5
	global_load_lds_dwordx4 v[2:3], off
	ds_read_b64 v[2:3], v155
	s_lshl_b32 s1, s6, 13
	s_and_b32 s7, s7, 0x60
	s_add_u32 s34, s54, 0x5c00080
	s_addc_u32 s35, s55, 0
	s_add_i32 s75, s71, 0x8000
	s_add_i32 s76, s71, 0xa000
	s_mov_b32 m0, s75
	s_add_u32 s10, s8, 0x200080
	s_waitcnt lgkmcnt(0)
	global_load_lds_dwordx4 v2, s[34:35]
	s_mov_b32 m0, s76
	s_addc_u32 s11, s9, 0
	global_load_lds_dwordx4 v3, s[34:35]
	s_add_i32 m0, s71, 0x1c000
	global_load_lds_dwordx4 v160, s[10:11]
	v_lshl_add_u64 v[2:3], s[10:11], 0, v[162:163]
	s_add_i32 m0, s71, 0x1e000
	s_cmpk_lt_u32 s0, 0x100
	global_load_lds_dwordx4 v[2:3], off
	s_cselect_b64 s[36:37], -1, 0
	s_add_u32 s38, s54, 0x5c00100
	s_addc_u32 s39, s55, 0
	s_add_u32 s40, s54, 0x5c00180
	s_addc_u32 s41, s55, 0
	s_add_u32 s42, s54, 0x5c00200
	s_addc_u32 s43, s55, 0
	s_add_u32 s44, s54, 0x5c00280
	s_addc_u32 s45, s55, 0
	s_add_u32 s46, s54, 0x5c00300
	v_lshlrev_b32_e32 v3, 2, v222
	s_addc_u32 s47, s55, 0
	v_lshl_or_b32 v2, v222, 6, v143
	v_and_b32_e32 v3, 32, v3
	s_waitcnt vmcnt(6)
	s_add_u32 s48, s54, 0x5c00380
	v_lshl_or_b32 v157, s6, 6, v222
	v_bitop3_b32 v2, v2, s1, v3 bitop3:0xde
	v_lshl_or_b32 v159, s7, 7, v144
	s_addc_u32 s49, s55, 0
	s_add_i32 s0, 0, 0x224f0
	s_add_i32 s78, 0, 0x14000
	s_add_i32 s79, 0, 0x10000
	v_or_b32_e32 v184, v7, v154
	v_or_b32_e32 v185, v6, v154
	v_add_u32_e32 v186, 0, v2
	v_or_b32_e32 v187, 16, v157
	v_or_b32_e32 v188, 32, v157
	v_or_b32_e32 v189, 48, v157
	v_add_u32_e32 v195, 0x80, v157
	v_add_u32_e32 v196, 0x90, v157
	v_add_u32_e32 v197, 0xa0, v157
	v_add_u32_e32 v198, 0xb0, v157
	v_or_b32_e32 v199, s7, v142
	v_mov_b32_e32 v200, s0
	s_add_i32 s77, 0, 0x22400
	v_add_u32_e32 v201, s78, v159
	v_add_u32_e32 v202, s79, v159
	s_mov_b64 s[50:51], 0x100
	s_mov_b64 s[52:53], 0x180
	s_mov_b64 s[54:55], 0x200
	s_mov_b64 s[56:57], 0x280
	s_mov_b64 s[58:59], 0x300
	s_mov_b64 s[60:61], 0x380
	s_mov_b32 s80, 0
	s_barrier
	s_branch .LBB0_1075

.LBB0_1099:
	s_and_b64 s[0:1], s[10:11], exec
	s_cselect_b32 s65, s86, s21
	s_lshl_b32 s12, s68, 6
	s_ashr_i32 s13, s12, 31
	s_cmpk_lt_i32 s64, 0x81
	s_waitcnt vmcnt(0)
	v_lshl_add_u32 v130, s21, 2, v155
	s_mov_b64 s[14:15], -1
	s_cbranch_scc0 .LBB0_1113
	ds_read_b128 v[2:5], v201 offset:3072
	ds_read_b128 v[6:9], v201 offset:2048
	ds_read_b128 v[10:13], v201 offset:1024
	ds_read_b128 v[14:17], v201
	ds_read_b128 v[18:21], v202 offset:3072
	ds_read_b128 v[22:25], v202 offset:2048
	ds_read_b128 v[26:29], v202 offset:1024
	ds_read_b128 v[30:33], v202
	s_mov_b32 s67, s95
	ds_read_b128 v[34:37], v186
	ds_read_b128 v[38:41], v186 offset:1024
	ds_read_b128 v[42:45], v186 offset:2048
	ds_read_b128 v[46:49], v186 offset:3072
	ds_read_b128 v[50:53], v186 offset:4096
	ds_read_b128 v[54:57], v186 offset:5120
	ds_read2_b32 v[66:67], v130 offset0:2 offset1:3
	ds_read_b128 v[58:61], v186 offset:6144
	ds_read_b128 v[62:65], v186 offset:7168
	s_add_i32 s88, s71, 0xc000
	s_mov_b32 m0, s88
	s_add_i32 s89, s71, 0xe000
	s_waitcnt lgkmcnt(0)
	global_load_lds_dwordx4 v66, s[34:35]
	s_mov_b32 m0, s89
	s_nop 0
	global_load_lds_dwordx4 v67, s[34:35]
	s_waitcnt vmcnt(8)
	s_waitcnt lgkmcnt(0)
	s_barrier
	s_setprio 1
	v_mfma_f32_16x16x32_bf16 v[66:69], v[30:33], v[34:37], 0
	v_mfma_f32_16x16x32_bf16 v[72:75], v[26:29], v[38:41], v[66:69]
	v_mfma_f32_16x16x32_bf16 v[66:69], v[22:25], v[34:37], 0
	v_mfma_f32_16x16x32_bf16 v[76:79], v[18:21], v[38:41], v[66:69]
	v_mfma_f32_16x16x32_bf16 v[66:69], v[30:33], v[42:45], 0
	v_mfma_f32_16x16x32_bf16 v[80:83], v[26:29], v[46:49], v[66:69]
	v_mfma_f32_16x16x32_bf16 v[66:69], v[22:25], v[42:45], 0
	v_mfma_f32_16x16x32_bf16 v[84:87], v[18:21], v[46:49], v[66:69]
	v_mfma_f32_16x16x32_bf16 v[66:69], v[30:33], v[50:53], 0
	v_mfma_f32_16x16x32_bf16 v[88:91], v[26:29], v[54:57], v[66:69]
	v_mfma_f32_16x16x32_bf16 v[66:69], v[22:25], v[50:53], 0
	v_mfma_f32_16x16x32_bf16 v[30:33], v[30:33], v[58:61], 0
	v_mfma_f32_16x16x32_bf16 v[22:25], v[22:25], v[58:61], 0
	v_mfma_f32_16x16x32_bf16 v[92:95], v[18:21], v[54:57], v[66:69]
	v_mfma_f32_16x16x32_bf16 v[26:29], v[26:29], v[62:65], v[30:33]
	v_mfma_f32_16x16x32_bf16 v[18:21], v[18:21], v[62:65], v[22:25]
	s_setprio 0
	s_setprio 1
	v_mfma_f32_16x16x32_bf16 v[22:25], v[14:17], v[34:37], 0
	v_mfma_f32_16x16x32_bf16 v[30:33], v[6:9], v[34:37], 0
	v_mfma_f32_16x16x32_bf16 v[22:25], v[10:13], v[38:41], v[22:25]
	v_mfma_f32_16x16x32_bf16 v[30:33], v[2:5], v[38:41], v[30:33]
	v_mfma_f32_16x16x32_bf16 v[34:37], v[14:17], v[42:45], 0
	v_mfma_f32_16x16x32_bf16 v[38:41], v[6:9], v[42:45], 0
	v_mfma_f32_16x16x32_bf16 v[34:37], v[10:13], v[46:49], v[34:37]
	v_mfma_f32_16x16x32_bf16 v[38:41], v[2:5], v[46:49], v[38:41]
	v_mfma_f32_16x16x32_bf16 v[42:45], v[14:17], v[50:53], 0
	v_mfma_f32_16x16x32_bf16 v[46:49], v[6:9], v[50:53], 0
	v_mfma_f32_16x16x32_bf16 v[14:17], v[14:17], v[58:61], 0
	v_mfma_f32_16x16x32_bf16 v[6:9], v[6:9], v[58:61], 0
	v_mfma_f32_16x16x32_bf16 v[42:45], v[10:13], v[54:57], v[42:45]
	v_mfma_f32_16x16x32_bf16 v[46:49], v[2:5], v[54:57], v[46:49]
	v_mfma_f32_16x16x32_bf16 v[10:13], v[10:13], v[62:65], v[14:17]
	v_mfma_f32_16x16x32_bf16 v[2:5], v[2:5], v[62:65], v[6:9]
	s_setprio 0
	s_barrier
	s_add_i32 s90, s79, s70
	v_lshl_add_u64 v[66:67], s[8:9], 0, v[160:161]
	s_add_i32 s91, s90, 0x2000
	v_lshl_add_u64 v[6:7], v[66:67], 0, s[50:51]
	s_mov_b32 m0, s90
	v_lshl_add_u64 v[68:69], s[8:9], 0, v[162:163]
	s_add_u32 s0, s8, 0x200100
	global_load_lds_dwordx4 v[6:7], off
	v_lshl_add_u64 v[6:7], v[68:69], 0, s[50:51]
	s_mov_b32 m0, s91
	s_addc_u32 s1, s9, 0
	s_add_i32 s94, s78, s70
	global_load_lds_dwordx4 v[6:7], off
	s_mov_b32 m0, s94
	s_add_i32 s95, s94, 0x2000
	global_load_lds_dwordx4 v160, s[0:1]
	s_mov_b32 m0, s95
	s_nop 0
	global_load_lds_dwordx4 v162, s[0:1]
	ds_read2_b32 v[6:7], v130 offset1:1
	s_mov_b32 m0, s71
	s_waitcnt lgkmcnt(0)
	global_load_lds_dwordx4 v6, s[38:39]
	s_mov_b32 m0, s72
	s_nop 0
	global_load_lds_dwordx4 v7, s[38:39]
	s_waitcnt vmcnt(8)
	s_waitcnt lgkmcnt(0)
	s_barrier
	s_barrier
	s_add_i32 s97, 0, 0x18000
	s_add_i32 s0, 0, 0x1c000
	v_add_u32_e32 v70, s97, v159
	v_add_u32_e32 v71, s0, v159
	ds_read_b128 v[6:9], v70
	ds_read_b128 v[14:17], v70 offset:1024
	ds_read_b128 v[50:53], v70 offset:2048
	ds_read_b128 v[54:57], v70 offset:3072
	ds_read_b128 v[58:61], v71
	ds_read_b128 v[62:65], v71 offset:1024
	ds_read_b128 v[96:99], v71 offset:2048
	ds_read_b128 v[100:103], v71 offset:3072
	ds_read_b128 v[104:107], v186 offset:32768
	ds_read_b128 v[108:111], v186 offset:33792
	ds_read_b128 v[112:115], v186 offset:34816
	ds_read_b128 v[116:119], v186 offset:35840
	ds_read_b128 v[120:123], v186 offset:36864
	ds_read_b128 v[124:127], v186 offset:37888
	ds_read2_b32 v[128:129], v130 offset0:2 offset1:3
	ds_read_b128 v[132:135], v186 offset:38912
	ds_read_b128 v[136:139], v186 offset:39936
	s_mov_b32 m0, s73
	s_waitcnt lgkmcnt(0)
	global_load_lds_dwordx4 v128, s[38:39]
	s_mov_b32 m0, s74
	s_nop 0
	global_load_lds_dwordx4 v129, s[38:39]
	s_waitcnt vmcnt(8)
	s_waitcnt lgkmcnt(0)
	s_barrier
	s_setprio 1
	v_mfma_f32_16x16x32_bf16 v[72:75], v[6:9], v[104:107], v[72:75]
	v_mfma_f32_16x16x32_bf16 v[80:83], v[6:9], v[112:115], v[80:83]
	v_mfma_f32_16x16x32_bf16 v[88:91], v[6:9], v[120:123], v[88:91]
	v_mfma_f32_16x16x32_bf16 v[6:9], v[6:9], v[132:135], v[26:29]
	v_mfma_f32_16x16x32_bf16 v[72:75], v[14:17], v[108:111], v[72:75]
	v_mfma_f32_16x16x32_bf16 v[80:83], v[14:17], v[116:119], v[80:83]
	v_mfma_f32_16x16x32_bf16 v[88:91], v[14:17], v[124:127], v[88:91]
	v_mfma_f32_16x16x32_bf16 v[6:9], v[14:17], v[136:139], v[6:9]
	v_mfma_f32_16x16x32_bf16 v[14:17], v[50:53], v[132:135], v[18:21]
	v_mfma_f32_16x16x32_bf16 v[76:79], v[50:53], v[104:107], v[76:79]
	v_mfma_f32_16x16x32_bf16 v[84:87], v[50:53], v[112:115], v[84:87]
	v_mfma_f32_16x16x32_bf16 v[92:95], v[50:53], v[120:123], v[92:95]
	v_mfma_f32_16x16x32_bf16 v[14:17], v[54:57], v[136:139], v[14:17]
	v_mfma_f32_16x16x32_bf16 v[76:79], v[54:57], v[108:111], v[76:79]
	v_mfma_f32_16x16x32_bf16 v[84:87], v[54:57], v[116:119], v[84:87]
	v_mfma_f32_16x16x32_bf16 v[92:95], v[54:57], v[124:127], v[92:95]
	s_setprio 0
	s_setprio 1
	v_mfma_f32_16x16x32_bf16 v[18:21], v[58:61], v[104:107], v[22:25]
	v_mfma_f32_16x16x32_bf16 v[22:25], v[96:99], v[104:107], v[30:33]
	v_mfma_f32_16x16x32_bf16 v[26:29], v[58:61], v[112:115], v[34:37]
	v_mfma_f32_16x16x32_bf16 v[30:33], v[96:99], v[112:115], v[38:41]
	v_mfma_f32_16x16x32_bf16 v[34:37], v[58:61], v[120:123], v[42:45]
	v_mfma_f32_16x16x32_bf16 v[38:41], v[96:99], v[120:123], v[46:49]
	v_mfma_f32_16x16x32_bf16 v[10:13], v[58:61], v[132:135], v[10:13]
	v_mfma_f32_16x16x32_bf16 v[2:5], v[96:99], v[132:135], v[2:5]
	v_mfma_f32_16x16x32_bf16 v[18:21], v[62:65], v[108:111], v[18:21]
	v_mfma_f32_16x16x32_bf16 v[22:25], v[100:103], v[108:111], v[22:25]
	v_mfma_f32_16x16x32_bf16 v[26:29], v[62:65], v[116:119], v[26:29]
	v_mfma_f32_16x16x32_bf16 v[30:33], v[100:103], v[116:119], v[30:33]
	v_mfma_f32_16x16x32_bf16 v[34:37], v[62:65], v[124:127], v[34:37]
	v_mfma_f32_16x16x32_bf16 v[38:41], v[100:103], v[124:127], v[38:41]
	v_mfma_f32_16x16x32_bf16 v[10:13], v[62:65], v[136:139], v[10:13]
	v_mfma_f32_16x16x32_bf16 v[2:5], v[100:103], v[136:139], v[2:5]
	s_setprio 0
	s_barrier
	s_add_i32 s97, s97, s70
	s_add_i32 s96, s97, 0x2000
	v_lshl_add_u64 v[42:43], v[66:67], 0, s[52:53]
	s_mov_b32 m0, s97
	s_add_u32 s14, s8, 0x200180
	global_load_lds_dwordx4 v[42:43], off
	v_lshl_add_u64 v[42:43], v[68:69], 0, s[52:53]
	s_mov_b32 m0, s96
	s_addc_u32 s15, s9, 0
	s_add_i32 s0, s0, s70
	global_load_lds_dwordx4 v[42:43], off
	s_mov_b32 m0, s0
	s_add_i32 s1, s0, 0x2000
	global_load_lds_dwordx4 v160, s[14:15]
	s_mov_b32 m0, s1
	s_nop 0
	global_load_lds_dwordx4 v162, s[14:15]
	ds_read2_b32 v[42:43], v130 offset1:1
	s_mov_b32 m0, s75
	s_waitcnt lgkmcnt(0)
	global_load_lds_dwordx4 v42, s[40:41]
	s_mov_b32 m0, s76
	s_nop 0
	global_load_lds_dwordx4 v43, s[40:41]
	s_waitcnt vmcnt(8)
	s_waitcnt lgkmcnt(0)
	s_barrier
	s_barrier
	ds_read_b128 v[42:45], v201 offset:3072
	ds_read_b128 v[46:49], v201 offset:2048
	ds_read_b128 v[50:53], v201 offset:1024
	ds_read_b128 v[54:57], v201
	ds_read_b128 v[58:61], v202 offset:3072
	ds_read_b128 v[62:65], v202 offset:2048
	ds_read_b128 v[96:99], v202 offset:1024
	ds_read_b128 v[100:103], v202
	ds_read_b128 v[104:107], v186
	ds_read_b128 v[108:111], v186 offset:1024
	ds_read_b128 v[112:115], v186 offset:2048
	ds_read_b128 v[116:119], v186 offset:3072
	ds_read_b128 v[120:123], v186 offset:4096
	ds_read_b128 v[124:127], v186 offset:5120
	ds_read2_b32 v[128:129], v130 offset0:2 offset1:3
	ds_read_b128 v[132:135], v186 offset:6144
	ds_read_b128 v[136:139], v186 offset:7168
	s_mov_b32 m0, s88
	s_waitcnt lgkmcnt(0)
	global_load_lds_dwordx4 v128, s[40:41]
	s_mov_b32 m0, s89
	s_nop 0
	global_load_lds_dwordx4 v129, s[40:41]
	s_waitcnt vmcnt(8)
	s_waitcnt lgkmcnt(0)
	s_barrier
	s_setprio 1
	v_mfma_f32_16x16x32_bf16 v[6:9], v[100:103], v[132:135], v[6:9]
	v_mfma_f32_16x16x32_bf16 v[14:17], v[62:65], v[132:135], v[14:17]
	v_mfma_f32_16x16x32_bf16 v[72:75], v[100:103], v[104:107], v[72:75]
	v_mfma_f32_16x16x32_bf16 v[76:79], v[62:65], v[104:107], v[76:79]
	v_mfma_f32_16x16x32_bf16 v[80:83], v[100:103], v[112:115], v[80:83]
	v_mfma_f32_16x16x32_bf16 v[84:87], v[62:65], v[112:115], v[84:87]
	v_mfma_f32_16x16x32_bf16 v[88:91], v[100:103], v[120:123], v[88:91]
	v_mfma_f32_16x16x32_bf16 v[92:95], v[62:65], v[120:123], v[92:95]
	v_mfma_f32_16x16x32_bf16 v[6:9], v[96:99], v[136:139], v[6:9]
	v_mfma_f32_16x16x32_bf16 v[14:17], v[58:61], v[136:139], v[14:17]
	v_mfma_f32_16x16x32_bf16 v[72:75], v[96:99], v[108:111], v[72:75]
	v_mfma_f32_16x16x32_bf16 v[76:79], v[58:61], v[108:111], v[76:79]
	v_mfma_f32_16x16x32_bf16 v[80:83], v[96:99], v[116:119], v[80:83]
	v_mfma_f32_16x16x32_bf16 v[84:87], v[58:61], v[116:119], v[84:87]
	v_mfma_f32_16x16x32_bf16 v[88:91], v[96:99], v[124:127], v[88:91]
	v_mfma_f32_16x16x32_bf16 v[92:95], v[58:61], v[124:127], v[92:95]
	s_setprio 0
	s_setprio 1
	v_mfma_f32_16x16x32_bf16 v[18:21], v[54:57], v[104:107], v[18:21]
	v_mfma_f32_16x16x32_bf16 v[22:25], v[46:49], v[104:107], v[22:25]
	v_mfma_f32_16x16x32_bf16 v[26:29], v[54:57], v[112:115], v[26:29]
	v_mfma_f32_16x16x32_bf16 v[30:33], v[46:49], v[112:115], v[30:33]
	v_mfma_f32_16x16x32_bf16 v[34:37], v[54:57], v[120:123], v[34:37]
	v_mfma_f32_16x16x32_bf16 v[38:41], v[46:49], v[120:123], v[38:41]
	v_mfma_f32_16x16x32_bf16 v[10:13], v[54:57], v[132:135], v[10:13]
	v_mfma_f32_16x16x32_bf16 v[2:5], v[46:49], v[132:135], v[2:5]
	v_mfma_f32_16x16x32_bf16 v[18:21], v[50:53], v[108:111], v[18:21]
	v_mfma_f32_16x16x32_bf16 v[22:25], v[42:45], v[108:111], v[22:25]
	v_mfma_f32_16x16x32_bf16 v[26:29], v[50:53], v[116:119], v[26:29]
	v_mfma_f32_16x16x32_bf16 v[30:33], v[42:45], v[116:119], v[30:33]
	v_mfma_f32_16x16x32_bf16 v[34:37], v[50:53], v[124:127], v[34:37]
	v_mfma_f32_16x16x32_bf16 v[38:41], v[42:45], v[124:127], v[38:41]
	v_mfma_f32_16x16x32_bf16 v[10:13], v[50:53], v[136:139], v[10:13]
	v_mfma_f32_16x16x32_bf16 v[2:5], v[42:45], v[136:139], v[2:5]
	s_setprio 0
	s_barrier
	s_mov_b32 m0, s90
	v_lshl_add_u64 v[42:43], v[66:67], 0, s[54:55]
	s_add_u32 s14, s8, 0x200200
	global_load_lds_dwordx4 v[42:43], off
	v_lshl_add_u64 v[42:43], v[68:69], 0, s[54:55]
	s_mov_b32 m0, s91
	s_addc_u32 s15, s9, 0
	global_load_lds_dwordx4 v[42:43], off
	s_mov_b32 m0, s94
	s_nop 0
	global_load_lds_dwordx4 v160, s[14:15]
	s_mov_b32 m0, s95
	s_nop 0
	global_load_lds_dwordx4 v162, s[14:15]
	ds_read2_b32 v[42:43], v130 offset1:1
	s_mov_b32 m0, s71
	s_waitcnt lgkmcnt(0)
	global_load_lds_dwordx4 v42, s[42:43]
	s_mov_b32 m0, s72
	s_nop 0
	global_load_lds_dwordx4 v43, s[42:43]
	s_waitcnt vmcnt(8)
	s_waitcnt lgkmcnt(0)
	s_barrier
	s_barrier
	ds_read_b128 v[42:45], v70
	ds_read_b128 v[46:49], v70 offset:1024
	ds_read_b128 v[50:53], v70 offset:2048
	ds_read_b128 v[54:57], v70 offset:3072
	ds_read_b128 v[58:61], v71
	ds_read_b128 v[62:65], v71 offset:1024
	ds_read_b128 v[96:99], v71 offset:2048
	ds_read_b128 v[100:103], v71 offset:3072
	ds_read_b128 v[104:107], v186 offset:32768
	ds_read_b128 v[108:111], v186 offset:33792
	ds_read_b128 v[112:115], v186 offset:34816
	ds_read_b128 v[116:119], v186 offset:35840
	ds_read_b128 v[120:123], v186 offset:36864
	ds_read_b128 v[124:127], v186 offset:37888
	ds_read2_b32 v[128:129], v130 offset0:2 offset1:3
	ds_read_b128 v[132:135], v186 offset:38912
	ds_read_b128 v[136:139], v186 offset:39936
	s_mov_b32 m0, s73
	s_waitcnt lgkmcnt(0)
	global_load_lds_dwordx4 v128, s[42:43]
	s_mov_b32 m0, s74
	s_nop 0
	global_load_lds_dwordx4 v129, s[42:43]
	s_waitcnt vmcnt(8)
	s_waitcnt lgkmcnt(0)
	s_barrier
	s_setprio 1
	v_mfma_f32_16x16x32_bf16 v[6:9], v[42:45], v[132:135], v[6:9]
	v_mfma_f32_16x16x32_bf16 v[14:17], v[50:53], v[132:135], v[14:17]
	v_mfma_f32_16x16x32_bf16 v[72:75], v[42:45], v[104:107], v[72:75]
	v_mfma_f32_16x16x32_bf16 v[76:79], v[50:53], v[104:107], v[76:79]
	v_mfma_f32_16x16x32_bf16 v[80:83], v[42:45], v[112:115], v[80:83]
	v_mfma_f32_16x16x32_bf16 v[84:87], v[50:53], v[112:115], v[84:87]
	v_mfma_f32_16x16x32_bf16 v[88:91], v[42:45], v[120:123], v[88:91]
	v_mfma_f32_16x16x32_bf16 v[92:95], v[50:53], v[120:123], v[92:95]
	v_mfma_f32_16x16x32_bf16 v[6:9], v[46:49], v[136:139], v[6:9]
	v_mfma_f32_16x16x32_bf16 v[14:17], v[54:57], v[136:139], v[14:17]
	v_mfma_f32_16x16x32_bf16 v[72:75], v[46:49], v[108:111], v[72:75]
	v_mfma_f32_16x16x32_bf16 v[76:79], v[54:57], v[108:111], v[76:79]
	v_mfma_f32_16x16x32_bf16 v[80:83], v[46:49], v[116:119], v[80:83]
	v_mfma_f32_16x16x32_bf16 v[84:87], v[54:57], v[116:119], v[84:87]
	v_mfma_f32_16x16x32_bf16 v[88:91], v[46:49], v[124:127], v[88:91]
	v_mfma_f32_16x16x32_bf16 v[92:95], v[54:57], v[124:127], v[92:95]
	s_setprio 0
	s_setprio 1
	v_mfma_f32_16x16x32_bf16 v[18:21], v[58:61], v[104:107], v[18:21]
	v_mfma_f32_16x16x32_bf16 v[22:25], v[96:99], v[104:107], v[22:25]
	v_mfma_f32_16x16x32_bf16 v[26:29], v[58:61], v[112:115], v[26:29]
	v_mfma_f32_16x16x32_bf16 v[30:33], v[96:99], v[112:115], v[30:33]
	v_mfma_f32_16x16x32_bf16 v[34:37], v[58:61], v[120:123], v[34:37]
	v_mfma_f32_16x16x32_bf16 v[38:41], v[96:99], v[120:123], v[38:41]
	v_mfma_f32_16x16x32_bf16 v[10:13], v[58:61], v[132:135], v[10:13]
	v_mfma_f32_16x16x32_bf16 v[2:5], v[96:99], v[132:135], v[2:5]
	v_mfma_f32_16x16x32_bf16 v[18:21], v[62:65], v[108:111], v[18:21]
	v_mfma_f32_16x16x32_bf16 v[22:25], v[100:103], v[108:111], v[22:25]
	v_mfma_f32_16x16x32_bf16 v[26:29], v[62:65], v[116:119], v[26:29]
	v_mfma_f32_16x16x32_bf16 v[30:33], v[100:103], v[116:119], v[30:33]
	v_mfma_f32_16x16x32_bf16 v[34:37], v[62:65], v[124:127], v[34:37]
	v_mfma_f32_16x16x32_bf16 v[38:41], v[100:103], v[124:127], v[38:41]
	v_mfma_f32_16x16x32_bf16 v[10:13], v[62:65], v[136:139], v[10:13]
	v_mfma_f32_16x16x32_bf16 v[2:5], v[100:103], v[136:139], v[2:5]
	s_setprio 0
	s_barrier
	s_mov_b32 m0, s97
	v_lshl_add_u64 v[42:43], v[66:67], 0, s[56:57]
	s_add_u32 s14, s8, 0x200280
	global_load_lds_dwordx4 v[42:43], off
	v_lshl_add_u64 v[42:43], v[68:69], 0, s[56:57]
	s_mov_b32 m0, s96
	s_addc_u32 s15, s9, 0
	global_load_lds_dwordx4 v[42:43], off
	s_mov_b32 m0, s0
	s_nop 0
	global_load_lds_dwordx4 v160, s[14:15]
	s_mov_b32 m0, s1
	s_nop 0
	global_load_lds_dwordx4 v162, s[14:15]
	ds_read2_b32 v[42:43], v130 offset1:1
	s_mov_b32 m0, s75
	s_waitcnt lgkmcnt(0)
	global_load_lds_dwordx4 v42, s[44:45]
	s_mov_b32 m0, s76
	s_nop 0
	global_load_lds_dwordx4 v43, s[44:45]
	s_waitcnt vmcnt(8)
	s_waitcnt lgkmcnt(0)
	s_barrier
	s_barrier
	ds_read_b128 v[42:45], v201 offset:3072
	ds_read_b128 v[46:49], v201 offset:2048
	ds_read_b128 v[50:53], v201 offset:1024
	ds_read_b128 v[54:57], v201
	ds_read_b128 v[58:61], v202 offset:3072
	ds_read_b128 v[62:65], v202 offset:2048
	ds_read_b128 v[96:99], v202 offset:1024
	ds_read_b128 v[100:103], v202
	ds_read_b128 v[104:107], v186
	ds_read_b128 v[108:111], v186 offset:1024
	ds_read_b128 v[112:115], v186 offset:2048
	ds_read_b128 v[116:119], v186 offset:3072
	ds_read_b128 v[120:123], v186 offset:4096
	ds_read_b128 v[124:127], v186 offset:5120
	ds_read2_b32 v[128:129], v130 offset0:2 offset1:3
	ds_read_b128 v[132:135], v186 offset:6144
	ds_read_b128 v[136:139], v186 offset:7168
	s_mov_b32 m0, s88
	s_waitcnt lgkmcnt(0)
	global_load_lds_dwordx4 v128, s[44:45]
	s_mov_b32 m0, s89
	s_nop 0
	global_load_lds_dwordx4 v129, s[44:45]
	s_waitcnt vmcnt(8)
	s_waitcnt lgkmcnt(0)
	s_barrier
	s_setprio 1
	v_mfma_f32_16x16x32_bf16 v[72:75], v[100:103], v[104:107], v[72:75]
	v_mfma_f32_16x16x32_bf16 v[80:83], v[100:103], v[112:115], v[80:83]
	v_mfma_f32_16x16x32_bf16 v[88:91], v[100:103], v[120:123], v[88:91]
	v_mfma_f32_16x16x32_bf16 v[6:9], v[100:103], v[132:135], v[6:9]
	v_mfma_f32_16x16x32_bf16 v[72:75], v[96:99], v[108:111], v[72:75]
	v_mfma_f32_16x16x32_bf16 v[76:79], v[62:65], v[104:107], v[76:79]
	v_mfma_f32_16x16x32_bf16 v[80:83], v[96:99], v[116:119], v[80:83]
	v_mfma_f32_16x16x32_bf16 v[84:87], v[62:65], v[112:115], v[84:87]
	v_mfma_f32_16x16x32_bf16 v[88:91], v[96:99], v[124:127], v[88:91]
	v_mfma_f32_16x16x32_bf16 v[92:95], v[62:65], v[120:123], v[92:95]
	v_mfma_f32_16x16x32_bf16 v[96:99], v[96:99], v[136:139], v[6:9]
	v_mfma_f32_16x16x32_bf16 v[6:9], v[62:65], v[132:135], v[14:17]
	v_mfma_f32_16x16x32_bf16 v[76:79], v[58:61], v[108:111], v[76:79]
	v_mfma_f32_16x16x32_bf16 v[84:87], v[58:61], v[116:119], v[84:87]
	v_mfma_f32_16x16x32_bf16 v[92:95], v[58:61], v[124:127], v[92:95]
	v_mfma_f32_16x16x32_bf16 v[58:61], v[58:61], v[136:139], v[6:9]
	s_setprio 0
	s_setprio 1
	v_mfma_f32_16x16x32_bf16 v[6:9], v[54:57], v[104:107], v[18:21]
	v_mfma_f32_16x16x32_bf16 v[62:65], v[50:53], v[108:111], v[6:9]
	v_mfma_f32_16x16x32_bf16 v[6:9], v[46:49], v[104:107], v[22:25]
	v_mfma_f32_16x16x32_bf16 v[100:103], v[42:45], v[108:111], v[6:9]
	v_mfma_f32_16x16x32_bf16 v[6:9], v[54:57], v[112:115], v[26:29]
	v_mfma_f32_16x16x32_bf16 v[104:107], v[50:53], v[116:119], v[6:9]
	v_mfma_f32_16x16x32_bf16 v[6:9], v[46:49], v[112:115], v[30:33]
	v_mfma_f32_16x16x32_bf16 v[108:111], v[42:45], v[116:119], v[6:9]
	v_mfma_f32_16x16x32_bf16 v[6:9], v[54:57], v[120:123], v[34:37]
	v_mfma_f32_16x16x32_bf16 v[112:115], v[50:53], v[124:127], v[6:9]
	v_mfma_f32_16x16x32_bf16 v[6:9], v[46:49], v[120:123], v[38:41]
	v_mfma_f32_16x16x32_bf16 v[116:119], v[42:45], v[124:127], v[6:9]
	v_mfma_f32_16x16x32_bf16 v[6:9], v[54:57], v[132:135], v[10:13]
	v_mfma_f32_16x16x32_bf16 v[2:5], v[46:49], v[132:135], v[2:5]
	v_mfma_f32_16x16x32_bf16 v[120:123], v[50:53], v[136:139], v[6:9]
	v_mfma_f32_16x16x32_bf16 v[124:127], v[42:45], v[136:139], v[2:5]
	s_setprio 0
	s_barrier
	s_mov_b32 m0, s90
	s_nop 2
	v_lshl_add_u64 v[2:3], v[66:67], 0, s[58:59]
	s_add_u32 s14, s8, 0x200300
	global_load_lds_dwordx4 v[2:3], off
	v_lshl_add_u64 v[2:3], v[68:69], 0, s[58:59]
	s_mov_b32 m0, s91
	s_addc_u32 s15, s9, 0
	global_load_lds_dwordx4 v[2:3], off
	s_mov_b32 m0, s94
	s_nop 0
	global_load_lds_dwordx4 v160, s[14:15]
	s_mov_b32 m0, s95
	s_nop 0
	global_load_lds_dwordx4 v162, s[14:15]
	ds_read2_b32 v[2:3], v130 offset1:1
	s_mov_b32 m0, s71
	s_waitcnt lgkmcnt(0)
	global_load_lds_dwordx4 v2, s[46:47]
	s_mov_b32 m0, s72
	s_nop 0
	global_load_lds_dwordx4 v3, s[46:47]
	s_waitcnt vmcnt(8)
	s_waitcnt lgkmcnt(0)
	s_barrier
	s_barrier
	ds_read_b128 v[26:29], v70
	ds_read_b128 v[30:33], v70 offset:1024
	ds_read_b128 v[34:37], v70 offset:2048
	ds_read_b128 v[38:41], v70 offset:3072
	ds_read_b128 v[132:135], v71
	ds_read_b128 v[136:139], v71 offset:1024
	ds_read_b128 v[140:143], v71 offset:2048
	ds_read_b128 v[144:147], v71 offset:3072
	ds_read_b128 v[42:45], v186 offset:32768
	ds_read_b128 v[46:49], v186 offset:33792
	ds_read_b128 v[50:53], v186 offset:34816
	ds_read_b128 v[54:57], v186 offset:35840
	ds_read_b128 v[148:151], v186 offset:36864
	ds_read_b128 v[166:169], v186 offset:37888
	ds_read2_b32 v[2:3], v130 offset0:2 offset1:3
	ds_read_b128 v[170:173], v186 offset:38912
	ds_read_b128 v[174:177], v186 offset:39936
	s_mov_b32 m0, s73
	s_waitcnt lgkmcnt(0)
	global_load_lds_dwordx4 v2, s[46:47]
	s_mov_b32 m0, s74
	s_nop 0
	global_load_lds_dwordx4 v3, s[46:47]
	s_waitcnt vmcnt(8)
	s_waitcnt lgkmcnt(0)
	s_barrier
	s_setprio 1
	v_mfma_f32_16x16x32_bf16 v[2:5], v[26:29], v[42:45], v[72:75]
	v_mfma_f32_16x16x32_bf16 v[10:13], v[26:29], v[50:53], v[80:83]
	v_mfma_f32_16x16x32_bf16 v[18:21], v[26:29], v[148:151], v[88:91]
	v_mfma_f32_16x16x32_bf16 v[26:29], v[26:29], v[170:173], v[96:99]
	v_mfma_f32_16x16x32_bf16 v[2:5], v[30:33], v[46:49], v[2:5]
	v_mfma_f32_16x16x32_bf16 v[6:9], v[34:37], v[42:45], v[76:79]
	v_mfma_f32_16x16x32_bf16 v[10:13], v[30:33], v[54:57], v[10:13]
	v_mfma_f32_16x16x32_bf16 v[14:17], v[34:37], v[50:53], v[84:87]
	v_mfma_f32_16x16x32_bf16 v[18:21], v[30:33], v[166:169], v[18:21]
	v_mfma_f32_16x16x32_bf16 v[22:25], v[34:37], v[148:151], v[92:95]
	v_mfma_f32_16x16x32_bf16 v[26:29], v[30:33], v[174:177], v[26:29]
	v_mfma_f32_16x16x32_bf16 v[30:33], v[34:37], v[170:173], v[58:61]
	v_mfma_f32_16x16x32_bf16 v[6:9], v[38:41], v[46:49], v[6:9]
	v_mfma_f32_16x16x32_bf16 v[14:17], v[38:41], v[54:57], v[14:17]
	v_mfma_f32_16x16x32_bf16 v[22:25], v[38:41], v[166:169], v[22:25]
	v_mfma_f32_16x16x32_bf16 v[30:33], v[38:41], v[174:177], v[30:33]
	s_setprio 0
	s_setprio 1
	v_mfma_f32_16x16x32_bf16 v[34:37], v[132:135], v[42:45], v[62:65]
	v_mfma_f32_16x16x32_bf16 v[38:41], v[140:143], v[42:45], v[100:103]
	v_mfma_f32_16x16x32_bf16 v[34:37], v[136:139], v[46:49], v[34:37]
	v_mfma_f32_16x16x32_bf16 v[38:41], v[144:147], v[46:49], v[38:41]
	v_mfma_f32_16x16x32_bf16 v[42:45], v[132:135], v[50:53], v[104:107]
	v_mfma_f32_16x16x32_bf16 v[46:49], v[140:143], v[50:53], v[108:111]
	v_mfma_f32_16x16x32_bf16 v[42:45], v[136:139], v[54:57], v[42:45]
	v_mfma_f32_16x16x32_bf16 v[46:49], v[144:147], v[54:57], v[46:49]
	v_mfma_f32_16x16x32_bf16 v[50:53], v[132:135], v[148:151], v[112:115]
	v_mfma_f32_16x16x32_bf16 v[54:57], v[140:143], v[148:151], v[116:119]
	v_mfma_f32_16x16x32_bf16 v[58:61], v[132:135], v[170:173], v[120:123]
	v_mfma_f32_16x16x32_bf16 v[62:65], v[140:143], v[170:173], v[124:127]
	v_mfma_f32_16x16x32_bf16 v[50:53], v[136:139], v[166:169], v[50:53]
	v_mfma_f32_16x16x32_bf16 v[54:57], v[144:147], v[166:169], v[54:57]
	v_mfma_f32_16x16x32_bf16 v[58:61], v[136:139], v[174:177], v[58:61]
	v_mfma_f32_16x16x32_bf16 v[62:65], v[144:147], v[174:177], v[62:65]
	s_setprio 0
	s_barrier
	s_mov_b32 m0, s97
	v_lshl_add_u64 v[66:67], v[66:67], 0, s[60:61]
	s_add_u32 s14, s8, 0x200380
	global_load_lds_dwordx4 v[66:67], off
	v_lshl_add_u64 v[66:67], v[68:69], 0, s[60:61]
	s_mov_b32 m0, s96
	s_addc_u32 s15, s9, 0
	global_load_lds_dwordx4 v[66:67], off
	s_mov_b32 m0, s0
	s_nop 0
	global_load_lds_dwordx4 v160, s[14:15]
	s_mov_b32 m0, s1
	s_nop 0
	global_load_lds_dwordx4 v162, s[14:15]
	ds_read2_b32 v[66:67], v130 offset1:1
	s_mov_b32 m0, s75
	s_waitcnt lgkmcnt(0)
	global_load_lds_dwordx4 v66, s[48:49]
	s_mov_b32 m0, s76
	s_nop 0
	global_load_lds_dwordx4 v67, s[48:49]
	s_waitcnt vmcnt(8)
	s_waitcnt lgkmcnt(0)
	s_barrier
	s_barrier
	s_and_b64 vcc, exec, s[6:7]
	s_cbranch_vccnz .LBB0_1112
	s_and_saveexec_b64 s[14:15], s[4:5]
	s_cbranch_execz .LBB0_1111
	s_lshl_b64 s[16:17], s[12:13], 2
	v_readlane_b32 s18, v253, 42
	s_add_u32 s16, s18, s16
	v_readlane_b32 s18, v255, 7
	s_addc_u32 s17, s18, s17
	s_mov_b32 s66, 0x400001
	s_branch .LBB0_1104

.LBB0_1112:
	ds_read_b128 v[66:69], v202
	ds_read_b128 v[72:75], v202 offset:1024
	ds_read_b128 v[76:79], v202 offset:2048
	ds_read_b128 v[80:83], v202 offset:3072
	ds_read_b128 v[84:87], v201
	ds_read_b128 v[88:91], v201 offset:1024
	ds_read_b128 v[92:95], v201 offset:2048
	ds_read_b128 v[96:99], v201 offset:3072
	ds_read_b128 v[100:103], v186
	ds_read_b128 v[104:107], v186 offset:1024
	ds_read_b128 v[108:111], v186 offset:2048
	ds_read_b128 v[112:115], v186 offset:3072
	ds_read_b128 v[116:119], v186 offset:4096
	ds_read_b128 v[120:123], v186 offset:5120
	ds_read2_b32 v[128:129], v130 offset0:2 offset1:3
	ds_read_b128 v[124:127], v186 offset:6144
	ds_read_b128 v[132:135], v186 offset:7168
	s_mov_b32 m0, s88
	s_waitcnt lgkmcnt(0)
	global_load_lds_dwordx4 v128, s[48:49]
	s_mov_b32 m0, s89
	s_nop 0
	global_load_lds_dwordx4 v129, s[48:49]
	s_waitcnt vmcnt(8)
	s_waitcnt lgkmcnt(0)
	s_barrier
	s_setprio 1
	v_mfma_f32_16x16x32_bf16 v[2:5], v[66:69], v[100:103], v[2:5]
	v_mfma_f32_16x16x32_bf16 v[6:9], v[76:79], v[100:103], v[6:9]
	v_mfma_f32_16x16x32_bf16 v[10:13], v[66:69], v[108:111], v[10:13]
	v_mfma_f32_16x16x32_bf16 v[14:17], v[76:79], v[108:111], v[14:17]
	v_mfma_f32_16x16x32_bf16 v[18:21], v[66:69], v[116:119], v[18:21]
	v_mfma_f32_16x16x32_bf16 v[22:25], v[76:79], v[116:119], v[22:25]
	v_mfma_f32_16x16x32_bf16 v[26:29], v[66:69], v[124:127], v[26:29]
	v_mfma_f32_16x16x32_bf16 v[30:33], v[76:79], v[124:127], v[30:33]
	v_mfma_f32_16x16x32_bf16 v[2:5], v[72:75], v[104:107], v[2:5]
	v_mfma_f32_16x16x32_bf16 v[6:9], v[80:83], v[104:107], v[6:9]
	v_mfma_f32_16x16x32_bf16 v[10:13], v[72:75], v[112:115], v[10:13]
	v_mfma_f32_16x16x32_bf16 v[14:17], v[80:83], v[112:115], v[14:17]
	v_mfma_f32_16x16x32_bf16 v[18:21], v[72:75], v[120:123], v[18:21]
	v_mfma_f32_16x16x32_bf16 v[22:25], v[80:83], v[120:123], v[22:25]
	v_mfma_f32_16x16x32_bf16 v[26:29], v[72:75], v[132:135], v[26:29]
	v_mfma_f32_16x16x32_bf16 v[30:33], v[80:83], v[132:135], v[30:33]
	s_setprio 0
	s_setprio 1
	v_mfma_f32_16x16x32_bf16 v[58:61], v[84:87], v[124:127], v[58:61]
	v_mfma_f32_16x16x32_bf16 v[34:37], v[84:87], v[100:103], v[34:37]
	v_mfma_f32_16x16x32_bf16 v[38:41], v[92:95], v[100:103], v[38:41]
	v_mfma_f32_16x16x32_bf16 v[42:45], v[84:87], v[108:111], v[42:45]
	v_mfma_f32_16x16x32_bf16 v[46:49], v[92:95], v[108:111], v[46:49]
	v_mfma_f32_16x16x32_bf16 v[50:53], v[84:87], v[116:119], v[50:53]
	v_mfma_f32_16x16x32_bf16 v[54:57], v[92:95], v[116:119], v[54:57]
	v_mfma_f32_16x16x32_bf16 v[58:61], v[88:91], v[132:135], v[58:61]
	v_mfma_f32_16x16x32_bf16 v[62:65], v[92:95], v[124:127], v[62:65]
	v_mfma_f32_16x16x32_bf16 v[34:37], v[88:91], v[104:107], v[34:37]
	v_mfma_f32_16x16x32_bf16 v[38:41], v[96:99], v[104:107], v[38:41]
	v_mfma_f32_16x16x32_bf16 v[42:45], v[88:91], v[112:115], v[42:45]
	v_mfma_f32_16x16x32_bf16 v[46:49], v[96:99], v[112:115], v[46:49]
	v_mfma_f32_16x16x32_bf16 v[50:53], v[88:91], v[120:123], v[50:53]
	v_mfma_f32_16x16x32_bf16 v[54:57], v[96:99], v[120:123], v[54:57]
	v_mfma_f32_16x16x32_bf16 v[66:69], v[96:99], v[132:135], v[62:65]
	s_setprio 0
	s_barrier
	s_mov_b32 m0, s90
	v_lshl_add_u64 v[152:153], s[62:63], 0, v[160:161]
	s_add_u32 s14, s62, 0x200000
	global_load_lds_dwordx4 v[152:153], off
	v_lshl_add_u64 v[182:183], s[62:63], 0, v[162:163]
	s_mov_b32 m0, s91
	s_addc_u32 s15, s63, 0
	global_load_lds_dwordx4 v[182:183], off
	s_mov_b32 m0, s94
	v_lshl_add_u32 v131, s65, 2, v155
	global_load_lds_dwordx4 v160, s[14:15]
	s_mov_b32 m0, s95
	s_nop 0
	global_load_lds_dwordx4 v162, s[14:15]
	ds_read2_b32 v[62:63], v131 offset1:1
	s_mov_b32 m0, s71
	s_waitcnt lgkmcnt(0)
	global_load_lds_dwordx4 v62, s[26:27]
	s_mov_b32 m0, s72
	s_nop 0
	global_load_lds_dwordx4 v63, s[26:27]
	s_waitcnt vmcnt(8)
	s_waitcnt lgkmcnt(0)
	s_barrier
	s_barrier
	ds_read_b128 v[62:65], v70
	ds_read_b128 v[72:75], v70 offset:1024
	ds_read_b128 v[82:85], v70 offset:2048
	ds_read_b128 v[86:89], v70 offset:3072
	ds_read_b128 v[132:135], v71
	ds_read_b128 v[136:139], v71 offset:1024
	ds_read_b128 v[140:143], v71 offset:2048
	ds_read_b128 v[144:147], v71 offset:3072
	ds_read_b128 v[98:101], v186 offset:32768
	ds_read_b128 v[102:105], v186 offset:33792
	ds_read_b128 v[148:151], v186 offset:34816
	ds_read_b128 v[166:169], v186 offset:35840
	ds_read_b128 v[170:173], v186 offset:36864
	ds_read_b128 v[174:177], v186 offset:37888
	ds_read2_b32 v[70:71], v131 offset0:2 offset1:3
	ds_read_b128 v[178:181], v186 offset:38912
	ds_read_b128 v[204:207], v186 offset:39936
	s_mov_b32 m0, s73
	s_waitcnt lgkmcnt(0)
	global_load_lds_dwordx4 v70, s[26:27]
	s_mov_b32 m0, s74
	s_nop 0
	global_load_lds_dwordx4 v71, s[26:27]
	s_waitcnt vmcnt(8)
	s_waitcnt lgkmcnt(0)
	s_barrier
	s_setprio 1
	v_mfma_f32_16x16x32_bf16 v[2:5], v[62:65], v[98:101], v[2:5]
	v_mfma_f32_16x16x32_bf16 v[126:129], v[72:75], v[102:105], v[2:5]
	v_mfma_f32_16x16x32_bf16 v[2:5], v[82:85], v[98:101], v[6:9]
	v_mfma_f32_16x16x32_bf16 v[122:125], v[86:89], v[102:105], v[2:5]
	v_mfma_f32_16x16x32_bf16 v[2:5], v[62:65], v[148:151], v[10:13]
	v_mfma_f32_16x16x32_bf16 v[110:113], v[72:75], v[166:169], v[2:5]
	v_mfma_f32_16x16x32_bf16 v[2:5], v[82:85], v[148:151], v[14:17]
	v_mfma_f32_16x16x32_bf16 v[106:109], v[86:89], v[166:169], v[2:5]
	v_mfma_f32_16x16x32_bf16 v[2:5], v[62:65], v[170:173], v[18:21]
	v_mfma_f32_16x16x32_bf16 v[94:97], v[72:75], v[174:177], v[2:5]
	v_mfma_f32_16x16x32_bf16 v[2:5], v[82:85], v[170:173], v[22:25]
	v_mfma_f32_16x16x32_bf16 v[90:93], v[86:89], v[174:177], v[2:5]
	v_mfma_f32_16x16x32_bf16 v[2:5], v[62:65], v[178:181], v[26:29]
	v_mfma_f32_16x16x32_bf16 v[78:81], v[72:75], v[204:207], v[2:5]
	v_mfma_f32_16x16x32_bf16 v[2:5], v[82:85], v[178:181], v[30:33]
	v_mfma_f32_16x16x32_bf16 v[74:77], v[86:89], v[204:207], v[2:5]
	s_setprio 0
	s_setprio 1
	v_mfma_f32_16x16x32_bf16 v[2:5], v[132:135], v[98:101], v[34:37]
	v_mfma_f32_16x16x32_bf16 v[118:121], v[136:139], v[102:105], v[2:5]
	v_mfma_f32_16x16x32_bf16 v[2:5], v[140:143], v[98:101], v[38:41]
	v_mfma_f32_16x16x32_bf16 v[114:117], v[144:147], v[102:105], v[2:5]
	v_mfma_f32_16x16x32_bf16 v[2:5], v[132:135], v[148:151], v[42:45]
	v_mfma_f32_16x16x32_bf16 v[102:105], v[136:139], v[166:169], v[2:5]
	v_mfma_f32_16x16x32_bf16 v[2:5], v[140:143], v[148:151], v[46:49]
	v_mfma_f32_16x16x32_bf16 v[98:101], v[144:147], v[166:169], v[2:5]
	v_mfma_f32_16x16x32_bf16 v[2:5], v[132:135], v[170:173], v[50:53]
	v_mfma_f32_16x16x32_bf16 v[86:89], v[136:139], v[174:177], v[2:5]
	v_mfma_f32_16x16x32_bf16 v[2:5], v[140:143], v[170:173], v[54:57]
	v_mfma_f32_16x16x32_bf16 v[82:85], v[144:147], v[174:177], v[2:5]
	v_mfma_f32_16x16x32_bf16 v[2:5], v[132:135], v[178:181], v[58:61]
	v_mfma_f32_16x16x32_bf16 v[62:65], v[136:139], v[204:207], v[2:5]
	v_mfma_f32_16x16x32_bf16 v[2:5], v[140:143], v[178:181], v[66:69]
	v_mfma_f32_16x16x32_bf16 v[58:61], v[144:147], v[204:207], v[2:5]
	s_setprio 0
	s_barrier
	s_mov_b32 m0, s97
	s_nop 3
	v_lshl_add_u64 v[2:3], v[152:153], 0, s[30:31]
	s_add_u32 s14, s62, 0x200080
	global_load_lds_dwordx4 v[2:3], off
	v_lshl_add_u64 v[2:3], v[182:183], 0, s[30:31]
	s_mov_b32 m0, s96
	s_addc_u32 s15, s63, 0
	global_load_lds_dwordx4 v[2:3], off
	s_mov_b32 m0, s0
	s_nop 0
	global_load_lds_dwordx4 v160, s[14:15]
	s_mov_b32 m0, s1
	s_nop 0
	global_load_lds_dwordx4 v162, s[14:15]
	ds_read2_b32 v[2:3], v131 offset1:1
	s_mov_b32 m0, s75
	s_waitcnt lgkmcnt(0)
	global_load_lds_dwordx4 v2, s[34:35]
	s_mov_b32 m0, s76
	s_nop 0
	global_load_lds_dwordx4 v3, s[34:35]
	s_waitcnt vmcnt(8)
	s_waitcnt lgkmcnt(0)
	s_barrier
	s_barrier
	v_readlane_b32 s90, v254, 1
	v_readlane_b32 s96, v254, 3
	s_mov_b64 s[14:15], 0
	s_mov_b32 s95, s67
	v_readlane_b32 s89, v254, 0
	v_readlane_b32 s91, v254, 2
	v_readlane_b32 s97, v254, 4
	v_readlane_b32 s94, v254, 5

.LBB0_1127:
	s_lshl_b32 s18, s88, 7
	ds_read_b128 v[132:135], v202
	ds_read_b128 v[136:139], v202 offset:1024
	ds_read_b128 v[140:143], v202 offset:2048
	ds_read_b128 v[144:147], v202 offset:3072
	ds_read_b128 v[148:151], v201
	ds_read_b128 v[166:169], v201 offset:1024
	ds_read_b128 v[170:173], v201 offset:2048
	ds_read_b128 v[174:177], v201 offset:3072
	s_add_u32 s0, s26, s18
	s_addc_u32 s1, s27, 0
	s_add_u32 s19, s0, 0x100
	s_addc_u32 s66, s1, 0
	s_and_b64 s[16:17], s[14:15], exec
	s_cselect_b32 s17, s27, s66
	s_cselect_b32 s16, s26, s19
	s_add_u32 s18, s8, s18
	s_addc_u32 s19, s9, 0
	s_add_u32 s18, s18, 0x100
	s_addc_u32 s19, s19, 0
	s_and_b64 s[14:15], s[14:15], exec
	s_cselect_b32 s15, s63, s19
	s_cselect_b32 s14, s62, s18
	s_cselect_b32 s18, s65, s21
	ds_read_b128 v[178:181], v186
	ds_read_b128 v[204:207], v186 offset:1024
	ds_read_b128 v[210:213], v186 offset:2048
	ds_read_b128 v[214:217], v186 offset:3072
	ds_read2_b32 v[152:153], v130 offset0:2 offset1:3
	ds_read_b128 v[218:221], v186 offset:4096
	ds_read_b128 v[230:233], v186 offset:5120
	ds_read_b128 v[234:237], v186 offset:6144
	ds_read_b128 v[238:241], v186 offset:7168
	s_waitcnt lgkmcnt(0)
	v_mov_b32_e32 v164, v152
	v_lshl_add_u64 v[182:183], s[0:1], 0, v[164:165]
	v_mov_b32_e32 v164, v153
	v_lshl_add_u64 v[182:183], v[182:183], 0, s[30:31]
	s_add_i32 m0, s71, 0xc000
	v_lshl_add_u64 v[152:153], s[0:1], 0, v[164:165]
	global_load_lds_dwordx4 v[182:183], off
	v_lshl_add_u64 v[152:153], v[152:153], 0, s[30:31]
	s_add_i32 m0, s71, 0xe000
	s_nop 0
	global_load_lds_dwordx4 v[152:153], off
	s_waitcnt vmcnt(8)
	s_waitcnt lgkmcnt(0)
	s_barrier
	s_setprio 1
	v_mfma_f32_16x16x32_bf16 v[126:129], v[132:135], v[178:181], v[126:129]
	v_mfma_f32_16x16x32_bf16 v[122:125], v[140:143], v[178:181], v[122:125]
	v_mfma_f32_16x16x32_bf16 v[110:113], v[132:135], v[210:213], v[110:113]
	v_mfma_f32_16x16x32_bf16 v[106:109], v[140:143], v[210:213], v[106:109]
	v_mfma_f32_16x16x32_bf16 v[94:97], v[132:135], v[218:221], v[94:97]
	v_mfma_f32_16x16x32_bf16 v[90:93], v[140:143], v[218:221], v[90:93]
	v_mfma_f32_16x16x32_bf16 v[78:81], v[132:135], v[234:237], v[78:81]
	v_mfma_f32_16x16x32_bf16 v[74:77], v[140:143], v[234:237], v[74:77]
	v_mfma_f32_16x16x32_bf16 v[126:129], v[136:139], v[204:207], v[126:129]
	v_mfma_f32_16x16x32_bf16 v[122:125], v[144:147], v[204:207], v[122:125]
	v_mfma_f32_16x16x32_bf16 v[110:113], v[136:139], v[214:217], v[110:113]
	v_mfma_f32_16x16x32_bf16 v[106:109], v[144:147], v[214:217], v[106:109]
	v_mfma_f32_16x16x32_bf16 v[94:97], v[136:139], v[230:233], v[94:97]
	v_mfma_f32_16x16x32_bf16 v[90:93], v[144:147], v[230:233], v[90:93]
	v_mfma_f32_16x16x32_bf16 v[78:81], v[136:139], v[238:241], v[78:81]
	v_mfma_f32_16x16x32_bf16 v[74:77], v[144:147], v[238:241], v[74:77]
	s_setprio 0
	s_setprio 1
	v_mfma_f32_16x16x32_bf16 v[118:121], v[148:151], v[178:181], v[118:121]
	v_mfma_f32_16x16x32_bf16 v[114:117], v[170:173], v[178:181], v[114:117]
	v_mfma_f32_16x16x32_bf16 v[102:105], v[148:151], v[210:213], v[102:105]
	v_mfma_f32_16x16x32_bf16 v[98:101], v[170:173], v[210:213], v[98:101]
	v_mfma_f32_16x16x32_bf16 v[86:89], v[148:151], v[218:221], v[86:89]
	v_mfma_f32_16x16x32_bf16 v[82:85], v[170:173], v[218:221], v[82:85]
	v_mfma_f32_16x16x32_bf16 v[62:65], v[148:151], v[234:237], v[62:65]
	v_mfma_f32_16x16x32_bf16 v[58:61], v[170:173], v[234:237], v[58:61]
	v_mfma_f32_16x16x32_bf16 v[118:121], v[166:169], v[204:207], v[118:121]
	v_mfma_f32_16x16x32_bf16 v[114:117], v[174:177], v[204:207], v[114:117]
	v_mfma_f32_16x16x32_bf16 v[102:105], v[166:169], v[214:217], v[102:105]
	v_mfma_f32_16x16x32_bf16 v[98:101], v[174:177], v[214:217], v[98:101]
	v_mfma_f32_16x16x32_bf16 v[86:89], v[166:169], v[230:233], v[86:89]
	v_mfma_f32_16x16x32_bf16 v[82:85], v[174:177], v[230:233], v[82:85]
	v_mfma_f32_16x16x32_bf16 v[62:65], v[166:169], v[238:241], v[62:65]
	v_mfma_f32_16x16x32_bf16 v[58:61], v[174:177], v[238:241], v[58:61]
	s_setprio 0
	s_barrier
	s_add_i32 s0, s79, s70
	v_lshl_add_u64 v[152:153], s[14:15], 0, v[160:161]
	s_mov_b32 m0, s0
	ds_read_b128 v[178:181], v186 offset:16384
	ds_read_b128 v[204:207], v186 offset:17408
	ds_read_b128 v[210:213], v186 offset:18432
	ds_read_b128 v[214:217], v186 offset:19456
	ds_read_b128 v[218:221], v186 offset:20480
	ds_read_b128 v[230:233], v186 offset:21504
	ds_read_b128 v[234:237], v186 offset:22528
	ds_read_b128 v[238:241], v186 offset:23552
	global_load_lds_dwordx4 v[152:153], off
	s_add_i32 m0, s0, 0x2000
	s_add_u32 s0, s14, 0x200000
	v_lshl_add_u64 v[182:183], s[14:15], 0, v[162:163]
	s_addc_u32 s1, s15, 0
	s_add_i32 s19, s78, s70
	global_load_lds_dwordx4 v[182:183], off
	s_mov_b32 m0, s19
	v_lshl_add_u32 v131, s18, 2, v155
	global_load_lds_dwordx4 v160, s[0:1]
	s_add_i32 m0, s19, 0x2000
	s_nop 0
	global_load_lds_dwordx4 v162, s[0:1]
	ds_read2_b32 v[190:191], v131 offset1:1
	s_mov_b32 m0, s71
	s_waitcnt lgkmcnt(0)
	global_load_lds_dwordx4 v190, s[16:17]
	s_mov_b32 m0, s72
	s_nop 0
	global_load_lds_dwordx4 v191, s[16:17]
	s_waitcnt vmcnt(8)
	s_waitcnt lgkmcnt(0)
	s_barrier
	s_setprio 1
	v_mfma_f32_16x16x32_bf16 v[70:73], v[132:135], v[178:181], v[70:73]
	v_mfma_f32_16x16x32_bf16 v[66:69], v[140:143], v[178:181], v[66:69]
	v_mfma_f32_16x16x32_bf16 v[46:49], v[132:135], v[210:213], v[46:49]
	v_mfma_f32_16x16x32_bf16 v[42:45], v[140:143], v[210:213], v[42:45]
	v_mfma_f32_16x16x32_bf16 v[30:33], v[132:135], v[218:221], v[30:33]
	v_mfma_f32_16x16x32_bf16 v[26:29], v[140:143], v[218:221], v[26:29]
	v_mfma_f32_16x16x32_bf16 v[14:17], v[132:135], v[234:237], v[14:17]
	v_mfma_f32_16x16x32_bf16 v[10:13], v[140:143], v[234:237], v[10:13]
	v_mfma_f32_16x16x32_bf16 v[70:73], v[136:139], v[204:207], v[70:73]
	v_mfma_f32_16x16x32_bf16 v[66:69], v[144:147], v[204:207], v[66:69]
	v_mfma_f32_16x16x32_bf16 v[46:49], v[136:139], v[214:217], v[46:49]
	v_mfma_f32_16x16x32_bf16 v[42:45], v[144:147], v[214:217], v[42:45]
	v_mfma_f32_16x16x32_bf16 v[30:33], v[136:139], v[230:233], v[30:33]
	v_mfma_f32_16x16x32_bf16 v[26:29], v[144:147], v[230:233], v[26:29]
	v_mfma_f32_16x16x32_bf16 v[14:17], v[136:139], v[238:241], v[14:17]
	v_mfma_f32_16x16x32_bf16 v[10:13], v[144:147], v[238:241], v[10:13]
	s_setprio 0
	s_setprio 1
	v_mfma_f32_16x16x32_bf16 v[54:57], v[148:151], v[178:181], v[54:57]
	v_mfma_f32_16x16x32_bf16 v[50:53], v[170:173], v[178:181], v[50:53]
	v_mfma_f32_16x16x32_bf16 v[38:41], v[148:151], v[210:213], v[38:41]
	v_mfma_f32_16x16x32_bf16 v[34:37], v[170:173], v[210:213], v[34:37]
	v_mfma_f32_16x16x32_bf16 v[22:25], v[148:151], v[218:221], v[22:25]
	v_mfma_f32_16x16x32_bf16 v[18:21], v[170:173], v[218:221], v[18:21]
	v_mfma_f32_16x16x32_bf16 v[6:9], v[148:151], v[234:237], v[6:9]
	v_mfma_f32_16x16x32_bf16 v[2:5], v[170:173], v[234:237], v[2:5]
	v_mfma_f32_16x16x32_bf16 v[54:57], v[166:169], v[204:207], v[54:57]
	v_mfma_f32_16x16x32_bf16 v[50:53], v[174:177], v[204:207], v[50:53]
	v_mfma_f32_16x16x32_bf16 v[38:41], v[166:169], v[214:217], v[38:41]
	v_mfma_f32_16x16x32_bf16 v[34:37], v[174:177], v[214:217], v[34:37]
	v_mfma_f32_16x16x32_bf16 v[22:25], v[166:169], v[230:233], v[22:25]
	v_mfma_f32_16x16x32_bf16 v[18:21], v[174:177], v[230:233], v[18:21]
	v_mfma_f32_16x16x32_bf16 v[6:9], v[166:169], v[238:241], v[6:9]
	v_mfma_f32_16x16x32_bf16 v[2:5], v[174:177], v[238:241], v[2:5]
	s_setprio 0
	s_barrier
	s_add_i32 s0, 0, 0x18000
	s_add_i32 s18, 0, 0x1c000
	v_add_u32_e32 v144, s0, v159
	v_add_u32_e32 v164, s18, v159
	ds_read_b128 v[132:135], v144
	ds_read_b128 v[136:139], v144 offset:1024
	ds_read_b128 v[140:143], v144 offset:2048
	ds_read_b128 v[144:147], v144 offset:3072
	ds_read_b128 v[148:151], v164
	ds_read_b128 v[166:169], v164 offset:1024
	ds_read_b128 v[170:173], v164 offset:2048
	ds_read_b128 v[174:177], v164 offset:3072
	ds_read_b128 v[178:181], v186 offset:32768
	ds_read_b128 v[204:207], v186 offset:33792
	ds_read_b128 v[210:213], v186 offset:34816
	ds_read_b128 v[214:217], v186 offset:35840
	ds_read_b128 v[218:221], v186 offset:36864
	ds_read_b128 v[230:233], v186 offset:37888
	ds_read2_b32 v[190:191], v131 offset0:2 offset1:3
	ds_read_b128 v[234:237], v186 offset:38912
	ds_read_b128 v[238:241], v186 offset:39936
	s_mov_b32 m0, s73
	s_waitcnt lgkmcnt(0)
	global_load_lds_dwordx4 v190, s[16:17]
	s_mov_b32 m0, s74
	s_nop 0
	global_load_lds_dwordx4 v191, s[16:17]
	s_waitcnt vmcnt(8)
	s_waitcnt lgkmcnt(0)
	s_barrier
	s_setprio 1
	v_mfma_f32_16x16x32_bf16 v[126:129], v[132:135], v[178:181], v[126:129]
	v_mfma_f32_16x16x32_bf16 v[122:125], v[140:143], v[178:181], v[122:125]
	v_mfma_f32_16x16x32_bf16 v[110:113], v[132:135], v[210:213], v[110:113]
	v_mfma_f32_16x16x32_bf16 v[106:109], v[140:143], v[210:213], v[106:109]
	v_mfma_f32_16x16x32_bf16 v[94:97], v[132:135], v[218:221], v[94:97]
	v_mfma_f32_16x16x32_bf16 v[90:93], v[140:143], v[218:221], v[90:93]
	v_mfma_f32_16x16x32_bf16 v[78:81], v[132:135], v[234:237], v[78:81]
	v_mfma_f32_16x16x32_bf16 v[74:77], v[140:143], v[234:237], v[74:77]
	v_mfma_f32_16x16x32_bf16 v[126:129], v[136:139], v[204:207], v[126:129]
	v_mfma_f32_16x16x32_bf16 v[122:125], v[144:147], v[204:207], v[122:125]
	v_mfma_f32_16x16x32_bf16 v[110:113], v[136:139], v[214:217], v[110:113]
	v_mfma_f32_16x16x32_bf16 v[106:109], v[144:147], v[214:217], v[106:109]
	v_mfma_f32_16x16x32_bf16 v[94:97], v[136:139], v[230:233], v[94:97]
	v_mfma_f32_16x16x32_bf16 v[90:93], v[144:147], v[230:233], v[90:93]
	v_mfma_f32_16x16x32_bf16 v[78:81], v[136:139], v[238:241], v[78:81]
	v_mfma_f32_16x16x32_bf16 v[74:77], v[144:147], v[238:241], v[74:77]
	s_setprio 0
	s_setprio 1
	v_mfma_f32_16x16x32_bf16 v[118:121], v[148:151], v[178:181], v[118:121]
	v_mfma_f32_16x16x32_bf16 v[114:117], v[170:173], v[178:181], v[114:117]
	v_mfma_f32_16x16x32_bf16 v[102:105], v[148:151], v[210:213], v[102:105]
	v_mfma_f32_16x16x32_bf16 v[98:101], v[170:173], v[210:213], v[98:101]
	v_mfma_f32_16x16x32_bf16 v[86:89], v[148:151], v[218:221], v[86:89]
	v_mfma_f32_16x16x32_bf16 v[82:85], v[170:173], v[218:221], v[82:85]
	v_mfma_f32_16x16x32_bf16 v[62:65], v[148:151], v[234:237], v[62:65]
	v_mfma_f32_16x16x32_bf16 v[58:61], v[170:173], v[234:237], v[58:61]
	v_mfma_f32_16x16x32_bf16 v[118:121], v[166:169], v[204:207], v[118:121]
	v_mfma_f32_16x16x32_bf16 v[114:117], v[174:177], v[204:207], v[114:117]
	v_mfma_f32_16x16x32_bf16 v[102:105], v[166:169], v[214:217], v[102:105]
	v_mfma_f32_16x16x32_bf16 v[98:101], v[174:177], v[214:217], v[98:101]
	v_mfma_f32_16x16x32_bf16 v[86:89], v[166:169], v[230:233], v[86:89]
	v_mfma_f32_16x16x32_bf16 v[82:85], v[174:177], v[230:233], v[82:85]
	v_mfma_f32_16x16x32_bf16 v[62:65], v[166:169], v[238:241], v[62:65]
	v_mfma_f32_16x16x32_bf16 v[58:61], v[174:177], v[238:241], v[58:61]
	s_setprio 0
	s_barrier
	s_add_i32 s0, s0, s70
	v_lshl_add_u64 v[152:153], v[152:153], 0, s[30:31]
	s_mov_b32 m0, s0
	ds_read_b128 v[178:181], v186 offset:49152
	ds_read_b128 v[204:207], v186 offset:50176
	ds_read_b128 v[210:213], v186 offset:51200
	ds_read_b128 v[214:217], v186 offset:52224
	ds_read_b128 v[218:221], v186 offset:53248
	ds_read_b128 v[230:233], v186 offset:54272
	ds_read_b128 v[234:237], v186 offset:55296
	ds_read_b128 v[238:241], v186 offset:56320
	global_load_lds_dwordx4 v[152:153], off
	s_add_i32 m0, s0, 0x2000
	s_add_u32 s0, s14, 0x200080
	v_lshl_add_u64 v[152:153], v[182:183], 0, s[30:31]
	s_addc_u32 s1, s15, 0
	s_add_i32 s14, s18, s70
	global_load_lds_dwordx4 v[152:153], off
	s_mov_b32 m0, s14
	s_nop 0
	global_load_lds_dwordx4 v160, s[0:1]
	s_add_i32 m0, s14, 0x2000
	s_nop 0
	global_load_lds_dwordx4 v162, s[0:1]
	ds_read2_b32 v[152:153], v131 offset1:1
	s_mov_b32 m0, s75
	s_waitcnt lgkmcnt(0)
	v_mov_b32_e32 v164, v152
	v_lshl_add_u64 v[182:183], s[16:17], 0, v[164:165]
	v_mov_b32_e32 v164, v153
	v_lshl_add_u64 v[182:183], v[182:183], 0, s[30:31]
	v_lshl_add_u64 v[152:153], s[16:17], 0, v[164:165]
	global_load_lds_dwordx4 v[182:183], off
	v_lshl_add_u64 v[152:153], v[152:153], 0, s[30:31]
	s_mov_b32 m0, s76
	s_nop 0
	global_load_lds_dwordx4 v[152:153], off
	s_waitcnt vmcnt(8)
	s_waitcnt lgkmcnt(0)
	s_barrier
	s_setprio 1
	v_mfma_f32_16x16x32_bf16 v[70:73], v[132:135], v[178:181], v[70:73]
	v_mfma_f32_16x16x32_bf16 v[66:69], v[140:143], v[178:181], v[66:69]
	v_mfma_f32_16x16x32_bf16 v[46:49], v[132:135], v[210:213], v[46:49]
	v_mfma_f32_16x16x32_bf16 v[42:45], v[140:143], v[210:213], v[42:45]
	v_mfma_f32_16x16x32_bf16 v[30:33], v[132:135], v[218:221], v[30:33]
	v_mfma_f32_16x16x32_bf16 v[26:29], v[140:143], v[218:221], v[26:29]
	v_mfma_f32_16x16x32_bf16 v[14:17], v[132:135], v[234:237], v[14:17]
	v_mfma_f32_16x16x32_bf16 v[10:13], v[140:143], v[234:237], v[10:13]
	v_mfma_f32_16x16x32_bf16 v[70:73], v[136:139], v[204:207], v[70:73]
	v_mfma_f32_16x16x32_bf16 v[66:69], v[144:147], v[204:207], v[66:69]
	v_mfma_f32_16x16x32_bf16 v[46:49], v[136:139], v[214:217], v[46:49]
	v_mfma_f32_16x16x32_bf16 v[42:45], v[144:147], v[214:217], v[42:45]
	v_mfma_f32_16x16x32_bf16 v[30:33], v[136:139], v[230:233], v[30:33]
	v_mfma_f32_16x16x32_bf16 v[26:29], v[144:147], v[230:233], v[26:29]
	v_mfma_f32_16x16x32_bf16 v[14:17], v[136:139], v[238:241], v[14:17]
	v_mfma_f32_16x16x32_bf16 v[10:13], v[144:147], v[238:241], v[10:13]
	s_setprio 0
	s_setprio 1
	v_mfma_f32_16x16x32_bf16 v[54:57], v[148:151], v[178:181], v[54:57]
	v_mfma_f32_16x16x32_bf16 v[50:53], v[170:173], v[178:181], v[50:53]
	v_mfma_f32_16x16x32_bf16 v[38:41], v[148:151], v[210:213], v[38:41]
	v_mfma_f32_16x16x32_bf16 v[34:37], v[170:173], v[210:213], v[34:37]
	v_mfma_f32_16x16x32_bf16 v[22:25], v[148:151], v[218:221], v[22:25]
	v_mfma_f32_16x16x32_bf16 v[18:21], v[170:173], v[218:221], v[18:21]
	v_mfma_f32_16x16x32_bf16 v[6:9], v[148:151], v[234:237], v[6:9]
	v_mfma_f32_16x16x32_bf16 v[2:5], v[170:173], v[234:237], v[2:5]
	v_mfma_f32_16x16x32_bf16 v[54:57], v[166:169], v[204:207], v[54:57]
	v_mfma_f32_16x16x32_bf16 v[50:53], v[174:177], v[204:207], v[50:53]
	v_mfma_f32_16x16x32_bf16 v[38:41], v[166:169], v[214:217], v[38:41]
	v_mfma_f32_16x16x32_bf16 v[34:37], v[174:177], v[214:217], v[34:37]
	v_mfma_f32_16x16x32_bf16 v[22:25], v[166:169], v[230:233], v[22:25]
	v_mfma_f32_16x16x32_bf16 v[18:21], v[174:177], v[230:233], v[18:21]
	v_mfma_f32_16x16x32_bf16 v[6:9], v[166:169], v[238:241], v[6:9]
	v_mfma_f32_16x16x32_bf16 v[2:5], v[174:177], v[238:241], v[2:5]
	s_setprio 0
	s_barrier
	s_add_i32 s0, s88, 2
	s_cmp_gt_u32 s88, 5
	s_cbranch_scc1 .LBB0_1129
	s_mov_b32 s88, s0
	s_branch .LBB0_1115

.LBB0_1469:
	s_mov_b64 s[14:15], 0x80
	s_add_i32 m0, s41, 0x18000
	v_lshl_add_u64 v[8:9], v[8:9], 0, s[14:15]
	s_and_b32 s9, s5, 3
	s_lshl_b32 s47, s4, 6
	s_lshl_b32 s17, s4, 13
	s_waitcnt vmcnt(2)
	s_barrier
	global_load_lds_dwordx4 v[8:9], off
	v_lshl_add_u64 v[6:7], v[6:7], 0, s[14:15]
	s_add_i32 m0, s41, 0x1a000
	s_add_i32 s48, s41, 0x8000
	s_add_i32 s49, s41, 0xa000
	global_load_lds_dwordx4 v[6:7], off
	v_lshl_add_u64 v[4:5], v[4:5], 0, s[14:15]
	s_mov_b32 m0, s48
	s_add_u32 s4, s36, 0x10080
	global_load_lds_dwordx4 v[4:5], off
	v_lshl_add_u64 v[2:3], v[2:3], 0, s[14:15]
	s_mov_b32 m0, s49
	s_addc_u32 s5, s37, 0
	global_load_lds_dwordx4 v[2:3], off
	s_add_i32 m0, s41, 0x1c000
	global_load_lds_dwordx4 v148, s[4:5]
	v_lshl_add_u64 v[2:3], s[4:5], 0, v[152:153]
	s_add_i32 m0, s41, 0x1e000
	v_lshlrev_b32_e32 v4, 11, v159
	global_load_lds_dwordx4 v[2:3], off
	v_lshl_or_b32 v2, v222, 6, v210
	v_and_b32_e32 v3, 32, v154
	v_bitop3_b32 v2, v2, s17, v3 bitop3:0xde
	v_lshlrev_b32_e32 v3, 8, v0
	v_and_b32_e32 v3, 0x18000, v3
	v_or3_b32 v3, v1, v3, v4
	v_add_u32_e32 v162, v3, v155
	v_lshlrev_b32_e32 v3, 4, v195
	s_waitcnt vmcnt(6)
	s_cmpk_lt_u32 s16, 0x100
	v_readlane_b32 s60, v253, 18
	v_and_b32_e32 v3, 0x38000, v3
	v_lshl_or_b32 v212, s9, 12, v211
	s_cselect_b64 s[16:17], -1, 0
	v_lshlrev_b32_e32 v156, 2, v209
	v_readlane_b32 s61, v253, 19
	v_readlane_b32 s62, v253, 20
	v_readlane_b32 s63, v253, 21
	v_readlane_b32 s66, v253, 24
	v_readlane_b32 s67, v253, 25
	v_or3_b32 v3, v1, v3, v4
	s_add_i32 s52, 0, 0x10000
	s_add_i32 s53, 0, 0x14000
	s_ashr_i32 s50, s33, 31
	s_ashr_i32 s51, s89, 31
	v_lshl_add_u64 v[160:161], s[66:67], 0, v[156:157]
	v_lshl_or_b32 v213, s9, 6, v209
	v_mov_b32_e32 v163, v157
	v_add_u32_e32 v164, v3, v155
	v_mov_b32_e32 v165, v157
	v_mov_b64_e32 v[166:167], 0x200
	v_mov_b64_e32 v[168:169], 0x1ff
	v_add_u32_e32 v214, s52, v212
	v_add_u32_e32 v215, s53, v212
	v_add_u32_e32 v216, 0, v2
	s_mov_b32 s56, 0x800000
	s_movk_i32 s57, 0x4010
	s_movk_i32 s60, 0x3fff
	s_movk_i32 s61, 0x3f80
	s_movk_i32 s62, 0x3f70
	s_movk_i32 s63, 0x3f60
	v_mbcnt_hi_u32_b32 v217, -1, v227
	s_barrier
	v_readlane_b32 s64, v253, 22
	v_readlane_b32 s65, v253, 23
	v_readlane_b32 s68, v253, 26
	v_readlane_b32 s69, v253, 27
	v_readlane_b32 s70, v253, 28
	v_readlane_b32 s71, v253, 29
	v_readlane_b32 s72, v253, 30
	v_readlane_b32 s73, v253, 31
	v_readlane_b32 s74, v253, 32
	v_readlane_b32 s75, v253, 33
	s_branch .LBB0_1472

.LBB0_1479:
	s_waitcnt vmcnt(0)
	ds_read_b128 v[66:69], v214
	ds_read_b128 v[70:73], v214 offset:1024
	ds_read_b128 v[74:77], v214 offset:2048
	ds_read_b128 v[78:81], v214 offset:3072
	ds_read_b128 v[170:173], v215
	ds_read_b128 v[174:177], v215 offset:1024
	ds_read_b128 v[178:181], v215 offset:2048
	ds_read_b128 v[182:185], v215 offset:3072
	s_add_u32 s36, s6, 0xfffc0080
	s_addc_u32 s37, s7, -1
	s_cmp_eq_u32 s66, 12
	s_cselect_b32 s39, s9, s37
	s_cselect_b32 s38, s21, s36
	s_cselect_b32 s37, s19, s65
	s_cselect_b32 s36, s35, s64
	s_add_i32 m0, s41, 0xc000
	ds_read_b128 v[186:189], v216
	ds_read_b128 v[196:199], v216 offset:1024
	ds_read_b128 v[200:203], v216 offset:2048
	ds_read_b128 v[204:207], v216 offset:3072
	ds_read_b128 v[218:221], v216 offset:4096
	ds_read_b128 v[230:233], v216 offset:5120
	ds_read_b128 v[234:237], v216 offset:6144
	ds_read_b128 v[238:241], v216 offset:7168
	global_load_lds_dwordx4 v162, s[6:7]
	s_add_i32 m0, s41, 0xe000
	s_nop 0
	global_load_lds_dwordx4 v164, s[6:7]
	s_waitcnt vmcnt(8)
	s_waitcnt lgkmcnt(0)
	s_barrier
	s_setprio 1
	s_waitcnt lgkmcnt(0)
	v_mfma_f32_16x16x32_bf16 v[142:145], v[66:69], v[186:189], v[142:145]
	v_mfma_f32_16x16x32_bf16 v[138:141], v[74:77], v[186:189], v[138:141]
	v_mfma_f32_16x16x32_bf16 v[126:129], v[66:69], v[200:203], v[126:129]
	v_mfma_f32_16x16x32_bf16 v[122:125], v[74:77], v[200:203], v[122:125]
	v_mfma_f32_16x16x32_bf16 v[110:113], v[66:69], v[218:221], v[110:113]
	v_mfma_f32_16x16x32_bf16 v[106:109], v[74:77], v[218:221], v[106:109]
	v_mfma_f32_16x16x32_bf16 v[94:97], v[66:69], v[234:237], v[94:97]
	v_mfma_f32_16x16x32_bf16 v[90:93], v[74:77], v[234:237], v[90:93]
	v_mfma_f32_16x16x32_bf16 v[142:145], v[70:73], v[196:199], v[142:145]
	v_mfma_f32_16x16x32_bf16 v[138:141], v[78:81], v[196:199], v[138:141]
	v_mfma_f32_16x16x32_bf16 v[126:129], v[70:73], v[204:207], v[126:129]
	v_mfma_f32_16x16x32_bf16 v[122:125], v[78:81], v[204:207], v[122:125]
	v_mfma_f32_16x16x32_bf16 v[110:113], v[70:73], v[230:233], v[110:113]
	v_mfma_f32_16x16x32_bf16 v[106:109], v[78:81], v[230:233], v[106:109]
	v_mfma_f32_16x16x32_bf16 v[94:97], v[70:73], v[238:241], v[94:97]
	v_mfma_f32_16x16x32_bf16 v[90:93], v[78:81], v[238:241], v[90:93]
	s_setprio 0
	s_setprio 1
	v_mfma_f32_16x16x32_bf16 v[134:137], v[170:173], v[186:189], v[134:137]
	v_mfma_f32_16x16x32_bf16 v[130:133], v[178:181], v[186:189], v[130:133]
	v_mfma_f32_16x16x32_bf16 v[118:121], v[170:173], v[200:203], v[118:121]
	v_mfma_f32_16x16x32_bf16 v[114:117], v[178:181], v[200:203], v[114:117]
	v_mfma_f32_16x16x32_bf16 v[102:105], v[170:173], v[218:221], v[102:105]
	v_mfma_f32_16x16x32_bf16 v[98:101], v[178:181], v[218:221], v[98:101]
	v_mfma_f32_16x16x32_bf16 v[86:89], v[170:173], v[234:237], v[86:89]
	v_mfma_f32_16x16x32_bf16 v[82:85], v[178:181], v[234:237], v[82:85]
	v_mfma_f32_16x16x32_bf16 v[134:137], v[174:177], v[196:199], v[134:137]
	v_mfma_f32_16x16x32_bf16 v[130:133], v[182:185], v[196:199], v[130:133]
	v_mfma_f32_16x16x32_bf16 v[118:121], v[174:177], v[204:207], v[118:121]
	v_mfma_f32_16x16x32_bf16 v[114:117], v[182:185], v[204:207], v[114:117]
	v_mfma_f32_16x16x32_bf16 v[102:105], v[174:177], v[230:233], v[102:105]
	v_mfma_f32_16x16x32_bf16 v[98:101], v[182:185], v[230:233], v[98:101]
	v_mfma_f32_16x16x32_bf16 v[86:89], v[174:177], v[238:241], v[86:89]
	v_mfma_f32_16x16x32_bf16 v[82:85], v[182:185], v[238:241], v[82:85]
	s_setprio 0
	s_barrier
	s_add_i32 s67, s52, s40
	v_lshl_add_u64 v[190:191], s[36:37], 0, v[148:149]
	s_mov_b32 m0, s67
	ds_read_b128 v[186:189], v216 offset:16384
	ds_read_b128 v[196:199], v216 offset:17408
	ds_read_b128 v[200:203], v216 offset:18432
	ds_read_b128 v[204:207], v216 offset:19456
	ds_read_b128 v[218:221], v216 offset:20480
	ds_read_b128 v[230:233], v216 offset:21504
	ds_read_b128 v[234:237], v216 offset:22528
	ds_read_b128 v[238:241], v216 offset:23552
	global_load_lds_dwordx4 v[190:191], off
	s_add_i32 m0, s67, 0x2000
	s_add_u32 s68, s36, 0x10000
	v_lshl_add_u64 v[242:243], s[36:37], 0, v[152:153]
	s_addc_u32 s69, s37, 0
	s_add_i32 s67, s53, s40
	global_load_lds_dwordx4 v[242:243], off
	s_mov_b32 m0, s67
	v_lshl_add_u64 v[246:247], s[38:39], 0, v[150:151]
	global_load_lds_dwordx4 v148, s[68:69]
	s_add_i32 m0, s67, 0x2000
	s_nop 0
	global_load_lds_dwordx4 v152, s[68:69]
	v_lshl_add_u64 v[244:245], s[38:39], 0, v[146:147]
	s_mov_b32 m0, s41
	s_nop 0
	global_load_lds_dwordx4 v[244:245], off
	s_mov_b32 m0, s42
	s_nop 0
	global_load_lds_dwordx4 v[246:247], off
	s_waitcnt vmcnt(8)
	s_waitcnt lgkmcnt(0)
	s_barrier
	s_setprio 1
	s_waitcnt lgkmcnt(0)
	v_mfma_f32_16x16x32_bf16 v[62:65], v[66:69], v[186:189], v[62:65]
	v_mfma_f32_16x16x32_bf16 v[58:61], v[74:77], v[186:189], v[58:61]
	v_mfma_f32_16x16x32_bf16 v[46:49], v[66:69], v[200:203], v[46:49]
	v_mfma_f32_16x16x32_bf16 v[42:45], v[74:77], v[200:203], v[42:45]
	v_mfma_f32_16x16x32_bf16 v[30:33], v[66:69], v[218:221], v[30:33]
	v_mfma_f32_16x16x32_bf16 v[26:29], v[74:77], v[218:221], v[26:29]
	v_mfma_f32_16x16x32_bf16 v[14:17], v[66:69], v[234:237], v[14:17]
	v_mfma_f32_16x16x32_bf16 v[10:13], v[74:77], v[234:237], v[10:13]
	v_mfma_f32_16x16x32_bf16 v[62:65], v[70:73], v[196:199], v[62:65]
	v_mfma_f32_16x16x32_bf16 v[58:61], v[78:81], v[196:199], v[58:61]
	v_mfma_f32_16x16x32_bf16 v[46:49], v[70:73], v[204:207], v[46:49]
	v_mfma_f32_16x16x32_bf16 v[42:45], v[78:81], v[204:207], v[42:45]
	v_mfma_f32_16x16x32_bf16 v[30:33], v[70:73], v[230:233], v[30:33]
	v_mfma_f32_16x16x32_bf16 v[26:29], v[78:81], v[230:233], v[26:29]
	v_mfma_f32_16x16x32_bf16 v[14:17], v[70:73], v[238:241], v[14:17]
	v_mfma_f32_16x16x32_bf16 v[10:13], v[78:81], v[238:241], v[10:13]
	s_setprio 0
	s_setprio 1
	v_mfma_f32_16x16x32_bf16 v[54:57], v[170:173], v[186:189], v[54:57]
	v_mfma_f32_16x16x32_bf16 v[50:53], v[178:181], v[186:189], v[50:53]
	v_mfma_f32_16x16x32_bf16 v[38:41], v[170:173], v[200:203], v[38:41]
	v_mfma_f32_16x16x32_bf16 v[34:37], v[178:181], v[200:203], v[34:37]
	v_mfma_f32_16x16x32_bf16 v[22:25], v[170:173], v[218:221], v[22:25]
	v_mfma_f32_16x16x32_bf16 v[18:21], v[178:181], v[218:221], v[18:21]
	v_mfma_f32_16x16x32_bf16 v[6:9], v[170:173], v[234:237], v[6:9]
	v_mfma_f32_16x16x32_bf16 v[2:5], v[178:181], v[234:237], v[2:5]
	v_mfma_f32_16x16x32_bf16 v[54:57], v[174:177], v[196:199], v[54:57]
	v_mfma_f32_16x16x32_bf16 v[50:53], v[182:185], v[196:199], v[50:53]
	v_mfma_f32_16x16x32_bf16 v[38:41], v[174:177], v[204:207], v[38:41]
	v_mfma_f32_16x16x32_bf16 v[34:37], v[182:185], v[204:207], v[34:37]
	v_mfma_f32_16x16x32_bf16 v[22:25], v[174:177], v[230:233], v[22:25]
	v_mfma_f32_16x16x32_bf16 v[18:21], v[182:185], v[230:233], v[18:21]
	v_mfma_f32_16x16x32_bf16 v[6:9], v[174:177], v[238:241], v[6:9]
	v_mfma_f32_16x16x32_bf16 v[2:5], v[182:185], v[238:241], v[2:5]
	s_setprio 0
	s_barrier
	s_add_i32 s67, 0, 0x18000
	s_add_i32 s68, 0, 0x1c000
	v_add_u32_e32 v78, s67, v212
	v_add_u32_e32 v156, s68, v212
	ds_read_b128 v[66:69], v78
	ds_read_b128 v[70:73], v78 offset:1024
	ds_read_b128 v[74:77], v78 offset:2048
	ds_read_b128 v[78:81], v78 offset:3072
	ds_read_b128 v[170:173], v156
	ds_read_b128 v[174:177], v156 offset:1024
	ds_read_b128 v[178:181], v156 offset:2048
	ds_read_b128 v[182:185], v156 offset:3072
	s_add_u32 s38, s38, 0x40000
	s_addc_u32 s39, s39, 0
	s_mov_b32 m0, s43
	ds_read_b128 v[186:189], v216 offset:32768
	ds_read_b128 v[196:199], v216 offset:33792
	ds_read_b128 v[200:203], v216 offset:34816
	ds_read_b128 v[204:207], v216 offset:35840
	ds_read_b128 v[218:221], v216 offset:36864
	ds_read_b128 v[230:233], v216 offset:37888
	ds_read_b128 v[234:237], v216 offset:38912
	ds_read_b128 v[238:241], v216 offset:39936
	global_load_lds_dwordx4 v146, s[38:39]
	s_mov_b32 m0, s44
	s_nop 0
	global_load_lds_dwordx4 v150, s[38:39]
	s_waitcnt vmcnt(8)
	s_waitcnt lgkmcnt(0)
	s_barrier
	s_setprio 1
	s_waitcnt lgkmcnt(0)
	v_mfma_f32_16x16x32_bf16 v[142:145], v[66:69], v[186:189], v[142:145]
	v_mfma_f32_16x16x32_bf16 v[138:141], v[74:77], v[186:189], v[138:141]
	v_mfma_f32_16x16x32_bf16 v[126:129], v[66:69], v[200:203], v[126:129]
	v_mfma_f32_16x16x32_bf16 v[122:125], v[74:77], v[200:203], v[122:125]
	v_mfma_f32_16x16x32_bf16 v[110:113], v[66:69], v[218:221], v[110:113]
	v_mfma_f32_16x16x32_bf16 v[106:109], v[74:77], v[218:221], v[106:109]
	v_mfma_f32_16x16x32_bf16 v[94:97], v[66:69], v[234:237], v[94:97]
	v_mfma_f32_16x16x32_bf16 v[90:93], v[74:77], v[234:237], v[90:93]
	v_mfma_f32_16x16x32_bf16 v[142:145], v[70:73], v[196:199], v[142:145]
	v_mfma_f32_16x16x32_bf16 v[138:141], v[78:81], v[196:199], v[138:141]
	v_mfma_f32_16x16x32_bf16 v[126:129], v[70:73], v[204:207], v[126:129]
	v_mfma_f32_16x16x32_bf16 v[122:125], v[78:81], v[204:207], v[122:125]
	v_mfma_f32_16x16x32_bf16 v[110:113], v[70:73], v[230:233], v[110:113]
	v_mfma_f32_16x16x32_bf16 v[106:109], v[78:81], v[230:233], v[106:109]
	v_mfma_f32_16x16x32_bf16 v[94:97], v[70:73], v[238:241], v[94:97]
	v_mfma_f32_16x16x32_bf16 v[90:93], v[78:81], v[238:241], v[90:93]
	s_setprio 0
	s_setprio 1
	v_mfma_f32_16x16x32_bf16 v[134:137], v[170:173], v[186:189], v[134:137]
	v_mfma_f32_16x16x32_bf16 v[130:133], v[178:181], v[186:189], v[130:133]
	v_mfma_f32_16x16x32_bf16 v[118:121], v[170:173], v[200:203], v[118:121]
	v_mfma_f32_16x16x32_bf16 v[114:117], v[178:181], v[200:203], v[114:117]
	v_mfma_f32_16x16x32_bf16 v[102:105], v[170:173], v[218:221], v[102:105]
	v_mfma_f32_16x16x32_bf16 v[98:101], v[178:181], v[218:221], v[98:101]
	v_mfma_f32_16x16x32_bf16 v[86:89], v[170:173], v[234:237], v[86:89]
	v_mfma_f32_16x16x32_bf16 v[82:85], v[178:181], v[234:237], v[82:85]
	v_mfma_f32_16x16x32_bf16 v[134:137], v[174:177], v[196:199], v[134:137]
	v_mfma_f32_16x16x32_bf16 v[130:133], v[182:185], v[196:199], v[130:133]
	v_mfma_f32_16x16x32_bf16 v[118:121], v[174:177], v[204:207], v[118:121]
	v_mfma_f32_16x16x32_bf16 v[114:117], v[182:185], v[204:207], v[114:117]
	v_mfma_f32_16x16x32_bf16 v[102:105], v[174:177], v[230:233], v[102:105]
	v_mfma_f32_16x16x32_bf16 v[98:101], v[182:185], v[230:233], v[98:101]
	v_mfma_f32_16x16x32_bf16 v[86:89], v[174:177], v[238:241], v[86:89]
	v_mfma_f32_16x16x32_bf16 v[82:85], v[182:185], v[238:241], v[82:85]
	s_setprio 0
	s_barrier
	s_add_i32 s38, s67, s40
	v_lshl_add_u64 v[190:191], v[190:191], 0, s[14:15]
	s_mov_b32 m0, s38
	ds_read_b128 v[186:189], v216 offset:49152
	ds_read_b128 v[196:199], v216 offset:50176
	ds_read_b128 v[200:203], v216 offset:51200
	ds_read_b128 v[204:207], v216 offset:52224
	ds_read_b128 v[218:221], v216 offset:53248
	ds_read_b128 v[230:233], v216 offset:54272
	ds_read_b128 v[234:237], v216 offset:55296
	ds_read_b128 v[238:241], v216 offset:56320
	global_load_lds_dwordx4 v[190:191], off
	s_add_i32 m0, s38, 0x2000
	s_add_u32 s36, s36, 0x10080
	v_lshl_add_u64 v[190:191], v[242:243], 0, s[14:15]
	s_addc_u32 s37, s37, 0
	s_add_i32 s38, s68, s40
	global_load_lds_dwordx4 v[190:191], off
	s_mov_b32 m0, s38
	s_nop 0
	global_load_lds_dwordx4 v148, s[36:37]
	s_add_i32 m0, s38, 0x2000
	s_nop 0
	global_load_lds_dwordx4 v152, s[36:37]
	v_lshl_add_u64 v[190:191], v[244:245], 0, s[14:15]
	s_mov_b32 m0, s48
	s_nop 0
	global_load_lds_dwordx4 v[190:191], off
	v_lshl_add_u64 v[190:191], v[246:247], 0, s[14:15]
	s_mov_b32 m0, s49
	s_nop 0
	global_load_lds_dwordx4 v[190:191], off
	s_waitcnt vmcnt(8)
	s_waitcnt lgkmcnt(0)
	s_barrier
	s_setprio 1
	s_waitcnt lgkmcnt(0)
	v_mfma_f32_16x16x32_bf16 v[62:65], v[66:69], v[186:189], v[62:65]
	v_mfma_f32_16x16x32_bf16 v[58:61], v[74:77], v[186:189], v[58:61]
	v_mfma_f32_16x16x32_bf16 v[46:49], v[66:69], v[200:203], v[46:49]
	v_mfma_f32_16x16x32_bf16 v[42:45], v[74:77], v[200:203], v[42:45]
	v_mfma_f32_16x16x32_bf16 v[30:33], v[66:69], v[218:221], v[30:33]
	v_mfma_f32_16x16x32_bf16 v[26:29], v[74:77], v[218:221], v[26:29]
	v_mfma_f32_16x16x32_bf16 v[14:17], v[66:69], v[234:237], v[14:17]
	v_mfma_f32_16x16x32_bf16 v[10:13], v[74:77], v[234:237], v[10:13]
	v_mfma_f32_16x16x32_bf16 v[62:65], v[70:73], v[196:199], v[62:65]
	v_mfma_f32_16x16x32_bf16 v[58:61], v[78:81], v[196:199], v[58:61]
	v_mfma_f32_16x16x32_bf16 v[46:49], v[70:73], v[204:207], v[46:49]
	v_mfma_f32_16x16x32_bf16 v[42:45], v[78:81], v[204:207], v[42:45]
	v_mfma_f32_16x16x32_bf16 v[30:33], v[70:73], v[230:233], v[30:33]
	v_mfma_f32_16x16x32_bf16 v[26:29], v[78:81], v[230:233], v[26:29]
	v_mfma_f32_16x16x32_bf16 v[14:17], v[70:73], v[238:241], v[14:17]
	v_mfma_f32_16x16x32_bf16 v[10:13], v[78:81], v[238:241], v[10:13]
	s_setprio 0
	s_setprio 1
	v_mfma_f32_16x16x32_bf16 v[54:57], v[170:173], v[186:189], v[54:57]
	v_mfma_f32_16x16x32_bf16 v[50:53], v[178:181], v[186:189], v[50:53]
	v_mfma_f32_16x16x32_bf16 v[38:41], v[170:173], v[200:203], v[38:41]
	v_mfma_f32_16x16x32_bf16 v[34:37], v[178:181], v[200:203], v[34:37]
	v_mfma_f32_16x16x32_bf16 v[22:25], v[170:173], v[218:221], v[22:25]
	v_mfma_f32_16x16x32_bf16 v[18:21], v[178:181], v[218:221], v[18:21]
	v_mfma_f32_16x16x32_bf16 v[6:9], v[170:173], v[234:237], v[6:9]
	v_mfma_f32_16x16x32_bf16 v[2:5], v[178:181], v[234:237], v[2:5]
	v_mfma_f32_16x16x32_bf16 v[54:57], v[174:177], v[196:199], v[54:57]
	v_mfma_f32_16x16x32_bf16 v[50:53], v[182:185], v[196:199], v[50:53]
	v_mfma_f32_16x16x32_bf16 v[38:41], v[174:177], v[204:207], v[38:41]
	v_mfma_f32_16x16x32_bf16 v[34:37], v[182:185], v[204:207], v[34:37]
	v_mfma_f32_16x16x32_bf16 v[22:25], v[174:177], v[230:233], v[22:25]
	v_mfma_f32_16x16x32_bf16 v[18:21], v[182:185], v[230:233], v[18:21]
	v_mfma_f32_16x16x32_bf16 v[6:9], v[174:177], v[238:241], v[6:9]
	v_mfma_f32_16x16x32_bf16 v[2:5], v[182:185], v[238:241], v[2:5]
	s_setprio 0
	s_barrier
	s_add_i32 s66, s66, 2
	s_add_u32 s6, s6, 0x100
	s_addc_u32 s7, s7, 0
	s_add_u32 s64, s64, 0x100
	s_addc_u32 s65, s65, 0
	s_cmp_gt_u32 s66, 13
	s_cbranch_scc0 .LBB0_1479
	s_and_b64 vcc, exec, s[16:17]
	s_cbranch_vccz .LBB0_1482
	s_barrier

.LBB0_1589:
	s_and_b32 s14, s8, 3
	s_mov_b64 s[8:9], 0x80
	s_add_i32 m0, s35, 0x18000
	v_lshl_add_u64 v[8:9], v[8:9], 0, s[8:9]
	s_lshl_b32 s11, s5, 13
	s_waitcnt vmcnt(2)
	s_barrier
	global_load_lds_dwordx4 v[8:9], off
	v_lshl_add_u64 v[4:5], v[4:5], 0, s[8:9]
	s_add_i32 m0, s35, 0x1a000
	s_add_i32 s47, s35, 0x8000
	s_add_i32 s48, s35, 0xa000
	global_load_lds_dwordx4 v[4:5], off
	v_lshl_add_u64 v[2:3], v[2:3], 0, s[8:9]
	s_mov_b32 m0, s47
	s_add_u32 s16, s38, 0x10080
	global_load_lds_dwordx4 v[2:3], off
	v_lshl_add_u64 v[2:3], v[6:7], 0, s[8:9]
	s_mov_b32 m0, s48
	s_addc_u32 s17, s39, 0
	global_load_lds_dwordx4 v[2:3], off
	s_add_i32 m0, s35, 0x1c000
	global_load_lds_dwordx4 v148, s[16:17]
	v_lshl_add_u64 v[2:3], s[16:17], 0, v[152:153]
	s_add_i32 m0, s35, 0x1e000
	v_readlane_b32 s60, v253, 18
	global_load_lds_dwordx4 v[2:3], off
	v_lshl_or_b32 v2, v222, 6, v210
	v_and_b32_e32 v3, 32, v154
	v_bitop3_b32 v4, v2, s11, v3 bitop3:0xde
	v_lshlrev_b32_e32 v2, 2, v209
	v_mov_b32_e32 v3, v149
	v_readlane_b32 s70, v253, 28
	v_readlane_b32 s71, v253, 29
	s_waitcnt vmcnt(6)
	s_cmpk_lt_u32 s10, 0x100
	v_lshl_or_b32 v171, s14, 12, v211
	v_lshl_add_u64 v[130:131], s[70:71], 0, v[2:3]
	v_lshlrev_b32_e32 v2, 8, v0
	v_and_b32_e32 v2, 0x18000, v2
	v_lshlrev_b32_e32 v3, 11, v159
	v_or3_b32 v2, v1, v2, v3
	v_add_u32_e32 v132, v2, v155
	v_lshlrev_b32_e32 v2, 4, v195
	v_and_b32_e32 v2, 0x38000, v2
	s_cselect_b64 s[10:11], -1, 0
	v_or3_b32 v1, v1, v2, v3
	s_add_i32 s50, 0, 0x10000
	s_add_i32 s51, 0, 0x14000
	s_sext_i32_i8 s57, s4
	s_waitcnt vmcnt(0)
	v_lshl_or_b32 v170, s5, 6, v222
	s_ashr_i32 s49, s33, 31
	v_lshl_or_b32 v172, s14, 6, v209
	v_mov_b32_e32 v133, v149
	v_add_u32_e32 v134, v1, v155
	v_mov_b32_e32 v135, v149
	v_mov_b64_e32 v[136:137], 0x100
	v_mov_b64_e32 v[138:139], 0xff
	v_add_u32_e32 v1, s50, v171
	v_add_u32_e32 v159, s51, v171
	v_add_u32_e32 v173, 0, v4
	s_mov_b32 s14, 0x3e38aa3b
	v_mbcnt_hi_u32_b32 v174, -1, v227
	s_mov_b32 s52, 0x800000
	s_mov_b32 s53, 0x50000
	s_mov_b64 s[16:17], 0x58000
	s_mov_b32 s56, 0x58000
	s_barrier
	v_readlane_b32 s61, v253, 19
	v_readlane_b32 s62, v253, 20
	v_readlane_b32 s63, v253, 21
	v_readlane_b32 s64, v253, 22
	v_readlane_b32 s65, v253, 23
	v_readlane_b32 s66, v253, 24
	v_readlane_b32 s67, v253, 25
	v_readlane_b32 s68, v253, 26
	v_readlane_b32 s69, v253, 27
	v_readlane_b32 s72, v253, 30
	v_readlane_b32 s73, v253, 31
	v_readlane_b32 s74, v253, 32
	v_readlane_b32 s75, v253, 33
	s_branch .LBB0_1592

.LBB0_1599:
	ds_read_b128 v[140:143], v1
	ds_read_b128 v[154:157], v1 offset:1024
	ds_read_b128 v[160:163], v1 offset:2048
	ds_read_b128 v[164:167], v1 offset:3072
	ds_read_b128 v[176:179], v159
	ds_read_b128 v[180:183], v159 offset:1024
	ds_read_b128 v[184:187], v159 offset:2048
	ds_read_b128 v[196:199], v159 offset:3072
	s_add_u32 s38, s36, 0xfffc0080
	s_addc_u32 s39, s37, -1
	s_cmp_eq_u32 s64, 12
	s_cselect_b32 s41, s21, s39
	s_cselect_b32 s40, s60, s38
	s_cselect_b32 s39, s19, s63
	s_cselect_b32 s38, s61, s62
	s_add_i32 m0, s35, 0xc000
	ds_read_b128 v[200:203], v173
	ds_read_b128 v[204:207], v173 offset:1024
	ds_read_b128 v[210:213], v173 offset:2048
	ds_read_b128 v[214:217], v173 offset:3072
	ds_read_b128 v[218:221], v173 offset:4096
	ds_read_b128 v[230:233], v173 offset:5120
	ds_read_b128 v[234:237], v173 offset:6144
	ds_read_b128 v[238:241], v173 offset:7168
	global_load_lds_dwordx4 v132, s[36:37]
	s_add_i32 m0, s35, 0xe000
	s_nop 0
	global_load_lds_dwordx4 v134, s[36:37]
	s_waitcnt vmcnt(8)
	s_waitcnt lgkmcnt(0)
	s_barrier
	s_setprio 1
	s_waitcnt lgkmcnt(0)
	v_mfma_f32_16x16x32_bf16 v[126:129], v[140:143], v[200:203], v[126:129]
	v_mfma_f32_16x16x32_bf16 v[122:125], v[160:163], v[200:203], v[122:125]
	v_mfma_f32_16x16x32_bf16 v[114:117], v[140:143], v[210:213], v[114:117]
	v_mfma_f32_16x16x32_bf16 v[106:109], v[160:163], v[210:213], v[106:109]
	v_mfma_f32_16x16x32_bf16 v[98:101], v[140:143], v[218:221], v[98:101]
	v_mfma_f32_16x16x32_bf16 v[90:93], v[160:163], v[218:221], v[90:93]
	v_mfma_f32_16x16x32_bf16 v[82:85], v[140:143], v[234:237], v[82:85]
	v_mfma_f32_16x16x32_bf16 v[74:77], v[160:163], v[234:237], v[74:77]
	v_mfma_f32_16x16x32_bf16 v[126:129], v[154:157], v[204:207], v[126:129]
	v_mfma_f32_16x16x32_bf16 v[122:125], v[164:167], v[204:207], v[122:125]
	v_mfma_f32_16x16x32_bf16 v[114:117], v[154:157], v[214:217], v[114:117]
	v_mfma_f32_16x16x32_bf16 v[106:109], v[164:167], v[214:217], v[106:109]
	v_mfma_f32_16x16x32_bf16 v[98:101], v[154:157], v[230:233], v[98:101]
	v_mfma_f32_16x16x32_bf16 v[90:93], v[164:167], v[230:233], v[90:93]
	v_mfma_f32_16x16x32_bf16 v[82:85], v[154:157], v[238:241], v[82:85]
	v_mfma_f32_16x16x32_bf16 v[74:77], v[164:167], v[238:241], v[74:77]
	s_setprio 0
	s_setprio 1
	v_mfma_f32_16x16x32_bf16 v[118:121], v[176:179], v[200:203], v[118:121]
	v_mfma_f32_16x16x32_bf16 v[110:113], v[184:187], v[200:203], v[110:113]
	v_mfma_f32_16x16x32_bf16 v[102:105], v[176:179], v[210:213], v[102:105]
	v_mfma_f32_16x16x32_bf16 v[94:97], v[184:187], v[210:213], v[94:97]
	v_mfma_f32_16x16x32_bf16 v[86:89], v[176:179], v[218:221], v[86:89]
	v_mfma_f32_16x16x32_bf16 v[78:81], v[184:187], v[218:221], v[78:81]
	v_mfma_f32_16x16x32_bf16 v[70:73], v[176:179], v[234:237], v[70:73]
	v_mfma_f32_16x16x32_bf16 v[66:69], v[184:187], v[234:237], v[66:69]
	v_mfma_f32_16x16x32_bf16 v[118:121], v[180:183], v[204:207], v[118:121]
	v_mfma_f32_16x16x32_bf16 v[110:113], v[196:199], v[204:207], v[110:113]
	v_mfma_f32_16x16x32_bf16 v[102:105], v[180:183], v[214:217], v[102:105]
	v_mfma_f32_16x16x32_bf16 v[94:97], v[196:199], v[214:217], v[94:97]
	v_mfma_f32_16x16x32_bf16 v[86:89], v[180:183], v[230:233], v[86:89]
	v_mfma_f32_16x16x32_bf16 v[78:81], v[196:199], v[230:233], v[78:81]
	v_mfma_f32_16x16x32_bf16 v[70:73], v[180:183], v[238:241], v[70:73]
	v_mfma_f32_16x16x32_bf16 v[66:69], v[196:199], v[238:241], v[66:69]
	s_setprio 0
	s_barrier
	s_add_i32 s65, s50, s42
	v_lshl_add_u64 v[144:145], s[38:39], 0, v[148:149]
	s_mov_b32 m0, s65
	ds_read_b128 v[200:203], v173 offset:16384
	ds_read_b128 v[204:207], v173 offset:17408
	ds_read_b128 v[210:213], v173 offset:18432
	ds_read_b128 v[214:217], v173 offset:19456
	ds_read_b128 v[218:221], v173 offset:20480
	ds_read_b128 v[230:233], v173 offset:21504
	ds_read_b128 v[234:237], v173 offset:22528
	ds_read_b128 v[238:241], v173 offset:23552
	global_load_lds_dwordx4 v[144:145], off
	s_add_i32 m0, s65, 0x2000
	s_add_u32 s66, s38, 0x10000
	v_lshl_add_u64 v[168:169], s[38:39], 0, v[152:153]
	s_addc_u32 s67, s39, 0
	s_add_i32 s65, s51, s42
	global_load_lds_dwordx4 v[168:169], off
	s_mov_b32 m0, s65
	v_lshl_add_u64 v[190:191], s[40:41], 0, v[150:151]
	global_load_lds_dwordx4 v148, s[66:67]
	s_add_i32 m0, s65, 0x2000
	s_nop 0
	global_load_lds_dwordx4 v152, s[66:67]
	v_lshl_add_u64 v[188:189], s[40:41], 0, v[146:147]
	s_mov_b32 m0, s35
	s_nop 0
	global_load_lds_dwordx4 v[188:189], off
	s_mov_b32 m0, s43
	s_nop 0
	global_load_lds_dwordx4 v[190:191], off
	s_waitcnt vmcnt(8)
	s_waitcnt lgkmcnt(0)
	s_barrier
	s_setprio 1
	s_waitcnt lgkmcnt(0)
	v_mfma_f32_16x16x32_bf16 v[62:65], v[140:143], v[200:203], v[62:65]
	v_mfma_f32_16x16x32_bf16 v[58:61], v[160:163], v[200:203], v[58:61]
	v_mfma_f32_16x16x32_bf16 v[50:53], v[140:143], v[210:213], v[50:53]
	v_mfma_f32_16x16x32_bf16 v[42:45], v[160:163], v[210:213], v[42:45]
	v_mfma_f32_16x16x32_bf16 v[34:37], v[140:143], v[218:221], v[34:37]
	v_mfma_f32_16x16x32_bf16 v[26:29], v[160:163], v[218:221], v[26:29]
	v_mfma_f32_16x16x32_bf16 v[18:21], v[140:143], v[234:237], v[18:21]
	v_mfma_f32_16x16x32_bf16 v[10:13], v[160:163], v[234:237], v[10:13]
	v_mfma_f32_16x16x32_bf16 v[62:65], v[154:157], v[204:207], v[62:65]
	v_mfma_f32_16x16x32_bf16 v[58:61], v[164:167], v[204:207], v[58:61]
	v_mfma_f32_16x16x32_bf16 v[50:53], v[154:157], v[214:217], v[50:53]
	v_mfma_f32_16x16x32_bf16 v[42:45], v[164:167], v[214:217], v[42:45]
	v_mfma_f32_16x16x32_bf16 v[34:37], v[154:157], v[230:233], v[34:37]
	v_mfma_f32_16x16x32_bf16 v[26:29], v[164:167], v[230:233], v[26:29]
	v_mfma_f32_16x16x32_bf16 v[18:21], v[154:157], v[238:241], v[18:21]
	v_mfma_f32_16x16x32_bf16 v[10:13], v[164:167], v[238:241], v[10:13]
	s_setprio 0
	s_setprio 1
	v_mfma_f32_16x16x32_bf16 v[54:57], v[176:179], v[200:203], v[54:57]
	v_mfma_f32_16x16x32_bf16 v[46:49], v[184:187], v[200:203], v[46:49]
	v_mfma_f32_16x16x32_bf16 v[38:41], v[176:179], v[210:213], v[38:41]
	v_mfma_f32_16x16x32_bf16 v[30:33], v[184:187], v[210:213], v[30:33]
	v_mfma_f32_16x16x32_bf16 v[22:25], v[176:179], v[218:221], v[22:25]
	v_mfma_f32_16x16x32_bf16 v[14:17], v[184:187], v[218:221], v[14:17]
	v_mfma_f32_16x16x32_bf16 v[6:9], v[176:179], v[234:237], v[6:9]
	v_mfma_f32_16x16x32_bf16 v[2:5], v[184:187], v[234:237], v[2:5]
	v_mfma_f32_16x16x32_bf16 v[54:57], v[180:183], v[204:207], v[54:57]
	v_mfma_f32_16x16x32_bf16 v[46:49], v[196:199], v[204:207], v[46:49]
	v_mfma_f32_16x16x32_bf16 v[38:41], v[180:183], v[214:217], v[38:41]
	v_mfma_f32_16x16x32_bf16 v[30:33], v[196:199], v[214:217], v[30:33]
	v_mfma_f32_16x16x32_bf16 v[22:25], v[180:183], v[230:233], v[22:25]
	v_mfma_f32_16x16x32_bf16 v[14:17], v[196:199], v[230:233], v[14:17]
	v_mfma_f32_16x16x32_bf16 v[6:9], v[180:183], v[238:241], v[6:9]
	v_mfma_f32_16x16x32_bf16 v[2:5], v[196:199], v[238:241], v[2:5]
	s_setprio 0
	s_barrier
	s_add_i32 s65, 0, 0x18000
	s_add_i32 s66, 0, 0x1c000
	v_add_u32_e32 v164, s65, v171
	v_add_u32_e32 v175, s66, v171
	ds_read_b128 v[140:143], v164
	ds_read_b128 v[154:157], v164 offset:1024
	ds_read_b128 v[160:163], v164 offset:2048
	ds_read_b128 v[164:167], v164 offset:3072
	ds_read_b128 v[176:179], v175
	ds_read_b128 v[180:183], v175 offset:1024
	ds_read_b128 v[184:187], v175 offset:2048
	ds_read_b128 v[196:199], v175 offset:3072
	s_add_u32 s40, s40, 0x40000
	s_addc_u32 s41, s41, 0
	s_mov_b32 m0, s44
	ds_read_b128 v[200:203], v173 offset:32768
	ds_read_b128 v[204:207], v173 offset:33792
	ds_read_b128 v[210:213], v173 offset:34816
	ds_read_b128 v[214:217], v173 offset:35840
	ds_read_b128 v[218:221], v173 offset:36864
	ds_read_b128 v[230:233], v173 offset:37888
	ds_read_b128 v[234:237], v173 offset:38912
	ds_read_b128 v[238:241], v173 offset:39936
	global_load_lds_dwordx4 v146, s[40:41]
	v_lshl_add_u64 v[208:209], s[40:41], 0, v[150:151]
	s_mov_b32 m0, s45
	s_nop 0
	global_load_lds_dwordx4 v[208:209], off
	s_waitcnt vmcnt(8)
	s_waitcnt lgkmcnt(0)
	s_barrier
	s_setprio 1
	s_waitcnt lgkmcnt(0)
	v_mfma_f32_16x16x32_bf16 v[126:129], v[140:143], v[200:203], v[126:129]
	v_mfma_f32_16x16x32_bf16 v[122:125], v[160:163], v[200:203], v[122:125]
	v_mfma_f32_16x16x32_bf16 v[114:117], v[140:143], v[210:213], v[114:117]
	v_mfma_f32_16x16x32_bf16 v[106:109], v[160:163], v[210:213], v[106:109]
	v_mfma_f32_16x16x32_bf16 v[98:101], v[140:143], v[218:221], v[98:101]
	v_mfma_f32_16x16x32_bf16 v[90:93], v[160:163], v[218:221], v[90:93]
	v_mfma_f32_16x16x32_bf16 v[82:85], v[140:143], v[234:237], v[82:85]
	v_mfma_f32_16x16x32_bf16 v[74:77], v[160:163], v[234:237], v[74:77]
	v_mfma_f32_16x16x32_bf16 v[126:129], v[154:157], v[204:207], v[126:129]
	v_mfma_f32_16x16x32_bf16 v[122:125], v[164:167], v[204:207], v[122:125]
	v_mfma_f32_16x16x32_bf16 v[114:117], v[154:157], v[214:217], v[114:117]
	v_mfma_f32_16x16x32_bf16 v[106:109], v[164:167], v[214:217], v[106:109]
	v_mfma_f32_16x16x32_bf16 v[98:101], v[154:157], v[230:233], v[98:101]
	v_mfma_f32_16x16x32_bf16 v[90:93], v[164:167], v[230:233], v[90:93]
	v_mfma_f32_16x16x32_bf16 v[82:85], v[154:157], v[238:241], v[82:85]
	v_mfma_f32_16x16x32_bf16 v[74:77], v[164:167], v[238:241], v[74:77]
	s_setprio 0
	s_setprio 1
	v_mfma_f32_16x16x32_bf16 v[118:121], v[176:179], v[200:203], v[118:121]
	v_mfma_f32_16x16x32_bf16 v[110:113], v[184:187], v[200:203], v[110:113]
	v_mfma_f32_16x16x32_bf16 v[102:105], v[176:179], v[210:213], v[102:105]
	v_mfma_f32_16x16x32_bf16 v[94:97], v[184:187], v[210:213], v[94:97]
	v_mfma_f32_16x16x32_bf16 v[86:89], v[176:179], v[218:221], v[86:89]
	v_mfma_f32_16x16x32_bf16 v[78:81], v[184:187], v[218:221], v[78:81]
	v_mfma_f32_16x16x32_bf16 v[70:73], v[176:179], v[234:237], v[70:73]
	v_mfma_f32_16x16x32_bf16 v[66:69], v[184:187], v[234:237], v[66:69]
	v_mfma_f32_16x16x32_bf16 v[118:121], v[180:183], v[204:207], v[118:121]
	v_mfma_f32_16x16x32_bf16 v[110:113], v[196:199], v[204:207], v[110:113]
	v_mfma_f32_16x16x32_bf16 v[102:105], v[180:183], v[214:217], v[102:105]
	v_mfma_f32_16x16x32_bf16 v[94:97], v[196:199], v[214:217], v[94:97]
	v_mfma_f32_16x16x32_bf16 v[86:89], v[180:183], v[230:233], v[86:89]
	v_mfma_f32_16x16x32_bf16 v[78:81], v[196:199], v[230:233], v[78:81]
	v_mfma_f32_16x16x32_bf16 v[70:73], v[180:183], v[238:241], v[70:73]
	v_mfma_f32_16x16x32_bf16 v[66:69], v[196:199], v[238:241], v[66:69]
	s_setprio 0
	s_barrier
	s_add_i32 s40, s65, s42
	v_lshl_add_u64 v[144:145], v[144:145], 0, s[8:9]
	s_mov_b32 m0, s40
	ds_read_b128 v[200:203], v173 offset:49152
	ds_read_b128 v[204:207], v173 offset:50176
	ds_read_b128 v[210:213], v173 offset:51200
	ds_read_b128 v[214:217], v173 offset:52224
	ds_read_b128 v[218:221], v173 offset:53248
	ds_read_b128 v[230:233], v173 offset:54272
	ds_read_b128 v[234:237], v173 offset:55296
	ds_read_b128 v[238:241], v173 offset:56320
	global_load_lds_dwordx4 v[144:145], off
	s_add_i32 m0, s40, 0x2000
	s_add_u32 s38, s38, 0x10080
	v_lshl_add_u64 v[144:145], v[168:169], 0, s[8:9]
	s_addc_u32 s39, s39, 0
	s_add_i32 s40, s66, s42
	global_load_lds_dwordx4 v[144:145], off
	s_mov_b32 m0, s40
	s_nop 0
	global_load_lds_dwordx4 v148, s[38:39]
	s_add_i32 m0, s40, 0x2000
	s_nop 0
	global_load_lds_dwordx4 v152, s[38:39]
	v_lshl_add_u64 v[144:145], v[188:189], 0, s[8:9]
	s_mov_b32 m0, s47
	s_nop 0
	global_load_lds_dwordx4 v[144:145], off
	v_lshl_add_u64 v[144:145], v[190:191], 0, s[8:9]
	s_mov_b32 m0, s48
	s_nop 0
	global_load_lds_dwordx4 v[144:145], off
	s_waitcnt vmcnt(8)
	s_waitcnt lgkmcnt(0)
	s_barrier
	s_setprio 1
	s_waitcnt lgkmcnt(0)
	v_mfma_f32_16x16x32_bf16 v[62:65], v[140:143], v[200:203], v[62:65]
	v_mfma_f32_16x16x32_bf16 v[58:61], v[160:163], v[200:203], v[58:61]
	v_mfma_f32_16x16x32_bf16 v[50:53], v[140:143], v[210:213], v[50:53]
	v_mfma_f32_16x16x32_bf16 v[42:45], v[160:163], v[210:213], v[42:45]
	v_mfma_f32_16x16x32_bf16 v[34:37], v[140:143], v[218:221], v[34:37]
	v_mfma_f32_16x16x32_bf16 v[26:29], v[160:163], v[218:221], v[26:29]
	v_mfma_f32_16x16x32_bf16 v[18:21], v[140:143], v[234:237], v[18:21]
	v_mfma_f32_16x16x32_bf16 v[10:13], v[160:163], v[234:237], v[10:13]
	v_mfma_f32_16x16x32_bf16 v[62:65], v[154:157], v[204:207], v[62:65]
	v_mfma_f32_16x16x32_bf16 v[58:61], v[164:167], v[204:207], v[58:61]
	v_mfma_f32_16x16x32_bf16 v[50:53], v[154:157], v[214:217], v[50:53]
	v_mfma_f32_16x16x32_bf16 v[42:45], v[164:167], v[214:217], v[42:45]
	v_mfma_f32_16x16x32_bf16 v[34:37], v[154:157], v[230:233], v[34:37]
	v_mfma_f32_16x16x32_bf16 v[26:29], v[164:167], v[230:233], v[26:29]
	v_mfma_f32_16x16x32_bf16 v[18:21], v[154:157], v[238:241], v[18:21]
	v_mfma_f32_16x16x32_bf16 v[10:13], v[164:167], v[238:241], v[10:13]
	s_setprio 0
	s_setprio 1
	v_mfma_f32_16x16x32_bf16 v[54:57], v[176:179], v[200:203], v[54:57]
	v_mfma_f32_16x16x32_bf16 v[46:49], v[184:187], v[200:203], v[46:49]
	v_mfma_f32_16x16x32_bf16 v[38:41], v[176:179], v[210:213], v[38:41]
	v_mfma_f32_16x16x32_bf16 v[30:33], v[184:187], v[210:213], v[30:33]
	v_mfma_f32_16x16x32_bf16 v[22:25], v[176:179], v[218:221], v[22:25]
	v_mfma_f32_16x16x32_bf16 v[14:17], v[184:187], v[218:221], v[14:17]
	v_mfma_f32_16x16x32_bf16 v[6:9], v[176:179], v[234:237], v[6:9]
	v_mfma_f32_16x16x32_bf16 v[2:5], v[184:187], v[234:237], v[2:5]
	v_mfma_f32_16x16x32_bf16 v[54:57], v[180:183], v[204:207], v[54:57]
	v_mfma_f32_16x16x32_bf16 v[46:49], v[196:199], v[204:207], v[46:49]
	v_mfma_f32_16x16x32_bf16 v[38:41], v[180:183], v[214:217], v[38:41]
	v_mfma_f32_16x16x32_bf16 v[30:33], v[196:199], v[214:217], v[30:33]
	v_mfma_f32_16x16x32_bf16 v[22:25], v[180:183], v[230:233], v[22:25]
	v_mfma_f32_16x16x32_bf16 v[14:17], v[196:199], v[230:233], v[14:17]
	v_mfma_f32_16x16x32_bf16 v[6:9], v[180:183], v[238:241], v[6:9]
	v_mfma_f32_16x16x32_bf16 v[2:5], v[196:199], v[238:241], v[2:5]
	s_setprio 0
	s_barrier
	s_add_i32 s64, s64, 2
	s_add_u32 s36, s36, 0x100
	s_addc_u32 s37, s37, 0
	s_add_u32 s62, s62, 0x100
	s_addc_u32 s63, s63, 0
	s_cmp_gt_u32 s64, 13
	s_cbranch_scc0 .LBB0_1599
	s_and_b64 vcc, exec, s[10:11]
	s_cbranch_vccz .LBB0_1602
	s_barrier

.LBB0_1873:
	s_lshl_b32 s8, s8, 5
	s_and_b32 s14, s8, 0x60
	s_mov_b64 s[8:9], 0x80
	s_add_i32 m0, s21, 0x18000
	v_lshl_add_u64 v[8:9], v[8:9], 0, s[8:9]
	s_lshl_b32 s11, s5, 13
	s_lshl_b32 s15, s14, 7
	s_waitcnt vmcnt(2)
	s_barrier
	global_load_lds_dwordx4 v[8:9], off
	v_lshl_add_u64 v[6:7], v[6:7], 0, s[8:9]
	s_add_i32 m0, s21, 0x1a000
	s_add_i32 s42, s21, 0x8000
	s_add_i32 s43, s21, 0xa000
	global_load_lds_dwordx4 v[6:7], off
	v_lshl_add_u64 v[2:3], v[2:3], 0, s[8:9]
	s_mov_b32 m0, s42
	s_add_u32 s12, s30, 0x40080
	global_load_lds_dwordx4 v[2:3], off
	v_lshl_add_u64 v[2:3], v[4:5], 0, s[8:9]
	s_mov_b32 m0, s43
	s_addc_u32 s13, s31, 0
	global_load_lds_dwordx4 v[2:3], off
	s_add_i32 m0, s21, 0x1c000
	global_load_lds_dwordx4 v132, s[12:13]
	v_lshl_add_u64 v[2:3], s[12:13], 0, v[136:137]
	s_add_i32 m0, s21, 0x1e000
	s_sext_i32_i8 s47, s4
	global_load_lds_dwordx4 v[2:3], off
	v_lshlrev_b32_e32 v2, 1, v13
	s_movk_i32 s4, 0x3c0
	v_lshl_or_b32 v3, v222, 6, v2
	v_and_b32_e32 v4, 32, v252
	v_and_or_b32 v2, v194, s4, v2
	v_bitop3_b32 v162, s15, v2, v4 bitop3:0xf6
	v_lshlrev_b32_e32 v2, 8, v0
	v_bitop3_b32 v3, v3, s11, v4 bitop3:0xde
	v_and_b32_e32 v2, 0x18000, v2
	v_lshlrev_b32_e32 v4, 11, v12
	v_or3_b32 v2, v10, v2, v4
	v_add_u32_e32 v138, v2, v11
	v_lshlrev_b32_e32 v2, 4, v14
	s_waitcnt vmcnt(6)
	s_cmpk_lt_u32 s10, 0x100
	v_and_b32_e32 v2, 0x38000, v2
	s_cselect_b64 s[10:11], -1, 0
	v_or3_b32 v2, v10, v2, v4
	s_add_i32 s45, 0, 0x10000
	s_add_i32 s46, 0, 0x14000
	v_lshl_or_b32 v1, s5, 6, v222
	s_ashr_i32 s44, s33, 31
	v_or_b32_e32 v163, s14, v13
	v_mov_b32_e32 v139, v133
	v_add_u32_e32 v140, v2, v11
	v_mov_b32_e32 v141, v133
	v_mov_b64_e32 v[142:143], 0x100
	v_mov_b64_e32 v[144:145], 0xff
	v_add_u32_e32 v164, s45, v162
	v_add_u32_e32 v165, s46, v162
	v_add_u32_e32 v166, 0, v3
	s_barrier
	s_branch .LBB0_1876

.LBB0_1883:
	ds_read_b128 v[146:149], v164
	ds_read_b128 v[150:153], v164 offset:1024
	ds_read_b128 v[154:157], v164 offset:2048
	ds_read_b128 v[158:161], v164 offset:3072
	ds_read_b128 v[168:171], v165
	ds_read_b128 v[172:175], v165 offset:1024
	ds_read_b128 v[176:179], v165 offset:2048
	ds_read_b128 v[180:183], v165 offset:3072
	s_add_u32 s30, s22, 0xfffc0080
	s_addc_u32 s31, s23, -1
	s_cmp_eq_u32 s52, 12
	s_cselect_b32 s35, s15, s31
	s_cselect_b32 s34, s48, s30
	s_cselect_b32 s31, s13, s51
	s_cselect_b32 s30, s49, s50
	s_add_i32 m0, s21, 0xc000
	ds_read_b128 v[184:187], v166
	ds_read_b128 v[188:191], v166 offset:1024
	ds_read_b128 v[196:199], v166 offset:2048
	ds_read_b128 v[200:203], v166 offset:3072
	ds_read_b128 v[204:207], v166 offset:4096
	ds_read_b128 v[208:211], v166 offset:5120
	ds_read_b128 v[212:215], v166 offset:6144
	ds_read_b128 v[216:219], v166 offset:7168
	global_load_lds_dwordx4 v138, s[22:23]
	s_add_i32 m0, s21, 0xe000
	s_nop 0
	global_load_lds_dwordx4 v140, s[22:23]
	s_waitcnt vmcnt(8)
	s_waitcnt lgkmcnt(0)
	s_barrier
	s_setprio 1
	s_waitcnt lgkmcnt(0)
	v_mfma_f32_16x16x32_bf16 v[126:129], v[146:149], v[184:187], v[126:129]
	v_mfma_f32_16x16x32_bf16 v[122:125], v[154:157], v[184:187], v[122:125]
	v_mfma_f32_16x16x32_bf16 v[114:117], v[146:149], v[196:199], v[114:117]
	v_mfma_f32_16x16x32_bf16 v[106:109], v[154:157], v[196:199], v[106:109]
	v_mfma_f32_16x16x32_bf16 v[98:101], v[146:149], v[204:207], v[98:101]
	v_mfma_f32_16x16x32_bf16 v[90:93], v[154:157], v[204:207], v[90:93]
	v_mfma_f32_16x16x32_bf16 v[82:85], v[146:149], v[212:215], v[82:85]
	v_mfma_f32_16x16x32_bf16 v[74:77], v[154:157], v[212:215], v[74:77]
	v_mfma_f32_16x16x32_bf16 v[126:129], v[150:153], v[188:191], v[126:129]
	v_mfma_f32_16x16x32_bf16 v[122:125], v[158:161], v[188:191], v[122:125]
	v_mfma_f32_16x16x32_bf16 v[114:117], v[150:153], v[200:203], v[114:117]
	v_mfma_f32_16x16x32_bf16 v[106:109], v[158:161], v[200:203], v[106:109]
	v_mfma_f32_16x16x32_bf16 v[98:101], v[150:153], v[208:211], v[98:101]
	v_mfma_f32_16x16x32_bf16 v[90:93], v[158:161], v[208:211], v[90:93]
	v_mfma_f32_16x16x32_bf16 v[82:85], v[150:153], v[216:219], v[82:85]
	v_mfma_f32_16x16x32_bf16 v[74:77], v[158:161], v[216:219], v[74:77]
	s_setprio 0
	s_setprio 1
	v_mfma_f32_16x16x32_bf16 v[118:121], v[168:171], v[184:187], v[118:121]
	v_mfma_f32_16x16x32_bf16 v[110:113], v[176:179], v[184:187], v[110:113]
	v_mfma_f32_16x16x32_bf16 v[102:105], v[168:171], v[196:199], v[102:105]
	v_mfma_f32_16x16x32_bf16 v[94:97], v[176:179], v[196:199], v[94:97]
	v_mfma_f32_16x16x32_bf16 v[86:89], v[168:171], v[204:207], v[86:89]
	v_mfma_f32_16x16x32_bf16 v[78:81], v[176:179], v[204:207], v[78:81]
	v_mfma_f32_16x16x32_bf16 v[70:73], v[168:171], v[212:215], v[70:73]
	v_mfma_f32_16x16x32_bf16 v[66:69], v[176:179], v[212:215], v[66:69]
	v_mfma_f32_16x16x32_bf16 v[118:121], v[172:175], v[188:191], v[118:121]
	v_mfma_f32_16x16x32_bf16 v[110:113], v[180:183], v[188:191], v[110:113]
	v_mfma_f32_16x16x32_bf16 v[102:105], v[172:175], v[200:203], v[102:105]
	v_mfma_f32_16x16x32_bf16 v[94:97], v[180:183], v[200:203], v[94:97]
	v_mfma_f32_16x16x32_bf16 v[86:89], v[172:175], v[208:211], v[86:89]
	v_mfma_f32_16x16x32_bf16 v[78:81], v[180:183], v[208:211], v[78:81]
	v_mfma_f32_16x16x32_bf16 v[70:73], v[172:175], v[216:219], v[70:73]
	v_mfma_f32_16x16x32_bf16 v[66:69], v[180:183], v[216:219], v[66:69]
	s_setprio 0
	s_barrier
	s_add_i32 s53, s45, s37
	v_lshl_add_u64 v[192:193], s[30:31], 0, v[132:133]
	s_mov_b32 m0, s53
	ds_read_b128 v[184:187], v166 offset:16384
	ds_read_b128 v[188:191], v166 offset:17408
	ds_read_b128 v[196:199], v166 offset:18432
	ds_read_b128 v[200:203], v166 offset:19456
	ds_read_b128 v[204:207], v166 offset:20480
	ds_read_b128 v[208:211], v166 offset:21504
	ds_read_b128 v[212:215], v166 offset:22528
	ds_read_b128 v[216:219], v166 offset:23552
	global_load_lds_dwordx4 v[192:193], off
	s_add_i32 m0, s53, 0x2000
	s_add_u32 s54, s30, 0x40000
	v_lshl_add_u64 v[220:221], s[30:31], 0, v[136:137]
	s_addc_u32 s55, s31, 0
	s_add_i32 s53, s46, s37
	global_load_lds_dwordx4 v[220:221], off
	s_mov_b32 m0, s53
	v_lshl_add_u64 v[232:233], s[34:35], 0, v[134:135]
	global_load_lds_dwordx4 v132, s[54:55]
	s_add_i32 m0, s53, 0x2000
	s_nop 0
	global_load_lds_dwordx4 v136, s[54:55]
	v_lshl_add_u64 v[230:231], s[34:35], 0, v[130:131]
	s_mov_b32 m0, s21
	s_nop 0
	global_load_lds_dwordx4 v[230:231], off
	s_mov_b32 m0, s38
	s_nop 0
	global_load_lds_dwordx4 v[232:233], off
	s_waitcnt vmcnt(8)
	s_waitcnt lgkmcnt(0)
	s_barrier
	s_setprio 1
	s_waitcnt lgkmcnt(0)
	v_mfma_f32_16x16x32_bf16 v[62:65], v[146:149], v[184:187], v[62:65]
	v_mfma_f32_16x16x32_bf16 v[58:61], v[154:157], v[184:187], v[58:61]
	v_mfma_f32_16x16x32_bf16 v[50:53], v[146:149], v[196:199], v[50:53]
	v_mfma_f32_16x16x32_bf16 v[42:45], v[154:157], v[196:199], v[42:45]
	v_mfma_f32_16x16x32_bf16 v[34:37], v[146:149], v[204:207], v[34:37]
	v_mfma_f32_16x16x32_bf16 v[26:29], v[154:157], v[204:207], v[26:29]
	v_mfma_f32_16x16x32_bf16 v[18:21], v[146:149], v[212:215], v[18:21]
	v_mfma_f32_16x16x32_bf16 v[10:13], v[154:157], v[212:215], v[10:13]
	v_mfma_f32_16x16x32_bf16 v[62:65], v[150:153], v[188:191], v[62:65]
	v_mfma_f32_16x16x32_bf16 v[58:61], v[158:161], v[188:191], v[58:61]
	v_mfma_f32_16x16x32_bf16 v[50:53], v[150:153], v[200:203], v[50:53]
	v_mfma_f32_16x16x32_bf16 v[42:45], v[158:161], v[200:203], v[42:45]
	v_mfma_f32_16x16x32_bf16 v[34:37], v[150:153], v[208:211], v[34:37]
	v_mfma_f32_16x16x32_bf16 v[26:29], v[158:161], v[208:211], v[26:29]
	v_mfma_f32_16x16x32_bf16 v[18:21], v[150:153], v[216:219], v[18:21]
	v_mfma_f32_16x16x32_bf16 v[10:13], v[158:161], v[216:219], v[10:13]
	s_setprio 0
	s_setprio 1
	v_mfma_f32_16x16x32_bf16 v[54:57], v[168:171], v[184:187], v[54:57]
	v_mfma_f32_16x16x32_bf16 v[46:49], v[176:179], v[184:187], v[46:49]
	v_mfma_f32_16x16x32_bf16 v[38:41], v[168:171], v[196:199], v[38:41]
	v_mfma_f32_16x16x32_bf16 v[30:33], v[176:179], v[196:199], v[30:33]
	v_mfma_f32_16x16x32_bf16 v[22:25], v[168:171], v[204:207], v[22:25]
	v_mfma_f32_16x16x32_bf16 v[14:17], v[176:179], v[204:207], v[14:17]
	v_mfma_f32_16x16x32_bf16 v[6:9], v[168:171], v[212:215], v[6:9]
	v_mfma_f32_16x16x32_bf16 v[2:5], v[176:179], v[212:215], v[2:5]
	v_mfma_f32_16x16x32_bf16 v[54:57], v[172:175], v[188:191], v[54:57]
	v_mfma_f32_16x16x32_bf16 v[46:49], v[180:183], v[188:191], v[46:49]
	v_mfma_f32_16x16x32_bf16 v[38:41], v[172:175], v[200:203], v[38:41]
	v_mfma_f32_16x16x32_bf16 v[30:33], v[180:183], v[200:203], v[30:33]
	v_mfma_f32_16x16x32_bf16 v[22:25], v[172:175], v[208:211], v[22:25]
	v_mfma_f32_16x16x32_bf16 v[14:17], v[180:183], v[208:211], v[14:17]
	v_mfma_f32_16x16x32_bf16 v[6:9], v[172:175], v[216:219], v[6:9]
	v_mfma_f32_16x16x32_bf16 v[2:5], v[180:183], v[216:219], v[2:5]
	s_setprio 0
	s_barrier
	s_add_i32 s53, 0, 0x18000
	s_add_i32 s54, 0, 0x1c000
	v_add_u32_e32 v158, s53, v162
	v_add_u32_e32 v167, s54, v162
	ds_read_b128 v[146:149], v158
	ds_read_b128 v[150:153], v158 offset:1024
	ds_read_b128 v[154:157], v158 offset:2048
	ds_read_b128 v[158:161], v158 offset:3072
	ds_read_b128 v[168:171], v167
	ds_read_b128 v[172:175], v167 offset:1024
	ds_read_b128 v[176:179], v167 offset:2048
	ds_read_b128 v[180:183], v167 offset:3072
	s_add_u32 s34, s34, 0x40000
	s_addc_u32 s35, s35, 0
	s_mov_b32 m0, s39
	ds_read_b128 v[184:187], v166 offset:32768
	ds_read_b128 v[188:191], v166 offset:33792
	ds_read_b128 v[196:199], v166 offset:34816
	ds_read_b128 v[200:203], v166 offset:35840
	ds_read_b128 v[204:207], v166 offset:36864
	ds_read_b128 v[208:211], v166 offset:37888
	ds_read_b128 v[212:215], v166 offset:38912
	ds_read_b128 v[216:219], v166 offset:39936
	global_load_lds_dwordx4 v130, s[34:35]
	v_lshl_add_u64 v[234:235], s[34:35], 0, v[134:135]
	s_mov_b32 m0, s40
	s_nop 0
	global_load_lds_dwordx4 v[234:235], off
	s_waitcnt vmcnt(8)
	s_waitcnt lgkmcnt(0)
	s_barrier
	s_setprio 1
	s_waitcnt lgkmcnt(0)
	v_mfma_f32_16x16x32_bf16 v[126:129], v[146:149], v[184:187], v[126:129]
	v_mfma_f32_16x16x32_bf16 v[122:125], v[154:157], v[184:187], v[122:125]
	v_mfma_f32_16x16x32_bf16 v[114:117], v[146:149], v[196:199], v[114:117]
	v_mfma_f32_16x16x32_bf16 v[106:109], v[154:157], v[196:199], v[106:109]
	v_mfma_f32_16x16x32_bf16 v[98:101], v[146:149], v[204:207], v[98:101]
	v_mfma_f32_16x16x32_bf16 v[90:93], v[154:157], v[204:207], v[90:93]
	v_mfma_f32_16x16x32_bf16 v[82:85], v[146:149], v[212:215], v[82:85]
	v_mfma_f32_16x16x32_bf16 v[74:77], v[154:157], v[212:215], v[74:77]
	v_mfma_f32_16x16x32_bf16 v[126:129], v[150:153], v[188:191], v[126:129]
	v_mfma_f32_16x16x32_bf16 v[122:125], v[158:161], v[188:191], v[122:125]
	v_mfma_f32_16x16x32_bf16 v[114:117], v[150:153], v[200:203], v[114:117]
	v_mfma_f32_16x16x32_bf16 v[106:109], v[158:161], v[200:203], v[106:109]
	v_mfma_f32_16x16x32_bf16 v[98:101], v[150:153], v[208:211], v[98:101]
	v_mfma_f32_16x16x32_bf16 v[90:93], v[158:161], v[208:211], v[90:93]
	v_mfma_f32_16x16x32_bf16 v[82:85], v[150:153], v[216:219], v[82:85]
	v_mfma_f32_16x16x32_bf16 v[74:77], v[158:161], v[216:219], v[74:77]
	s_setprio 0
	s_setprio 1
	v_mfma_f32_16x16x32_bf16 v[118:121], v[168:171], v[184:187], v[118:121]
	v_mfma_f32_16x16x32_bf16 v[110:113], v[176:179], v[184:187], v[110:113]
	v_mfma_f32_16x16x32_bf16 v[102:105], v[168:171], v[196:199], v[102:105]
	v_mfma_f32_16x16x32_bf16 v[94:97], v[176:179], v[196:199], v[94:97]
	v_mfma_f32_16x16x32_bf16 v[86:89], v[168:171], v[204:207], v[86:89]
	v_mfma_f32_16x16x32_bf16 v[78:81], v[176:179], v[204:207], v[78:81]
	v_mfma_f32_16x16x32_bf16 v[70:73], v[168:171], v[212:215], v[70:73]
	v_mfma_f32_16x16x32_bf16 v[66:69], v[176:179], v[212:215], v[66:69]
	v_mfma_f32_16x16x32_bf16 v[118:121], v[172:175], v[188:191], v[118:121]
	v_mfma_f32_16x16x32_bf16 v[110:113], v[180:183], v[188:191], v[110:113]
	v_mfma_f32_16x16x32_bf16 v[102:105], v[172:175], v[200:203], v[102:105]
	v_mfma_f32_16x16x32_bf16 v[94:97], v[180:183], v[200:203], v[94:97]
	v_mfma_f32_16x16x32_bf16 v[86:89], v[172:175], v[208:211], v[86:89]
	v_mfma_f32_16x16x32_bf16 v[78:81], v[180:183], v[208:211], v[78:81]
	v_mfma_f32_16x16x32_bf16 v[70:73], v[172:175], v[216:219], v[70:73]
	v_mfma_f32_16x16x32_bf16 v[66:69], v[180:183], v[216:219], v[66:69]
	s_setprio 0
	s_barrier
	s_add_i32 s34, s53, s37
	v_lshl_add_u64 v[192:193], v[192:193], 0, s[8:9]
	s_mov_b32 m0, s34
	ds_read_b128 v[184:187], v166 offset:49152
	ds_read_b128 v[188:191], v166 offset:50176
	ds_read_b128 v[196:199], v166 offset:51200
	ds_read_b128 v[200:203], v166 offset:52224
	ds_read_b128 v[204:207], v166 offset:53248
	ds_read_b128 v[208:211], v166 offset:54272
	ds_read_b128 v[212:215], v166 offset:55296
	ds_read_b128 v[216:219], v166 offset:56320
	global_load_lds_dwordx4 v[192:193], off
	s_add_i32 m0, s34, 0x2000
	s_add_u32 s30, s30, 0x40080
	v_lshl_add_u64 v[192:193], v[220:221], 0, s[8:9]
	s_addc_u32 s31, s31, 0
	s_add_i32 s34, s54, s37
	global_load_lds_dwordx4 v[192:193], off
	s_mov_b32 m0, s34
	s_nop 0
	global_load_lds_dwordx4 v132, s[30:31]
	s_add_i32 m0, s34, 0x2000
	s_nop 0
	global_load_lds_dwordx4 v136, s[30:31]
	v_lshl_add_u64 v[192:193], v[230:231], 0, s[8:9]
	s_mov_b32 m0, s42
	s_nop 0
	global_load_lds_dwordx4 v[192:193], off
	v_lshl_add_u64 v[192:193], v[232:233], 0, s[8:9]
	s_mov_b32 m0, s43
	s_nop 0
	global_load_lds_dwordx4 v[192:193], off
	s_waitcnt vmcnt(8)
	s_waitcnt lgkmcnt(0)
	s_barrier
	s_setprio 1
	s_waitcnt lgkmcnt(0)
	v_mfma_f32_16x16x32_bf16 v[62:65], v[146:149], v[184:187], v[62:65]
	v_mfma_f32_16x16x32_bf16 v[58:61], v[154:157], v[184:187], v[58:61]
	v_mfma_f32_16x16x32_bf16 v[50:53], v[146:149], v[196:199], v[50:53]
	v_mfma_f32_16x16x32_bf16 v[42:45], v[154:157], v[196:199], v[42:45]
	v_mfma_f32_16x16x32_bf16 v[34:37], v[146:149], v[204:207], v[34:37]
	v_mfma_f32_16x16x32_bf16 v[26:29], v[154:157], v[204:207], v[26:29]
	v_mfma_f32_16x16x32_bf16 v[18:21], v[146:149], v[212:215], v[18:21]
	v_mfma_f32_16x16x32_bf16 v[10:13], v[154:157], v[212:215], v[10:13]
	v_mfma_f32_16x16x32_bf16 v[62:65], v[150:153], v[188:191], v[62:65]
	v_mfma_f32_16x16x32_bf16 v[58:61], v[158:161], v[188:191], v[58:61]
	v_mfma_f32_16x16x32_bf16 v[50:53], v[150:153], v[200:203], v[50:53]
	v_mfma_f32_16x16x32_bf16 v[42:45], v[158:161], v[200:203], v[42:45]
	v_mfma_f32_16x16x32_bf16 v[34:37], v[150:153], v[208:211], v[34:37]
	v_mfma_f32_16x16x32_bf16 v[26:29], v[158:161], v[208:211], v[26:29]
	v_mfma_f32_16x16x32_bf16 v[18:21], v[150:153], v[216:219], v[18:21]
	v_mfma_f32_16x16x32_bf16 v[10:13], v[158:161], v[216:219], v[10:13]
	s_setprio 0
	s_setprio 1
	v_mfma_f32_16x16x32_bf16 v[54:57], v[168:171], v[184:187], v[54:57]
	v_mfma_f32_16x16x32_bf16 v[46:49], v[176:179], v[184:187], v[46:49]
	v_mfma_f32_16x16x32_bf16 v[38:41], v[168:171], v[196:199], v[38:41]
	v_mfma_f32_16x16x32_bf16 v[30:33], v[176:179], v[196:199], v[30:33]
	v_mfma_f32_16x16x32_bf16 v[22:25], v[168:171], v[204:207], v[22:25]
	v_mfma_f32_16x16x32_bf16 v[14:17], v[176:179], v[204:207], v[14:17]
	v_mfma_f32_16x16x32_bf16 v[6:9], v[168:171], v[212:215], v[6:9]
	v_mfma_f32_16x16x32_bf16 v[2:5], v[176:179], v[212:215], v[2:5]
	v_mfma_f32_16x16x32_bf16 v[54:57], v[172:175], v[188:191], v[54:57]
	v_mfma_f32_16x16x32_bf16 v[46:49], v[180:183], v[188:191], v[46:49]
	v_mfma_f32_16x16x32_bf16 v[38:41], v[172:175], v[200:203], v[38:41]
	v_mfma_f32_16x16x32_bf16 v[30:33], v[180:183], v[200:203], v[30:33]
	v_mfma_f32_16x16x32_bf16 v[22:25], v[172:175], v[208:211], v[22:25]
	v_mfma_f32_16x16x32_bf16 v[14:17], v[180:183], v[208:211], v[14:17]
	v_mfma_f32_16x16x32_bf16 v[6:9], v[172:175], v[216:219], v[6:9]
	v_mfma_f32_16x16x32_bf16 v[2:5], v[180:183], v[216:219], v[2:5]
	s_setprio 0
	s_barrier
	s_add_i32 s52, s52, 2
	s_add_u32 s22, s22, 0x100
	s_addc_u32 s23, s23, 0
	s_add_u32 s50, s50, 0x100
	s_addc_u32 s51, s51, 0
	s_cmp_gt_u32 s52, 13
	s_cbranch_scc0 .LBB0_1883
	s_and_b64 vcc, exec, s[10:11]
	s_cbranch_vccz .LBB0_1886
	s_barrier

.LBB0_2059:
	s_mov_b64 s[6:7], 0x80
	s_add_i32 m0, s35, 0x18000
	v_lshl_add_u64 v[2:3], v[2:3], 0, s[6:7]
	s_waitcnt vmcnt(2)
	s_barrier
	global_load_lds_dwordx4 v[2:3], off
	v_lshl_add_u64 v[2:3], v[4:5], 0, s[6:7]
	s_add_i32 m0, s35, 0x1a000
	v_readlane_b32 s64, v253, 46
	global_load_lds_dwordx4 v[2:3], off
	v_readlane_b32 s76, v253, 58
	v_readlane_b32 s77, v253, 59
	s_lshl_b32 s1, s1, 5
	v_readlane_b32 s78, v253, 60
	v_readlane_b32 s79, v253, 61
	s_mov_b64 s[12:13], s[76:77]
	ds_read_b64 v[2:3], v149
	s_and_b32 s53, s95, 3
	s_lshl_b32 s3, s0, 13
	s_and_b32 s1, s1, 0x60
	s_mov_b64 s[14:15], s[78:79]
	s_add_u32 s8, s14, 0x3b00080
	s_addc_u32 s9, s15, 0
	s_add_i32 s39, s35, 0x8000
	s_add_i32 s40, s35, 0xa000
	s_mov_b32 m0, s39
	s_add_u32 s10, s16, 0x40080
	s_waitcnt lgkmcnt(0)
	global_load_lds_dwordx4 v2, s[8:9]
	s_mov_b32 m0, s40
	s_addc_u32 s11, s17, 0
	global_load_lds_dwordx4 v3, s[8:9]
	s_add_i32 m0, s35, 0x1c000
	global_load_lds_dwordx4 v134, s[10:11]
	v_lshl_add_u64 v[2:3], s[10:11], 0, v[132:133]
	s_add_i32 m0, s35, 0x1e000
	s_cmpk_lt_u32 s2, 0x100
	global_load_lds_dwordx4 v[2:3], off
	v_lshlrev_b32_e32 v3, 2, v222
	v_lshl_or_b32 v2, v222, 6, v139
	v_and_b32_e32 v3, 32, v3
	s_waitcnt vmcnt(6)
	v_lshl_or_b32 v150, s0, 6, v222
	v_bitop3_b32 v2, v2, s3, v3 bitop3:0xde
	v_lshl_or_b32 v151, s1, 7, v140
	s_cselect_b64 s[10:11], -1, 0
	s_add_i32 s2, 0, 0x224f0
	s_add_i32 s41, 0, 0x10000
	s_add_i32 s42, 0, 0x14000
	v_or_b32_e32 v153, s1, v138
	v_add_u32_e32 v154, 0x80, v150
	v_add_u32_e32 v155, 0x90, v150
	v_add_u32_e32 v156, 0xa0, v150
	v_add_u32_e32 v157, 0xb0, v150
	v_or_b32_e32 v158, 48, v150
	v_or_b32_e32 v159, 32, v150
	v_or_b32_e32 v160, 16, v150
	v_cmp_eq_u32_e64 s[0:1], 0, v82
	v_mov_b32_e32 v161, s2
	v_add_u32_e32 v162, s41, v151
	v_add_u32_e32 v163, s42, v151
	v_add_u32_e32 v164, 0, v2
	s_mov_b32 s43, 0
	v_readlane_b32 s65, v253, 47
	v_readlane_b32 s66, v253, 48
	v_readlane_b32 s67, v253, 49
	v_readlane_b32 s68, v253, 50
	v_readlane_b32 s69, v253, 51
	v_readlane_b32 s70, v253, 52
	v_readlane_b32 s71, v253, 53
	v_readlane_b32 s72, v253, 54
	v_readlane_b32 s73, v253, 55
	v_readlane_b32 s74, v253, 56
	v_readlane_b32 s75, v253, 57
	s_barrier
	s_branch .LBB0_2062

.LBB0_2070:
	ds_read_b128 v[14:17], v162
	ds_read_b128 v[22:25], v162 offset:1024
	ds_read_b128 v[26:29], v162 offset:2048
	ds_read_b128 v[30:33], v162 offset:3072
	ds_read_b128 v[46:49], v163
	ds_read_b128 v[50:53], v163 offset:1024
	ds_read_b128 v[58:61], v163 offset:2048
	ds_read_b128 v[62:65], v163 offset:3072
	s_add_u32 s18, s16, 0x80
	s_addc_u32 s19, s17, 0
	s_cmp_eq_u32 s62, 12
	s_cselect_b32 s19, s83, s19
	s_cselect_b32 s18, s82, s18
	s_cselect_b32 s21, s13, s59
	s_cselect_b32 s20, s12, s58
	s_cselect_b32 s63, s55, s54
	ds_read_b128 v[74:77], v164 offset:1024
	ds_read_b128 v[78:81], v164 offset:2048
	ds_read_b128 v[86:89], v164 offset:3072
	ds_read_b128 v[90:93], v164 offset:4096
	ds_read_b128 v[106:109], v164
	ds_read2_b32 v[166:167], v165 offset0:2 offset1:3
	ds_read_b128 v[110:113], v164 offset:5120
	ds_read_b128 v[114:117], v164 offset:6144
	ds_read_b128 v[118:121], v164 offset:7168
	s_add_i32 m0, s35, 0xc000
	s_waitcnt lgkmcnt(0)
	global_load_lds_dwordx4 v166, s[16:17]
	s_add_i32 m0, s35, 0xe000
	s_nop 0
	global_load_lds_dwordx4 v167, s[16:17]
	s_waitcnt vmcnt(8)
	s_waitcnt lgkmcnt(0)
	s_barrier
	s_setprio 1
	v_mfma_f32_16x16x32_bf16 v[126:129], v[14:17], v[106:109], v[126:129]
	v_mfma_f32_16x16x32_bf16 v[122:125], v[26:29], v[106:109], v[122:125]
	v_mfma_f32_16x16x32_bf16 v[94:97], v[14:17], v[78:81], v[94:97]
	v_mfma_f32_16x16x32_bf16 v[82:85], v[26:29], v[78:81], v[82:85]
	v_mfma_f32_16x16x32_bf16 v[54:57], v[14:17], v[90:93], v[54:57]
	v_mfma_f32_16x16x32_bf16 v[42:45], v[26:29], v[90:93], v[42:45]
	v_mfma_f32_16x16x32_bf16 v[10:13], v[26:29], v[114:117], v[10:13]
	v_mfma_f32_16x16x32_bf16 v[126:129], v[22:25], v[74:77], v[126:129]
	v_mfma_f32_16x16x32_bf16 v[122:125], v[30:33], v[74:77], v[122:125]
	v_mfma_f32_16x16x32_bf16 v[94:97], v[22:25], v[86:89], v[94:97]
	v_mfma_f32_16x16x32_bf16 v[82:85], v[30:33], v[86:89], v[82:85]
	v_mfma_f32_16x16x32_bf16 v[54:57], v[22:25], v[110:113], v[54:57]
	v_mfma_f32_16x16x32_bf16 v[42:45], v[30:33], v[110:113], v[42:45]
	v_mfma_f32_16x16x32_bf16 v[14:17], v[14:17], v[114:117], v[18:21]
	v_mfma_f32_16x16x32_bf16 v[10:13], v[30:33], v[118:121], v[10:13]
	v_mfma_f32_16x16x32_bf16 v[14:17], v[22:25], v[118:121], v[14:17]
	s_setprio 0
	s_setprio 1
	v_mfma_f32_16x16x32_bf16 v[18:21], v[46:49], v[106:109], v[102:105]
	v_mfma_f32_16x16x32_bf16 v[22:25], v[50:53], v[74:77], v[18:21]
	v_mfma_f32_16x16x32_bf16 v[18:21], v[58:61], v[106:109], v[98:101]
	v_mfma_f32_16x16x32_bf16 v[26:29], v[62:65], v[74:77], v[18:21]
	v_mfma_f32_16x16x32_bf16 v[18:21], v[46:49], v[78:81], v[70:73]
	v_mfma_f32_16x16x32_bf16 v[30:33], v[50:53], v[86:89], v[18:21]
	v_mfma_f32_16x16x32_bf16 v[18:21], v[58:61], v[78:81], v[66:69]
	v_mfma_f32_16x16x32_bf16 v[66:69], v[62:65], v[86:89], v[18:21]
	v_mfma_f32_16x16x32_bf16 v[18:21], v[46:49], v[90:93], v[38:41]
	v_mfma_f32_16x16x32_bf16 v[38:41], v[50:53], v[110:113], v[18:21]
	v_mfma_f32_16x16x32_bf16 v[18:21], v[58:61], v[90:93], v[34:37]
	v_mfma_f32_16x16x32_bf16 v[6:9], v[46:49], v[114:117], v[6:9]
	v_mfma_f32_16x16x32_bf16 v[2:5], v[58:61], v[114:117], v[2:5]
	v_mfma_f32_16x16x32_bf16 v[34:37], v[62:65], v[110:113], v[18:21]
	v_mfma_f32_16x16x32_bf16 v[6:9], v[50:53], v[118:121], v[6:9]
	v_mfma_f32_16x16x32_bf16 v[2:5], v[62:65], v[118:121], v[2:5]
	s_setprio 0
	s_barrier
	s_add_i32 s64, s41, s34
	v_lshl_add_u64 v[174:175], s[20:21], 0, v[134:135]
	s_mov_b32 m0, s64
	v_lshl_add_u64 v[176:177], s[20:21], 0, v[132:133]
	global_load_lds_dwordx4 v[174:175], off
	s_add_i32 m0, s64, 0x2000
	s_add_u32 s64, s20, 0x40000
	s_addc_u32 s65, s21, 0
	s_add_i32 s66, s42, s34
	global_load_lds_dwordx4 v[176:177], off
	s_mov_b32 m0, s66
	v_lshl_add_u32 v136, s63, 2, v149
	global_load_lds_dwordx4 v134, s[64:65]
	s_add_i32 m0, s66, 0x2000
	s_nop 0
	global_load_lds_dwordx4 v132, s[64:65]
	ds_read2_b32 v[18:19], v136 offset1:1
	s_mov_b32 m0, s35
	s_waitcnt lgkmcnt(0)
	global_load_lds_dwordx4 v18, s[18:19]
	s_mov_b32 m0, s36
	s_nop 0
	global_load_lds_dwordx4 v19, s[18:19]
	s_waitcnt vmcnt(8)
	s_waitcnt lgkmcnt(0)
	s_barrier
	s_barrier
	s_add_i32 s63, 0, 0x18000
	s_add_i32 s64, 0, 0x1c000
	v_add_u32_e32 v58, s63, v151
	v_add_u32_e32 v70, s64, v151
	ds_read_b128 v[18:21], v58
	ds_read_b128 v[46:49], v58 offset:1024
	ds_read_b128 v[50:53], v58 offset:2048
	ds_read_b128 v[58:61], v58 offset:3072
	ds_read_b128 v[62:65], v70
	ds_read_b128 v[74:77], v70 offset:1024
	ds_read_b128 v[78:81], v70 offset:2048
	ds_read_b128 v[86:89], v70 offset:3072
	ds_read_b128 v[70:73], v164 offset:32768
	ds_read_b128 v[90:93], v164 offset:33792
	ds_read_b128 v[106:109], v164 offset:34816
	ds_read_b128 v[110:113], v164 offset:35840
	ds_read_b128 v[114:117], v164 offset:36864
	ds_read_b128 v[118:121], v164 offset:37888
	ds_read2_b32 v[98:99], v136 offset0:2 offset1:3
	ds_read_b128 v[166:169], v164 offset:38912
	ds_read_b128 v[170:173], v164 offset:39936
	s_mov_b32 m0, s37
	s_waitcnt lgkmcnt(0)
	global_load_lds_dwordx4 v98, s[18:19]
	s_mov_b32 m0, s38
	s_nop 0
	global_load_lds_dwordx4 v99, s[18:19]
	s_waitcnt vmcnt(8)
	s_waitcnt lgkmcnt(0)
	s_barrier
	s_setprio 1
	v_mfma_f32_16x16x32_bf16 v[98:101], v[18:21], v[70:73], v[126:129]
	v_mfma_f32_16x16x32_bf16 v[126:129], v[46:49], v[90:93], v[98:101]
	v_mfma_f32_16x16x32_bf16 v[98:101], v[50:53], v[70:73], v[122:125]
	v_mfma_f32_16x16x32_bf16 v[94:97], v[18:21], v[106:109], v[94:97]
	v_mfma_f32_16x16x32_bf16 v[82:85], v[50:53], v[106:109], v[82:85]
	v_mfma_f32_16x16x32_bf16 v[54:57], v[18:21], v[114:117], v[54:57]
	v_mfma_f32_16x16x32_bf16 v[42:45], v[50:53], v[114:117], v[42:45]
	v_mfma_f32_16x16x32_bf16 v[14:17], v[18:21], v[166:169], v[14:17]
	v_mfma_f32_16x16x32_bf16 v[10:13], v[50:53], v[166:169], v[10:13]
	v_mfma_f32_16x16x32_bf16 v[122:125], v[58:61], v[90:93], v[98:101]
	v_mfma_f32_16x16x32_bf16 v[94:97], v[46:49], v[110:113], v[94:97]
	v_mfma_f32_16x16x32_bf16 v[82:85], v[58:61], v[110:113], v[82:85]
	v_mfma_f32_16x16x32_bf16 v[54:57], v[46:49], v[118:121], v[54:57]
	v_mfma_f32_16x16x32_bf16 v[42:45], v[58:61], v[118:121], v[42:45]
	v_mfma_f32_16x16x32_bf16 v[18:21], v[46:49], v[170:173], v[14:17]
	v_mfma_f32_16x16x32_bf16 v[10:13], v[58:61], v[170:173], v[10:13]
	s_setprio 0
	s_setprio 1
	v_mfma_f32_16x16x32_bf16 v[14:17], v[62:65], v[70:73], v[22:25]
	v_mfma_f32_16x16x32_bf16 v[102:105], v[74:77], v[90:93], v[14:17]
	v_mfma_f32_16x16x32_bf16 v[14:17], v[78:81], v[70:73], v[26:29]
	v_mfma_f32_16x16x32_bf16 v[98:101], v[86:89], v[90:93], v[14:17]
	v_mfma_f32_16x16x32_bf16 v[14:17], v[62:65], v[106:109], v[30:33]
	v_mfma_f32_16x16x32_bf16 v[70:73], v[74:77], v[110:113], v[14:17]
	v_mfma_f32_16x16x32_bf16 v[14:17], v[78:81], v[106:109], v[66:69]
	v_mfma_f32_16x16x32_bf16 v[66:69], v[86:89], v[110:113], v[14:17]
	v_mfma_f32_16x16x32_bf16 v[14:17], v[62:65], v[114:117], v[38:41]
	v_mfma_f32_16x16x32_bf16 v[38:41], v[74:77], v[118:121], v[14:17]
	v_mfma_f32_16x16x32_bf16 v[14:17], v[78:81], v[114:117], v[34:37]
	v_mfma_f32_16x16x32_bf16 v[6:9], v[62:65], v[166:169], v[6:9]
	v_mfma_f32_16x16x32_bf16 v[2:5], v[78:81], v[166:169], v[2:5]
	v_mfma_f32_16x16x32_bf16 v[34:37], v[86:89], v[118:121], v[14:17]
	v_mfma_f32_16x16x32_bf16 v[6:9], v[74:77], v[170:173], v[6:9]
	v_mfma_f32_16x16x32_bf16 v[2:5], v[86:89], v[170:173], v[2:5]
	s_setprio 0
	s_barrier
	s_add_i32 s63, s63, s34
	v_lshl_add_u64 v[14:15], v[174:175], 0, s[6:7]
	s_mov_b32 m0, s63
	s_nop 0
	global_load_lds_dwordx4 v[14:15], off
	s_add_i32 m0, s63, 0x2000
	s_add_u32 s20, s20, 0x40080
	v_lshl_add_u64 v[14:15], v[176:177], 0, s[6:7]
	s_addc_u32 s21, s21, 0
	s_add_i32 s63, s64, s34
	global_load_lds_dwordx4 v[14:15], off
	s_mov_b32 m0, s63
	s_nop 0
	global_load_lds_dwordx4 v134, s[20:21]
	s_add_i32 m0, s63, 0x2000
	s_nop 0
	global_load_lds_dwordx4 v132, s[20:21]
	ds_read2_b32 v[14:15], v136 offset1:1
	s_mov_b32 m0, s39
	s_waitcnt lgkmcnt(0)
	v_mov_b32_e32 v136, v14
	v_lshl_add_u64 v[16:17], s[18:19], 0, v[136:137]
	v_mov_b32_e32 v136, v15
	v_lshl_add_u64 v[16:17], v[16:17], 0, s[6:7]
	v_lshl_add_u64 v[14:15], s[18:19], 0, v[136:137]
	global_load_lds_dwordx4 v[16:17], off
	v_lshl_add_u64 v[14:15], v[14:15], 0, s[6:7]
	s_mov_b32 m0, s40
	s_nop 0
	global_load_lds_dwordx4 v[14:15], off
	s_waitcnt vmcnt(8)
	s_waitcnt lgkmcnt(0)
	s_barrier
	s_barrier
	s_add_i32 s62, s62, 2
	s_add_u32 s58, s58, 0x100
	s_addc_u32 s59, s59, 0
	s_add_u32 s16, s16, 0x100
	s_addc_u32 s17, s17, 0
	s_cmp_lt_u32 s62, 14
	s_cbranch_scc1 .LBB0_2070
	s_mov_b64 s[18:19], 0

.LBB0_2074:
	ds_read_b128 v[166:169], v162
	ds_read_b128 v[170:173], v162 offset:1024
	ds_read_b128 v[174:177], v162 offset:2048
	ds_read_b128 v[178:181], v162 offset:3072
	ds_read_b128 v[182:185], v163
	ds_read_b128 v[186:189], v163 offset:1024
	ds_read_b128 v[190:193], v163 offset:2048
	ds_read_b128 v[194:197], v163 offset:3072
	s_add_u32 s18, s16, 0x80
	s_addc_u32 s19, s17, 0
	s_cmp_eq_u32 s58, 12
	s_cselect_b32 s19, s83, s19
	s_cselect_b32 s18, s82, s18
	s_cselect_b32 s21, s13, s57
	s_cselect_b32 s20, s12, s56
	s_cselect_b32 s59, s55, s54
	ds_read_b128 v[198:201], v164 offset:1024
	ds_read_b128 v[202:205], v164 offset:2048
	ds_read_b128 v[206:209], v164 offset:3072
	ds_read_b128 v[210:213], v164 offset:4096
	ds_read_b128 v[214:217], v164
	ds_read2_b32 v[232:233], v165 offset0:2 offset1:3
	ds_read_b128 v[218:221], v164 offset:5120
	ds_read_b128 v[224:227], v164 offset:6144
	ds_read_b128 v[228:231], v164 offset:7168
	s_add_i32 m0, s35, 0xc000
	s_waitcnt lgkmcnt(0)
	global_load_lds_dwordx4 v232, s[16:17]
	s_add_i32 m0, s35, 0xe000
	s_nop 0
	global_load_lds_dwordx4 v233, s[16:17]
	s_waitcnt vmcnt(8)
	s_waitcnt lgkmcnt(0)
	s_barrier
	s_setprio 1
	v_mfma_f32_16x16x32_bf16 v[126:129], v[166:169], v[214:217], v[126:129]
	v_mfma_f32_16x16x32_bf16 v[122:125], v[174:177], v[214:217], v[122:125]
	v_mfma_f32_16x16x32_bf16 v[94:97], v[166:169], v[202:205], v[94:97]
	v_mfma_f32_16x16x32_bf16 v[82:85], v[174:177], v[202:205], v[82:85]
	v_mfma_f32_16x16x32_bf16 v[54:57], v[166:169], v[210:213], v[54:57]
	v_mfma_f32_16x16x32_bf16 v[42:45], v[174:177], v[210:213], v[42:45]
	v_mfma_f32_16x16x32_bf16 v[18:21], v[166:169], v[224:227], v[18:21]
	v_mfma_f32_16x16x32_bf16 v[10:13], v[174:177], v[224:227], v[10:13]
	v_mfma_f32_16x16x32_bf16 v[126:129], v[170:173], v[198:201], v[126:129]
	v_mfma_f32_16x16x32_bf16 v[122:125], v[178:181], v[198:201], v[122:125]
	v_mfma_f32_16x16x32_bf16 v[94:97], v[170:173], v[206:209], v[94:97]
	v_mfma_f32_16x16x32_bf16 v[82:85], v[178:181], v[206:209], v[82:85]
	v_mfma_f32_16x16x32_bf16 v[54:57], v[170:173], v[218:221], v[54:57]
	v_mfma_f32_16x16x32_bf16 v[42:45], v[178:181], v[218:221], v[42:45]
	v_mfma_f32_16x16x32_bf16 v[18:21], v[170:173], v[228:231], v[18:21]
	v_mfma_f32_16x16x32_bf16 v[10:13], v[178:181], v[228:231], v[10:13]
	s_setprio 0
	s_setprio 1
	v_mfma_f32_16x16x32_bf16 v[102:105], v[182:185], v[214:217], v[102:105]
	v_mfma_f32_16x16x32_bf16 v[98:101], v[190:193], v[214:217], v[98:101]
	v_mfma_f32_16x16x32_bf16 v[70:73], v[182:185], v[202:205], v[70:73]
	v_mfma_f32_16x16x32_bf16 v[66:69], v[190:193], v[202:205], v[66:69]
	v_mfma_f32_16x16x32_bf16 v[38:41], v[182:185], v[210:213], v[38:41]
	v_mfma_f32_16x16x32_bf16 v[34:37], v[190:193], v[210:213], v[34:37]
	v_mfma_f32_16x16x32_bf16 v[6:9], v[182:185], v[224:227], v[6:9]
	v_mfma_f32_16x16x32_bf16 v[2:5], v[190:193], v[224:227], v[2:5]
	v_mfma_f32_16x16x32_bf16 v[102:105], v[186:189], v[198:201], v[102:105]
	v_mfma_f32_16x16x32_bf16 v[98:101], v[194:197], v[198:201], v[98:101]
	v_mfma_f32_16x16x32_bf16 v[70:73], v[186:189], v[206:209], v[70:73]
	v_mfma_f32_16x16x32_bf16 v[66:69], v[194:197], v[206:209], v[66:69]
	v_mfma_f32_16x16x32_bf16 v[38:41], v[186:189], v[218:221], v[38:41]
	v_mfma_f32_16x16x32_bf16 v[34:37], v[194:197], v[218:221], v[34:37]
	v_mfma_f32_16x16x32_bf16 v[6:9], v[186:189], v[228:231], v[6:9]
	v_mfma_f32_16x16x32_bf16 v[2:5], v[194:197], v[228:231], v[2:5]
	s_setprio 0
	s_barrier
	s_add_i32 s62, s41, s34
	v_lshl_add_u64 v[232:233], s[20:21], 0, v[134:135]
	s_mov_b32 m0, s62
	ds_read_b128 v[198:201], v164 offset:16384
	ds_read_b128 v[202:205], v164 offset:17408
	ds_read_b128 v[206:209], v164 offset:18432
	ds_read_b128 v[210:213], v164 offset:19456
	ds_read_b128 v[214:217], v164 offset:20480
	ds_read_b128 v[218:221], v164 offset:21504
	ds_read_b128 v[224:227], v164 offset:22528
	ds_read_b128 v[228:231], v164 offset:23552
	global_load_lds_dwordx4 v[232:233], off
	s_add_i32 m0, s62, 0x2000
	s_add_u32 s62, s20, 0x40000
	v_lshl_add_u64 v[234:235], s[20:21], 0, v[132:133]
	s_addc_u32 s63, s21, 0
	s_add_i32 s64, s42, s34
	global_load_lds_dwordx4 v[234:235], off
	s_mov_b32 m0, s64
	v_lshl_add_u32 v136, s59, 2, v149
	global_load_lds_dwordx4 v134, s[62:63]
	s_add_i32 m0, s64, 0x2000
	s_nop 0
	global_load_lds_dwordx4 v132, s[62:63]
	ds_read2_b32 v[236:237], v136 offset1:1
	s_mov_b32 m0, s35
	s_waitcnt lgkmcnt(0)
	global_load_lds_dwordx4 v236, s[18:19]
	s_mov_b32 m0, s36
	s_nop 0
	global_load_lds_dwordx4 v237, s[18:19]
	s_waitcnt vmcnt(8)
	s_waitcnt lgkmcnt(0)
	s_barrier
	s_setprio 1
	v_mfma_f32_16x16x32_bf16 v[118:121], v[166:169], v[198:201], v[118:121]
	v_mfma_f32_16x16x32_bf16 v[114:117], v[174:177], v[198:201], v[114:117]
	v_mfma_f32_16x16x32_bf16 v[90:93], v[166:169], v[206:209], v[90:93]
	v_mfma_f32_16x16x32_bf16 v[86:89], v[174:177], v[206:209], v[86:89]
	v_mfma_f32_16x16x32_bf16 v[62:65], v[166:169], v[214:217], v[62:65]
	v_mfma_f32_16x16x32_bf16 v[58:61], v[174:177], v[214:217], v[58:61]
	v_mfma_f32_16x16x32_bf16 v[30:33], v[166:169], v[224:227], v[30:33]
	v_mfma_f32_16x16x32_bf16 v[26:29], v[174:177], v[224:227], v[26:29]
	v_mfma_f32_16x16x32_bf16 v[118:121], v[170:173], v[202:205], v[118:121]
	v_mfma_f32_16x16x32_bf16 v[114:117], v[178:181], v[202:205], v[114:117]
	v_mfma_f32_16x16x32_bf16 v[90:93], v[170:173], v[210:213], v[90:93]
	v_mfma_f32_16x16x32_bf16 v[86:89], v[178:181], v[210:213], v[86:89]
	v_mfma_f32_16x16x32_bf16 v[62:65], v[170:173], v[218:221], v[62:65]
	v_mfma_f32_16x16x32_bf16 v[58:61], v[178:181], v[218:221], v[58:61]
	v_mfma_f32_16x16x32_bf16 v[30:33], v[170:173], v[228:231], v[30:33]
	v_mfma_f32_16x16x32_bf16 v[26:29], v[178:181], v[228:231], v[26:29]
	s_setprio 0
	s_setprio 1
	v_mfma_f32_16x16x32_bf16 v[110:113], v[182:185], v[198:201], v[110:113]
	v_mfma_f32_16x16x32_bf16 v[106:109], v[190:193], v[198:201], v[106:109]
	v_mfma_f32_16x16x32_bf16 v[78:81], v[182:185], v[206:209], v[78:81]
	v_mfma_f32_16x16x32_bf16 v[74:77], v[190:193], v[206:209], v[74:77]
	v_mfma_f32_16x16x32_bf16 v[50:53], v[182:185], v[214:217], v[50:53]
	v_mfma_f32_16x16x32_bf16 v[46:49], v[190:193], v[214:217], v[46:49]
	v_mfma_f32_16x16x32_bf16 v[22:25], v[182:185], v[224:227], v[22:25]
	v_mfma_f32_16x16x32_bf16 v[14:17], v[190:193], v[224:227], v[14:17]
	v_mfma_f32_16x16x32_bf16 v[110:113], v[186:189], v[202:205], v[110:113]
	v_mfma_f32_16x16x32_bf16 v[106:109], v[194:197], v[202:205], v[106:109]
	v_mfma_f32_16x16x32_bf16 v[78:81], v[186:189], v[210:213], v[78:81]
	v_mfma_f32_16x16x32_bf16 v[74:77], v[194:197], v[210:213], v[74:77]
	v_mfma_f32_16x16x32_bf16 v[50:53], v[186:189], v[218:221], v[50:53]
	v_mfma_f32_16x16x32_bf16 v[46:49], v[194:197], v[218:221], v[46:49]
	v_mfma_f32_16x16x32_bf16 v[22:25], v[186:189], v[228:231], v[22:25]
	v_mfma_f32_16x16x32_bf16 v[14:17], v[194:197], v[228:231], v[14:17]
	s_setprio 0
	s_barrier
	s_add_i32 s59, 0, 0x18000
	s_add_i32 s62, 0, 0x1c000
	v_add_u32_e32 v178, s59, v151
	v_add_u32_e32 v194, s62, v151
	ds_read_b128 v[166:169], v178
	ds_read_b128 v[170:173], v178 offset:1024
	ds_read_b128 v[174:177], v178 offset:2048
	ds_read_b128 v[178:181], v178 offset:3072
	ds_read_b128 v[182:185], v194
	ds_read_b128 v[186:189], v194 offset:1024
	ds_read_b128 v[190:193], v194 offset:2048
	ds_read_b128 v[194:197], v194 offset:3072
	ds_read_b128 v[198:201], v164 offset:32768
	ds_read_b128 v[202:205], v164 offset:33792
	ds_read_b128 v[206:209], v164 offset:34816
	ds_read_b128 v[210:213], v164 offset:35840
	ds_read_b128 v[214:217], v164 offset:36864
	ds_read_b128 v[218:221], v164 offset:37888
	ds_read2_b32 v[236:237], v136 offset0:2 offset1:3
	ds_read_b128 v[224:227], v164 offset:38912
	ds_read_b128 v[228:231], v164 offset:39936
	s_mov_b32 m0, s37
	s_waitcnt lgkmcnt(0)
	global_load_lds_dwordx4 v236, s[18:19]
	s_mov_b32 m0, s38
	s_nop 0
	global_load_lds_dwordx4 v237, s[18:19]
	s_waitcnt vmcnt(8)
	s_waitcnt lgkmcnt(0)
	s_barrier
	s_setprio 1
	v_mfma_f32_16x16x32_bf16 v[126:129], v[166:169], v[198:201], v[126:129]
	v_mfma_f32_16x16x32_bf16 v[122:125], v[174:177], v[198:201], v[122:125]
	v_mfma_f32_16x16x32_bf16 v[94:97], v[166:169], v[206:209], v[94:97]
	v_mfma_f32_16x16x32_bf16 v[82:85], v[174:177], v[206:209], v[82:85]
	v_mfma_f32_16x16x32_bf16 v[54:57], v[166:169], v[214:217], v[54:57]
	v_mfma_f32_16x16x32_bf16 v[42:45], v[174:177], v[214:217], v[42:45]
	v_mfma_f32_16x16x32_bf16 v[18:21], v[166:169], v[224:227], v[18:21]
	v_mfma_f32_16x16x32_bf16 v[10:13], v[174:177], v[224:227], v[10:13]
	v_mfma_f32_16x16x32_bf16 v[126:129], v[170:173], v[202:205], v[126:129]
	v_mfma_f32_16x16x32_bf16 v[122:125], v[178:181], v[202:205], v[122:125]
	v_mfma_f32_16x16x32_bf16 v[94:97], v[170:173], v[210:213], v[94:97]
	v_mfma_f32_16x16x32_bf16 v[82:85], v[178:181], v[210:213], v[82:85]
	v_mfma_f32_16x16x32_bf16 v[54:57], v[170:173], v[218:221], v[54:57]
	v_mfma_f32_16x16x32_bf16 v[42:45], v[178:181], v[218:221], v[42:45]
	v_mfma_f32_16x16x32_bf16 v[18:21], v[170:173], v[228:231], v[18:21]
	v_mfma_f32_16x16x32_bf16 v[10:13], v[178:181], v[228:231], v[10:13]
	s_setprio 0
	s_setprio 1
	v_mfma_f32_16x16x32_bf16 v[102:105], v[182:185], v[198:201], v[102:105]
	v_mfma_f32_16x16x32_bf16 v[98:101], v[190:193], v[198:201], v[98:101]
	v_mfma_f32_16x16x32_bf16 v[70:73], v[182:185], v[206:209], v[70:73]
	v_mfma_f32_16x16x32_bf16 v[66:69], v[190:193], v[206:209], v[66:69]
	v_mfma_f32_16x16x32_bf16 v[38:41], v[182:185], v[214:217], v[38:41]
	v_mfma_f32_16x16x32_bf16 v[34:37], v[190:193], v[214:217], v[34:37]
	v_mfma_f32_16x16x32_bf16 v[6:9], v[182:185], v[224:227], v[6:9]
	v_mfma_f32_16x16x32_bf16 v[2:5], v[190:193], v[224:227], v[2:5]
	v_mfma_f32_16x16x32_bf16 v[102:105], v[186:189], v[202:205], v[102:105]
	v_mfma_f32_16x16x32_bf16 v[98:101], v[194:197], v[202:205], v[98:101]
	v_mfma_f32_16x16x32_bf16 v[70:73], v[186:189], v[210:213], v[70:73]
	v_mfma_f32_16x16x32_bf16 v[66:69], v[194:197], v[210:213], v[66:69]
	v_mfma_f32_16x16x32_bf16 v[38:41], v[186:189], v[218:221], v[38:41]
	v_mfma_f32_16x16x32_bf16 v[34:37], v[194:197], v[218:221], v[34:37]
	v_mfma_f32_16x16x32_bf16 v[6:9], v[186:189], v[228:231], v[6:9]
	v_mfma_f32_16x16x32_bf16 v[2:5], v[194:197], v[228:231], v[2:5]
	s_setprio 0
	s_barrier
	s_add_i32 s59, s59, s34
	v_lshl_add_u64 v[232:233], v[232:233], 0, s[6:7]
	s_mov_b32 m0, s59
	ds_read_b128 v[198:201], v164 offset:49152
	ds_read_b128 v[202:205], v164 offset:50176
	ds_read_b128 v[206:209], v164 offset:51200
	ds_read_b128 v[210:213], v164 offset:52224
	ds_read_b128 v[214:217], v164 offset:53248
	ds_read_b128 v[218:221], v164 offset:54272
	ds_read_b128 v[224:227], v164 offset:55296
	ds_read_b128 v[228:231], v164 offset:56320
	global_load_lds_dwordx4 v[232:233], off
	s_add_i32 m0, s59, 0x2000
	s_add_u32 s20, s20, 0x40080
	v_lshl_add_u64 v[232:233], v[234:235], 0, s[6:7]
	s_addc_u32 s21, s21, 0
	s_add_i32 s59, s62, s34
	global_load_lds_dwordx4 v[232:233], off
	s_mov_b32 m0, s59
	s_nop 0
	global_load_lds_dwordx4 v134, s[20:21]
	s_add_i32 m0, s59, 0x2000
	s_nop 0
	global_load_lds_dwordx4 v132, s[20:21]
	ds_read2_b32 v[232:233], v136 offset1:1
	s_mov_b32 m0, s39
	s_waitcnt lgkmcnt(0)
	v_mov_b32_e32 v136, v232
	v_lshl_add_u64 v[234:235], s[18:19], 0, v[136:137]
	v_mov_b32_e32 v136, v233
	v_lshl_add_u64 v[234:235], v[234:235], 0, s[6:7]
	v_lshl_add_u64 v[232:233], s[18:19], 0, v[136:137]
	global_load_lds_dwordx4 v[234:235], off
	v_lshl_add_u64 v[232:233], v[232:233], 0, s[6:7]
	s_mov_b32 m0, s40
	s_nop 0
	global_load_lds_dwordx4 v[232:233], off
	s_waitcnt vmcnt(8)
	s_waitcnt lgkmcnt(0)
	s_barrier
	s_setprio 1
	v_mfma_f32_16x16x32_bf16 v[118:121], v[166:169], v[198:201], v[118:121]
	v_mfma_f32_16x16x32_bf16 v[114:117], v[174:177], v[198:201], v[114:117]
	v_mfma_f32_16x16x32_bf16 v[90:93], v[166:169], v[206:209], v[90:93]
	v_mfma_f32_16x16x32_bf16 v[86:89], v[174:177], v[206:209], v[86:89]
	v_mfma_f32_16x16x32_bf16 v[62:65], v[166:169], v[214:217], v[62:65]
	v_mfma_f32_16x16x32_bf16 v[58:61], v[174:177], v[214:217], v[58:61]
	v_mfma_f32_16x16x32_bf16 v[30:33], v[166:169], v[224:227], v[30:33]
	v_mfma_f32_16x16x32_bf16 v[26:29], v[174:177], v[224:227], v[26:29]
	v_mfma_f32_16x16x32_bf16 v[118:121], v[170:173], v[202:205], v[118:121]
	v_mfma_f32_16x16x32_bf16 v[114:117], v[178:181], v[202:205], v[114:117]
	v_mfma_f32_16x16x32_bf16 v[90:93], v[170:173], v[210:213], v[90:93]
	v_mfma_f32_16x16x32_bf16 v[86:89], v[178:181], v[210:213], v[86:89]
	v_mfma_f32_16x16x32_bf16 v[62:65], v[170:173], v[218:221], v[62:65]
	v_mfma_f32_16x16x32_bf16 v[58:61], v[178:181], v[218:221], v[58:61]
	v_mfma_f32_16x16x32_bf16 v[30:33], v[170:173], v[228:231], v[30:33]
	v_mfma_f32_16x16x32_bf16 v[26:29], v[178:181], v[228:231], v[26:29]
	s_setprio 0
	s_setprio 1
	v_mfma_f32_16x16x32_bf16 v[110:113], v[182:185], v[198:201], v[110:113]
	v_mfma_f32_16x16x32_bf16 v[106:109], v[190:193], v[198:201], v[106:109]
	v_mfma_f32_16x16x32_bf16 v[78:81], v[182:185], v[206:209], v[78:81]
	v_mfma_f32_16x16x32_bf16 v[74:77], v[190:193], v[206:209], v[74:77]
	v_mfma_f32_16x16x32_bf16 v[50:53], v[182:185], v[214:217], v[50:53]
	v_mfma_f32_16x16x32_bf16 v[46:49], v[190:193], v[214:217], v[46:49]
	v_mfma_f32_16x16x32_bf16 v[22:25], v[182:185], v[224:227], v[22:25]
	v_mfma_f32_16x16x32_bf16 v[14:17], v[190:193], v[224:227], v[14:17]
	v_mfma_f32_16x16x32_bf16 v[110:113], v[186:189], v[202:205], v[110:113]
	v_mfma_f32_16x16x32_bf16 v[106:109], v[194:197], v[202:205], v[106:109]
	v_mfma_f32_16x16x32_bf16 v[78:81], v[186:189], v[210:213], v[78:81]
	v_mfma_f32_16x16x32_bf16 v[74:77], v[194:197], v[210:213], v[74:77]
	v_mfma_f32_16x16x32_bf16 v[50:53], v[186:189], v[218:221], v[50:53]
	v_mfma_f32_16x16x32_bf16 v[46:49], v[194:197], v[218:221], v[46:49]
	v_mfma_f32_16x16x32_bf16 v[22:25], v[186:189], v[228:231], v[22:25]
	v_mfma_f32_16x16x32_bf16 v[14:17], v[194:197], v[228:231], v[14:17]
	s_setprio 0
	s_barrier
	s_add_i32 s58, s58, 2
	s_add_u32 s56, s56, 0x100
	s_addc_u32 s57, s57, 0
	s_add_u32 s16, s16, 0x100
	s_addc_u32 s17, s17, 0
	s_cmp_gt_u32 s58, 13
	s_cbranch_scc0 .LBB0_2074

.LBB0_2119:
	s_mov_b64 s[20:21], 0x80
	s_add_i32 m0, s67, 0x18000
	v_lshl_add_u64 v[0:1], v[0:1], 0, s[20:21]
	s_waitcnt vmcnt(2)
	s_barrier
	global_load_lds_dwordx4 v[0:1], off
	v_lshl_add_u64 v[0:1], v[2:3], 0, s[20:21]
	s_add_i32 m0, s67, 0x1a000
	s_lshl_b32 s3, s3, 5
	global_load_lds_dwordx4 v[0:1], off
	ds_read_b64 v[0:1], v155
	s_lshl_b32 s9, s2, 13
	s_and_b32 s3, s3, 0x60
	s_add_u32 s22, s50, 0x5c00080
	s_addc_u32 s23, s51, 0
	s_add_i32 s71, s67, 0x8000
	s_add_i32 s72, s67, 0xa000
	s_mov_b32 m0, s71
	s_add_u32 s6, s4, 0x200080
	s_waitcnt lgkmcnt(0)
	global_load_lds_dwordx4 v0, s[22:23]
	s_mov_b32 m0, s72
	s_addc_u32 s7, s5, 0
	global_load_lds_dwordx4 v1, s[22:23]
	s_add_i32 m0, s67, 0x1c000
	global_load_lds_dwordx4 v156, s[6:7]
	v_lshl_add_u64 v[0:1], s[6:7], 0, v[158:159]
	s_add_i32 m0, s67, 0x1e000
	s_cmpk_lt_u32 s8, 0x100
	global_load_lds_dwordx4 v[0:1], off
	s_cselect_b64 s[28:29], -1, 0
	s_add_u32 s30, s50, 0x5c00100
	s_addc_u32 s31, s51, 0
	s_add_u32 s34, s50, 0x5c00180
	s_addc_u32 s35, s51, 0
	s_add_u32 s96, s50, 0x5c00200
	s_addc_u32 s97, s51, 0
	s_add_u32 s60, s50, 0x5c00280
	s_addc_u32 s61, s51, 0
	s_add_u32 s18, s50, 0x5c00300
	v_lshlrev_b32_e32 v1, 2, v222
	s_addc_u32 s19, s51, 0
	v_lshl_or_b32 v0, v222, 6, v139
	v_and_b32_e32 v1, 32, v1
	s_waitcnt vmcnt(6)
	s_add_u32 s52, s50, 0x5c00380
	v_lshl_or_b32 v180, s2, 6, v222
	v_bitop3_b32 v0, v0, s9, v1 bitop3:0xde
	v_lshl_or_b32 v181, s3, 7, v140
	s_addc_u32 s53, s51, 0
	s_add_i32 s2, 0, 0x224f0
	s_add_i32 s74, 0, 0x14000
	s_add_i32 s75, 0, 0x10000
	v_or_b32_e32 v182, v5, v152
	v_or_b32_e32 v183, v4, v152
	v_add_u32_e32 v184, 0, v0
	v_or_b32_e32 v185, 16, v180
	v_or_b32_e32 v186, 32, v180
	v_or_b32_e32 v187, 48, v180
	v_add_u32_e32 v188, 0x80, v180
	v_add_u32_e32 v189, 0x90, v180
	v_add_u32_e32 v190, 0xa0, v180
	v_add_u32_e32 v191, 0xb0, v180
	v_or_b32_e32 v192, s3, v138
	v_mov_b32_e32 v193, s2
	s_add_i32 s73, 0, 0x22400
	v_add_u32_e32 v194, s74, v181
	v_add_u32_e32 v195, s75, v181
	s_mov_b64 s[54:55], 0x380
	s_mov_b32 s76, 0
	s_barrier
	s_branch .LBB0_2122

.LBB0_2146:
	s_and_b64 s[8:9], s[6:7], exec
	s_cselect_b32 s59, s81, s17
	s_lshl_b32 s8, s62, 6
	s_ashr_i32 s9, s8, 31
	s_cmpk_lt_i32 s58, 0x81
	s_waitcnt vmcnt(0)
	v_lshl_add_u32 v128, s17, 2, v155
	s_mov_b64 s[10:11], -1
	s_cbranch_scc0 .LBB0_2160
	ds_read_b128 v[0:3], v194 offset:3072
	ds_read_b128 v[4:7], v194 offset:2048
	ds_read_b128 v[8:11], v194 offset:1024
	ds_read_b128 v[12:15], v194
	ds_read_b128 v[16:19], v195 offset:3072
	ds_read_b128 v[20:23], v195 offset:2048
	ds_read_b128 v[24:27], v195 offset:1024
	ds_read_b128 v[28:31], v195
	ds_read_b128 v[32:35], v184
	ds_read_b128 v[36:39], v184 offset:1024
	ds_read_b128 v[40:43], v184 offset:2048
	ds_read_b128 v[44:47], v184 offset:3072
	ds_read_b128 v[48:51], v184 offset:4096
	ds_read_b128 v[52:55], v184 offset:5120
	ds_read2_b32 v[64:65], v128 offset0:2 offset1:3
	ds_read_b128 v[56:59], v184 offset:6144
	ds_read_b128 v[60:63], v184 offset:7168
	s_add_i32 s84, s67, 0xc000
	s_mov_b32 m0, s84
	s_add_i32 s85, s67, 0xe000
	s_waitcnt lgkmcnt(0)
	global_load_lds_dwordx4 v64, s[22:23]
	s_mov_b32 m0, s85
	s_nop 0
	global_load_lds_dwordx4 v65, s[22:23]
	s_waitcnt vmcnt(8)
	s_waitcnt lgkmcnt(0)
	s_barrier
	s_setprio 1
	v_mfma_f32_16x16x32_bf16 v[64:67], v[28:31], v[32:35], 0
	v_mfma_f32_16x16x32_bf16 v[70:73], v[24:27], v[36:39], v[64:67]
	v_mfma_f32_16x16x32_bf16 v[64:67], v[20:23], v[32:35], 0
	v_mfma_f32_16x16x32_bf16 v[74:77], v[16:19], v[36:39], v[64:67]
	v_mfma_f32_16x16x32_bf16 v[64:67], v[28:31], v[40:43], 0
	v_mfma_f32_16x16x32_bf16 v[78:81], v[24:27], v[44:47], v[64:67]
	v_mfma_f32_16x16x32_bf16 v[64:67], v[20:23], v[40:43], 0
	v_mfma_f32_16x16x32_bf16 v[82:85], v[16:19], v[44:47], v[64:67]
	v_mfma_f32_16x16x32_bf16 v[64:67], v[28:31], v[48:51], 0
	v_mfma_f32_16x16x32_bf16 v[86:89], v[24:27], v[52:55], v[64:67]
	v_mfma_f32_16x16x32_bf16 v[64:67], v[20:23], v[48:51], 0
	v_mfma_f32_16x16x32_bf16 v[28:31], v[28:31], v[56:59], 0
	v_mfma_f32_16x16x32_bf16 v[20:23], v[20:23], v[56:59], 0
	v_mfma_f32_16x16x32_bf16 v[90:93], v[16:19], v[52:55], v[64:67]
	v_mfma_f32_16x16x32_bf16 v[24:27], v[24:27], v[60:63], v[28:31]
	v_mfma_f32_16x16x32_bf16 v[16:19], v[16:19], v[60:63], v[20:23]
	s_setprio 0
	s_setprio 1
	v_mfma_f32_16x16x32_bf16 v[20:23], v[12:15], v[32:35], 0
	v_mfma_f32_16x16x32_bf16 v[28:31], v[4:7], v[32:35], 0
	v_mfma_f32_16x16x32_bf16 v[20:23], v[8:11], v[36:39], v[20:23]
	v_mfma_f32_16x16x32_bf16 v[28:31], v[0:3], v[36:39], v[28:31]
	v_mfma_f32_16x16x32_bf16 v[32:35], v[12:15], v[40:43], 0
	v_mfma_f32_16x16x32_bf16 v[36:39], v[4:7], v[40:43], 0
	v_mfma_f32_16x16x32_bf16 v[32:35], v[8:11], v[44:47], v[32:35]
	v_mfma_f32_16x16x32_bf16 v[36:39], v[0:3], v[44:47], v[36:39]
	v_mfma_f32_16x16x32_bf16 v[40:43], v[12:15], v[48:51], 0
	v_mfma_f32_16x16x32_bf16 v[44:47], v[4:7], v[48:51], 0
	v_mfma_f32_16x16x32_bf16 v[12:15], v[12:15], v[56:59], 0
	v_mfma_f32_16x16x32_bf16 v[4:7], v[4:7], v[56:59], 0
	v_mfma_f32_16x16x32_bf16 v[40:43], v[8:11], v[52:55], v[40:43]
	v_mfma_f32_16x16x32_bf16 v[44:47], v[0:3], v[52:55], v[44:47]
	v_mfma_f32_16x16x32_bf16 v[8:11], v[8:11], v[60:63], v[12:15]
	v_mfma_f32_16x16x32_bf16 v[0:3], v[0:3], v[60:63], v[4:7]
	s_setprio 0
	s_barrier
	v_lshl_add_u64 v[64:65], s[4:5], 0, v[156:157]
	s_mov_b64 s[10:11], 0x100
	s_add_i32 s86, s75, s66
	v_lshl_add_u64 v[4:5], v[64:65], 0, s[10:11]
	s_mov_b32 m0, s86
	v_lshl_add_u64 v[66:67], s[4:5], 0, v[158:159]
	s_add_i32 s87, s86, 0x2000
	global_load_lds_dwordx4 v[4:5], off
	v_lshl_add_u64 v[4:5], v[66:67], 0, s[10:11]
	s_add_u32 s10, s4, 0x200100
	s_mov_b32 m0, s87
	s_addc_u32 s11, s5, 0
	s_add_i32 s88, s74, s66
	global_load_lds_dwordx4 v[4:5], off
	s_mov_b32 m0, s88
	s_add_i32 s89, s88, 0x2000
	global_load_lds_dwordx4 v156, s[10:11]
	s_mov_b32 m0, s89
	s_nop 0
	global_load_lds_dwordx4 v158, s[10:11]
	ds_read2_b32 v[4:5], v128 offset1:1
	s_mov_b32 m0, s67
	s_waitcnt lgkmcnt(0)
	global_load_lds_dwordx4 v4, s[30:31]
	s_mov_b32 m0, s68
	s_nop 0
	global_load_lds_dwordx4 v5, s[30:31]
	s_waitcnt vmcnt(8)
	s_waitcnt lgkmcnt(0)
	s_barrier
	s_barrier
	s_add_i32 s91, 0, 0x18000
	s_add_i32 s92, 0, 0x1c000
	v_add_u32_e32 v68, s91, v181
	v_add_u32_e32 v69, s92, v181
	ds_read_b128 v[4:7], v68
	ds_read_b128 v[12:15], v68 offset:1024
	ds_read_b128 v[48:51], v68 offset:2048
	ds_read_b128 v[52:55], v68 offset:3072
	ds_read_b128 v[56:59], v69
	ds_read_b128 v[60:63], v69 offset:1024
	ds_read_b128 v[94:97], v69 offset:2048
	ds_read_b128 v[98:101], v69 offset:3072
	ds_read_b128 v[102:105], v184 offset:32768
	ds_read_b128 v[106:109], v184 offset:33792
	ds_read_b128 v[110:113], v184 offset:34816
	ds_read_b128 v[114:117], v184 offset:35840
	ds_read_b128 v[118:121], v184 offset:36864
	ds_read_b128 v[122:125], v184 offset:37888
	ds_read2_b32 v[126:127], v128 offset0:2 offset1:3
	ds_read_b128 v[130:133], v184 offset:38912
	ds_read_b128 v[134:137], v184 offset:39936
	s_mov_b32 m0, s69
	s_waitcnt lgkmcnt(0)
	global_load_lds_dwordx4 v126, s[30:31]
	s_mov_b32 m0, s70
	s_nop 0
	global_load_lds_dwordx4 v127, s[30:31]
	s_waitcnt vmcnt(8)
	s_waitcnt lgkmcnt(0)
	s_barrier
	s_setprio 1
	v_mfma_f32_16x16x32_bf16 v[70:73], v[4:7], v[102:105], v[70:73]
	v_mfma_f32_16x16x32_bf16 v[78:81], v[4:7], v[110:113], v[78:81]
	v_mfma_f32_16x16x32_bf16 v[86:89], v[4:7], v[118:121], v[86:89]
	v_mfma_f32_16x16x32_bf16 v[4:7], v[4:7], v[130:133], v[24:27]
	v_mfma_f32_16x16x32_bf16 v[70:73], v[12:15], v[106:109], v[70:73]
	v_mfma_f32_16x16x32_bf16 v[78:81], v[12:15], v[114:117], v[78:81]
	v_mfma_f32_16x16x32_bf16 v[86:89], v[12:15], v[122:125], v[86:89]
	v_mfma_f32_16x16x32_bf16 v[4:7], v[12:15], v[134:137], v[4:7]
	v_mfma_f32_16x16x32_bf16 v[12:15], v[48:51], v[130:133], v[16:19]
	v_mfma_f32_16x16x32_bf16 v[74:77], v[48:51], v[102:105], v[74:77]
	v_mfma_f32_16x16x32_bf16 v[82:85], v[48:51], v[110:113], v[82:85]
	v_mfma_f32_16x16x32_bf16 v[90:93], v[48:51], v[118:121], v[90:93]
	v_mfma_f32_16x16x32_bf16 v[12:15], v[52:55], v[134:137], v[12:15]
	v_mfma_f32_16x16x32_bf16 v[74:77], v[52:55], v[106:109], v[74:77]
	v_mfma_f32_16x16x32_bf16 v[82:85], v[52:55], v[114:117], v[82:85]
	v_mfma_f32_16x16x32_bf16 v[90:93], v[52:55], v[122:125], v[90:93]
	s_setprio 0
	s_setprio 1
	v_mfma_f32_16x16x32_bf16 v[16:19], v[56:59], v[102:105], v[20:23]
	v_mfma_f32_16x16x32_bf16 v[20:23], v[94:97], v[102:105], v[28:31]
	v_mfma_f32_16x16x32_bf16 v[24:27], v[56:59], v[110:113], v[32:35]
	v_mfma_f32_16x16x32_bf16 v[28:31], v[94:97], v[110:113], v[36:39]
	v_mfma_f32_16x16x32_bf16 v[32:35], v[56:59], v[118:121], v[40:43]
	v_mfma_f32_16x16x32_bf16 v[36:39], v[94:97], v[118:121], v[44:47]
	v_mfma_f32_16x16x32_bf16 v[8:11], v[56:59], v[130:133], v[8:11]
	v_mfma_f32_16x16x32_bf16 v[0:3], v[94:97], v[130:133], v[0:3]
	v_mfma_f32_16x16x32_bf16 v[16:19], v[60:63], v[106:109], v[16:19]
	v_mfma_f32_16x16x32_bf16 v[20:23], v[98:101], v[106:109], v[20:23]
	v_mfma_f32_16x16x32_bf16 v[24:27], v[60:63], v[114:117], v[24:27]
	v_mfma_f32_16x16x32_bf16 v[28:31], v[98:101], v[114:117], v[28:31]
	v_mfma_f32_16x16x32_bf16 v[32:35], v[60:63], v[122:125], v[32:35]
	v_mfma_f32_16x16x32_bf16 v[36:39], v[98:101], v[122:125], v[36:39]
	v_mfma_f32_16x16x32_bf16 v[8:11], v[60:63], v[134:137], v[8:11]
	v_mfma_f32_16x16x32_bf16 v[0:3], v[98:101], v[134:137], v[0:3]
	s_setprio 0
	s_barrier
	s_mov_b64 s[10:11], 0x180
	s_add_i32 s91, s91, s66
	v_lshl_add_u64 v[40:41], v[64:65], 0, s[10:11]
	s_mov_b32 m0, s91
	s_add_i32 s90, s91, 0x2000
	global_load_lds_dwordx4 v[40:41], off
	v_lshl_add_u64 v[40:41], v[66:67], 0, s[10:11]
	s_add_u32 s10, s4, 0x200180
	s_mov_b32 m0, s90
	s_addc_u32 s11, s5, 0
	s_add_i32 s92, s92, s66
	global_load_lds_dwordx4 v[40:41], off
	s_mov_b32 m0, s92
	s_add_i32 s93, s92, 0x2000
	global_load_lds_dwordx4 v156, s[10:11]
	s_mov_b32 m0, s93
	s_nop 0
	global_load_lds_dwordx4 v158, s[10:11]
	ds_read2_b32 v[40:41], v128 offset1:1
	s_mov_b32 m0, s71
	s_waitcnt lgkmcnt(0)
	global_load_lds_dwordx4 v40, s[34:35]
	s_mov_b32 m0, s72
	s_nop 0
	global_load_lds_dwordx4 v41, s[34:35]
	s_waitcnt vmcnt(8)
	s_waitcnt lgkmcnt(0)
	s_barrier
	s_barrier
	ds_read_b128 v[40:43], v194 offset:3072
	ds_read_b128 v[44:47], v194 offset:2048
	ds_read_b128 v[48:51], v194 offset:1024
	ds_read_b128 v[52:55], v194
	ds_read_b128 v[56:59], v195 offset:3072
	ds_read_b128 v[60:63], v195 offset:2048
	ds_read_b128 v[94:97], v195 offset:1024
	ds_read_b128 v[98:101], v195
	ds_read_b128 v[102:105], v184
	ds_read_b128 v[106:109], v184 offset:1024
	ds_read_b128 v[110:113], v184 offset:2048
	ds_read_b128 v[114:117], v184 offset:3072
	ds_read_b128 v[118:121], v184 offset:4096
	ds_read_b128 v[122:125], v184 offset:5120
	ds_read2_b32 v[126:127], v128 offset0:2 offset1:3
	ds_read_b128 v[130:133], v184 offset:6144
	ds_read_b128 v[134:137], v184 offset:7168
	s_mov_b32 m0, s84
	s_waitcnt lgkmcnt(0)
	global_load_lds_dwordx4 v126, s[34:35]
	s_mov_b32 m0, s85
	s_nop 0
	global_load_lds_dwordx4 v127, s[34:35]
	s_waitcnt vmcnt(8)
	s_waitcnt lgkmcnt(0)
	s_barrier
	s_setprio 1
	v_mfma_f32_16x16x32_bf16 v[4:7], v[98:101], v[130:133], v[4:7]
	v_mfma_f32_16x16x32_bf16 v[12:15], v[60:63], v[130:133], v[12:15]
	v_mfma_f32_16x16x32_bf16 v[70:73], v[98:101], v[102:105], v[70:73]
	v_mfma_f32_16x16x32_bf16 v[74:77], v[60:63], v[102:105], v[74:77]
	v_mfma_f32_16x16x32_bf16 v[78:81], v[98:101], v[110:113], v[78:81]
	v_mfma_f32_16x16x32_bf16 v[82:85], v[60:63], v[110:113], v[82:85]
	v_mfma_f32_16x16x32_bf16 v[86:89], v[98:101], v[118:121], v[86:89]
	v_mfma_f32_16x16x32_bf16 v[90:93], v[60:63], v[118:121], v[90:93]
	v_mfma_f32_16x16x32_bf16 v[4:7], v[94:97], v[134:137], v[4:7]
	v_mfma_f32_16x16x32_bf16 v[12:15], v[56:59], v[134:137], v[12:15]
	v_mfma_f32_16x16x32_bf16 v[70:73], v[94:97], v[106:109], v[70:73]
	v_mfma_f32_16x16x32_bf16 v[74:77], v[56:59], v[106:109], v[74:77]
	v_mfma_f32_16x16x32_bf16 v[78:81], v[94:97], v[114:117], v[78:81]
	v_mfma_f32_16x16x32_bf16 v[82:85], v[56:59], v[114:117], v[82:85]
	v_mfma_f32_16x16x32_bf16 v[86:89], v[94:97], v[122:125], v[86:89]
	v_mfma_f32_16x16x32_bf16 v[90:93], v[56:59], v[122:125], v[90:93]
	s_setprio 0
	s_setprio 1
	v_mfma_f32_16x16x32_bf16 v[16:19], v[52:55], v[102:105], v[16:19]
	v_mfma_f32_16x16x32_bf16 v[20:23], v[44:47], v[102:105], v[20:23]
	v_mfma_f32_16x16x32_bf16 v[24:27], v[52:55], v[110:113], v[24:27]
	v_mfma_f32_16x16x32_bf16 v[28:31], v[44:47], v[110:113], v[28:31]
	v_mfma_f32_16x16x32_bf16 v[32:35], v[52:55], v[118:121], v[32:35]
	v_mfma_f32_16x16x32_bf16 v[36:39], v[44:47], v[118:121], v[36:39]
	v_mfma_f32_16x16x32_bf16 v[8:11], v[52:55], v[130:133], v[8:11]
	v_mfma_f32_16x16x32_bf16 v[0:3], v[44:47], v[130:133], v[0:3]
	v_mfma_f32_16x16x32_bf16 v[16:19], v[48:51], v[106:109], v[16:19]
	v_mfma_f32_16x16x32_bf16 v[20:23], v[40:43], v[106:109], v[20:23]
	v_mfma_f32_16x16x32_bf16 v[24:27], v[48:51], v[114:117], v[24:27]
	v_mfma_f32_16x16x32_bf16 v[28:31], v[40:43], v[114:117], v[28:31]
	v_mfma_f32_16x16x32_bf16 v[32:35], v[48:51], v[122:125], v[32:35]
	v_mfma_f32_16x16x32_bf16 v[36:39], v[40:43], v[122:125], v[36:39]
	v_mfma_f32_16x16x32_bf16 v[8:11], v[48:51], v[134:137], v[8:11]
	v_mfma_f32_16x16x32_bf16 v[0:3], v[40:43], v[134:137], v[0:3]
	s_setprio 0
	s_barrier
	s_mov_b64 s[10:11], 0x200
	s_mov_b32 m0, s86
	v_lshl_add_u64 v[40:41], v[64:65], 0, s[10:11]
	global_load_lds_dwordx4 v[40:41], off
	v_lshl_add_u64 v[40:41], v[66:67], 0, s[10:11]
	s_add_u32 s10, s4, 0x200200
	s_mov_b32 m0, s87
	s_addc_u32 s11, s5, 0
	global_load_lds_dwordx4 v[40:41], off
	s_mov_b32 m0, s88
	s_nop 0
	global_load_lds_dwordx4 v156, s[10:11]
	s_mov_b32 m0, s89
	s_nop 0
	global_load_lds_dwordx4 v158, s[10:11]
	ds_read2_b32 v[40:41], v128 offset1:1
	s_mov_b32 m0, s67
	s_waitcnt lgkmcnt(0)
	global_load_lds_dwordx4 v40, s[96:97]
	s_mov_b32 m0, s68
	s_nop 0
	global_load_lds_dwordx4 v41, s[96:97]
	s_waitcnt vmcnt(8)
	s_waitcnt lgkmcnt(0)
	s_barrier
	s_barrier
	ds_read_b128 v[40:43], v68
	ds_read_b128 v[44:47], v68 offset:1024
	ds_read_b128 v[48:51], v68 offset:2048
	ds_read_b128 v[52:55], v68 offset:3072
	ds_read_b128 v[56:59], v69
	ds_read_b128 v[60:63], v69 offset:1024
	ds_read_b128 v[94:97], v69 offset:2048
	ds_read_b128 v[98:101], v69 offset:3072
	ds_read_b128 v[102:105], v184 offset:32768
	ds_read_b128 v[106:109], v184 offset:33792
	ds_read_b128 v[110:113], v184 offset:34816
	ds_read_b128 v[114:117], v184 offset:35840
	ds_read_b128 v[118:121], v184 offset:36864
	ds_read_b128 v[122:125], v184 offset:37888
	ds_read2_b32 v[126:127], v128 offset0:2 offset1:3
	ds_read_b128 v[130:133], v184 offset:38912
	ds_read_b128 v[134:137], v184 offset:39936
	s_mov_b32 m0, s69
	s_waitcnt lgkmcnt(0)
	global_load_lds_dwordx4 v126, s[96:97]
	s_mov_b32 m0, s70
	s_nop 0
	global_load_lds_dwordx4 v127, s[96:97]
	s_waitcnt vmcnt(8)
	s_waitcnt lgkmcnt(0)
	s_barrier
	s_setprio 1
	v_mfma_f32_16x16x32_bf16 v[4:7], v[40:43], v[130:133], v[4:7]
	v_mfma_f32_16x16x32_bf16 v[12:15], v[48:51], v[130:133], v[12:15]
	v_mfma_f32_16x16x32_bf16 v[70:73], v[40:43], v[102:105], v[70:73]
	v_mfma_f32_16x16x32_bf16 v[74:77], v[48:51], v[102:105], v[74:77]
	v_mfma_f32_16x16x32_bf16 v[78:81], v[40:43], v[110:113], v[78:81]
	v_mfma_f32_16x16x32_bf16 v[82:85], v[48:51], v[110:113], v[82:85]
	v_mfma_f32_16x16x32_bf16 v[86:89], v[40:43], v[118:121], v[86:89]
	v_mfma_f32_16x16x32_bf16 v[90:93], v[48:51], v[118:121], v[90:93]
	v_mfma_f32_16x16x32_bf16 v[4:7], v[44:47], v[134:137], v[4:7]
	v_mfma_f32_16x16x32_bf16 v[12:15], v[52:55], v[134:137], v[12:15]
	v_mfma_f32_16x16x32_bf16 v[70:73], v[44:47], v[106:109], v[70:73]
	v_mfma_f32_16x16x32_bf16 v[74:77], v[52:55], v[106:109], v[74:77]
	v_mfma_f32_16x16x32_bf16 v[78:81], v[44:47], v[114:117], v[78:81]
	v_mfma_f32_16x16x32_bf16 v[82:85], v[52:55], v[114:117], v[82:85]
	v_mfma_f32_16x16x32_bf16 v[86:89], v[44:47], v[122:125], v[86:89]
	v_mfma_f32_16x16x32_bf16 v[90:93], v[52:55], v[122:125], v[90:93]
	s_setprio 0
	s_setprio 1
	v_mfma_f32_16x16x32_bf16 v[16:19], v[56:59], v[102:105], v[16:19]
	v_mfma_f32_16x16x32_bf16 v[20:23], v[94:97], v[102:105], v[20:23]
	v_mfma_f32_16x16x32_bf16 v[24:27], v[56:59], v[110:113], v[24:27]
	v_mfma_f32_16x16x32_bf16 v[28:31], v[94:97], v[110:113], v[28:31]
	v_mfma_f32_16x16x32_bf16 v[32:35], v[56:59], v[118:121], v[32:35]
	v_mfma_f32_16x16x32_bf16 v[36:39], v[94:97], v[118:121], v[36:39]
	v_mfma_f32_16x16x32_bf16 v[8:11], v[56:59], v[130:133], v[8:11]
	v_mfma_f32_16x16x32_bf16 v[0:3], v[94:97], v[130:133], v[0:3]
	v_mfma_f32_16x16x32_bf16 v[16:19], v[60:63], v[106:109], v[16:19]
	v_mfma_f32_16x16x32_bf16 v[20:23], v[98:101], v[106:109], v[20:23]
	v_mfma_f32_16x16x32_bf16 v[24:27], v[60:63], v[114:117], v[24:27]
	v_mfma_f32_16x16x32_bf16 v[28:31], v[98:101], v[114:117], v[28:31]
	v_mfma_f32_16x16x32_bf16 v[32:35], v[60:63], v[122:125], v[32:35]
	v_mfma_f32_16x16x32_bf16 v[36:39], v[98:101], v[122:125], v[36:39]
	v_mfma_f32_16x16x32_bf16 v[8:11], v[60:63], v[134:137], v[8:11]
	v_mfma_f32_16x16x32_bf16 v[0:3], v[98:101], v[134:137], v[0:3]
	s_setprio 0
	s_barrier
	s_mov_b64 s[10:11], 0x280
	s_mov_b32 m0, s91
	v_lshl_add_u64 v[40:41], v[64:65], 0, s[10:11]
	global_load_lds_dwordx4 v[40:41], off
	v_lshl_add_u64 v[40:41], v[66:67], 0, s[10:11]
	s_add_u32 s10, s4, 0x200280
	s_mov_b32 m0, s90
	s_addc_u32 s11, s5, 0
	global_load_lds_dwordx4 v[40:41], off
	s_mov_b32 m0, s92
	s_nop 0
	global_load_lds_dwordx4 v156, s[10:11]
	s_mov_b32 m0, s93
	s_nop 0
	global_load_lds_dwordx4 v158, s[10:11]
	ds_read2_b32 v[40:41], v128 offset1:1
	s_mov_b32 m0, s71
	s_waitcnt lgkmcnt(0)
	global_load_lds_dwordx4 v40, s[60:61]
	s_mov_b32 m0, s72
	s_nop 0
	global_load_lds_dwordx4 v41, s[60:61]
	s_waitcnt vmcnt(8)
	s_waitcnt lgkmcnt(0)
	s_barrier
	s_barrier
	ds_read_b128 v[40:43], v194 offset:3072
	ds_read_b128 v[44:47], v194 offset:2048
	ds_read_b128 v[48:51], v194 offset:1024
	ds_read_b128 v[52:55], v194
	ds_read_b128 v[56:59], v195 offset:3072
	ds_read_b128 v[60:63], v195 offset:2048
	ds_read_b128 v[94:97], v195 offset:1024
	ds_read_b128 v[98:101], v195
	ds_read_b128 v[102:105], v184
	ds_read_b128 v[106:109], v184 offset:1024
	ds_read_b128 v[110:113], v184 offset:2048
	ds_read_b128 v[114:117], v184 offset:3072
	ds_read_b128 v[118:121], v184 offset:4096
	ds_read_b128 v[122:125], v184 offset:5120
	ds_read2_b32 v[126:127], v128 offset0:2 offset1:3
	ds_read_b128 v[130:133], v184 offset:6144
	ds_read_b128 v[134:137], v184 offset:7168
	s_mov_b32 m0, s84
	s_waitcnt lgkmcnt(0)
	global_load_lds_dwordx4 v126, s[60:61]
	s_mov_b32 m0, s85
	s_nop 0
	global_load_lds_dwordx4 v127, s[60:61]
	s_waitcnt vmcnt(8)
	s_waitcnt lgkmcnt(0)
	s_barrier
	s_setprio 1
	v_mfma_f32_16x16x32_bf16 v[70:73], v[98:101], v[102:105], v[70:73]
	v_mfma_f32_16x16x32_bf16 v[78:81], v[98:101], v[110:113], v[78:81]
	v_mfma_f32_16x16x32_bf16 v[86:89], v[98:101], v[118:121], v[86:89]
	v_mfma_f32_16x16x32_bf16 v[4:7], v[98:101], v[130:133], v[4:7]
	v_mfma_f32_16x16x32_bf16 v[70:73], v[94:97], v[106:109], v[70:73]
	v_mfma_f32_16x16x32_bf16 v[74:77], v[60:63], v[102:105], v[74:77]
	v_mfma_f32_16x16x32_bf16 v[78:81], v[94:97], v[114:117], v[78:81]
	v_mfma_f32_16x16x32_bf16 v[82:85], v[60:63], v[110:113], v[82:85]
	v_mfma_f32_16x16x32_bf16 v[86:89], v[94:97], v[122:125], v[86:89]
	v_mfma_f32_16x16x32_bf16 v[90:93], v[60:63], v[118:121], v[90:93]
	v_mfma_f32_16x16x32_bf16 v[94:97], v[94:97], v[134:137], v[4:7]
	v_mfma_f32_16x16x32_bf16 v[4:7], v[60:63], v[130:133], v[12:15]
	v_mfma_f32_16x16x32_bf16 v[74:77], v[56:59], v[106:109], v[74:77]
	v_mfma_f32_16x16x32_bf16 v[82:85], v[56:59], v[114:117], v[82:85]
	v_mfma_f32_16x16x32_bf16 v[90:93], v[56:59], v[122:125], v[90:93]
	v_mfma_f32_16x16x32_bf16 v[56:59], v[56:59], v[134:137], v[4:7]
	s_setprio 0
	s_setprio 1
	v_mfma_f32_16x16x32_bf16 v[4:7], v[52:55], v[102:105], v[16:19]
	v_mfma_f32_16x16x32_bf16 v[60:63], v[48:51], v[106:109], v[4:7]
	v_mfma_f32_16x16x32_bf16 v[4:7], v[44:47], v[102:105], v[20:23]
	v_mfma_f32_16x16x32_bf16 v[98:101], v[40:43], v[106:109], v[4:7]
	v_mfma_f32_16x16x32_bf16 v[4:7], v[52:55], v[110:113], v[24:27]
	v_mfma_f32_16x16x32_bf16 v[102:105], v[48:51], v[114:117], v[4:7]
	v_mfma_f32_16x16x32_bf16 v[4:7], v[44:47], v[110:113], v[28:31]
	v_mfma_f32_16x16x32_bf16 v[106:109], v[40:43], v[114:117], v[4:7]
	v_mfma_f32_16x16x32_bf16 v[4:7], v[52:55], v[118:121], v[32:35]
	v_mfma_f32_16x16x32_bf16 v[110:113], v[48:51], v[122:125], v[4:7]
	v_mfma_f32_16x16x32_bf16 v[4:7], v[44:47], v[118:121], v[36:39]
	v_mfma_f32_16x16x32_bf16 v[114:117], v[40:43], v[122:125], v[4:7]
	v_mfma_f32_16x16x32_bf16 v[4:7], v[52:55], v[130:133], v[8:11]
	v_mfma_f32_16x16x32_bf16 v[0:3], v[44:47], v[130:133], v[0:3]
	v_mfma_f32_16x16x32_bf16 v[118:121], v[48:51], v[134:137], v[4:7]
	v_mfma_f32_16x16x32_bf16 v[122:125], v[40:43], v[134:137], v[0:3]
	s_setprio 0
	s_barrier
	s_mov_b64 s[10:11], 0x300
	s_mov_b32 m0, s86
	s_nop 1
	v_lshl_add_u64 v[0:1], v[64:65], 0, s[10:11]
	global_load_lds_dwordx4 v[0:1], off
	v_lshl_add_u64 v[0:1], v[66:67], 0, s[10:11]
	s_add_u32 s10, s4, 0x200300
	s_mov_b32 m0, s87
	s_addc_u32 s11, s5, 0
	global_load_lds_dwordx4 v[0:1], off
	s_mov_b32 m0, s88
	s_nop 0
	global_load_lds_dwordx4 v156, s[10:11]
	s_mov_b32 m0, s89
	s_nop 0
	global_load_lds_dwordx4 v158, s[10:11]
	ds_read2_b32 v[0:1], v128 offset1:1
	s_mov_b32 m0, s67
	s_waitcnt lgkmcnt(0)
	global_load_lds_dwordx4 v0, s[18:19]
	s_mov_b32 m0, s68
	s_nop 0
	global_load_lds_dwordx4 v1, s[18:19]
	s_waitcnt vmcnt(8)
	s_waitcnt lgkmcnt(0)
	s_barrier
	s_barrier
	ds_read_b128 v[24:27], v68
	ds_read_b128 v[28:31], v68 offset:1024
	ds_read_b128 v[32:35], v68 offset:2048
	ds_read_b128 v[36:39], v68 offset:3072
	ds_read_b128 v[130:133], v69
	ds_read_b128 v[134:137], v69 offset:1024
	ds_read_b128 v[138:141], v69 offset:2048
	ds_read_b128 v[142:145], v69 offset:3072
	ds_read_b128 v[40:43], v184 offset:32768
	ds_read_b128 v[44:47], v184 offset:33792
	ds_read_b128 v[48:51], v184 offset:34816
	ds_read_b128 v[52:55], v184 offset:35840
	ds_read_b128 v[146:149], v184 offset:36864
	ds_read_b128 v[162:165], v184 offset:37888
	ds_read2_b32 v[0:1], v128 offset0:2 offset1:3
	ds_read_b128 v[166:169], v184 offset:38912
	ds_read_b128 v[170:173], v184 offset:39936
	s_mov_b32 m0, s69
	s_waitcnt lgkmcnt(0)
	global_load_lds_dwordx4 v0, s[18:19]
	s_mov_b32 m0, s70
	s_nop 0
	global_load_lds_dwordx4 v1, s[18:19]
	s_waitcnt vmcnt(8)
	s_waitcnt lgkmcnt(0)
	s_barrier
	s_setprio 1
	v_mfma_f32_16x16x32_bf16 v[0:3], v[24:27], v[40:43], v[70:73]
	v_mfma_f32_16x16x32_bf16 v[8:11], v[24:27], v[48:51], v[78:81]
	v_mfma_f32_16x16x32_bf16 v[16:19], v[24:27], v[146:149], v[86:89]
	v_mfma_f32_16x16x32_bf16 v[24:27], v[24:27], v[166:169], v[94:97]
	v_mfma_f32_16x16x32_bf16 v[0:3], v[28:31], v[44:47], v[0:3]
	v_mfma_f32_16x16x32_bf16 v[4:7], v[32:35], v[40:43], v[74:77]
	v_mfma_f32_16x16x32_bf16 v[8:11], v[28:31], v[52:55], v[8:11]
	v_mfma_f32_16x16x32_bf16 v[12:15], v[32:35], v[48:51], v[82:85]
	v_mfma_f32_16x16x32_bf16 v[16:19], v[28:31], v[162:165], v[16:19]
	v_mfma_f32_16x16x32_bf16 v[20:23], v[32:35], v[146:149], v[90:93]
	v_mfma_f32_16x16x32_bf16 v[24:27], v[28:31], v[170:173], v[24:27]
	v_mfma_f32_16x16x32_bf16 v[28:31], v[32:35], v[166:169], v[56:59]
	v_mfma_f32_16x16x32_bf16 v[4:7], v[36:39], v[44:47], v[4:7]
	v_mfma_f32_16x16x32_bf16 v[12:15], v[36:39], v[52:55], v[12:15]
	v_mfma_f32_16x16x32_bf16 v[20:23], v[36:39], v[162:165], v[20:23]
	v_mfma_f32_16x16x32_bf16 v[28:31], v[36:39], v[170:173], v[28:31]
	s_setprio 0
	s_setprio 1
	v_mfma_f32_16x16x32_bf16 v[32:35], v[130:133], v[40:43], v[60:63]
	v_mfma_f32_16x16x32_bf16 v[36:39], v[138:141], v[40:43], v[98:101]
	v_mfma_f32_16x16x32_bf16 v[32:35], v[134:137], v[44:47], v[32:35]
	v_mfma_f32_16x16x32_bf16 v[36:39], v[142:145], v[44:47], v[36:39]
	v_mfma_f32_16x16x32_bf16 v[40:43], v[130:133], v[48:51], v[102:105]
	v_mfma_f32_16x16x32_bf16 v[44:47], v[138:141], v[48:51], v[106:109]
	v_mfma_f32_16x16x32_bf16 v[40:43], v[134:137], v[52:55], v[40:43]
	v_mfma_f32_16x16x32_bf16 v[44:47], v[142:145], v[52:55], v[44:47]
	v_mfma_f32_16x16x32_bf16 v[48:51], v[130:133], v[146:149], v[110:113]
	v_mfma_f32_16x16x32_bf16 v[52:55], v[138:141], v[146:149], v[114:117]
	v_mfma_f32_16x16x32_bf16 v[56:59], v[130:133], v[166:169], v[118:121]
	v_mfma_f32_16x16x32_bf16 v[60:63], v[138:141], v[166:169], v[122:125]
	v_mfma_f32_16x16x32_bf16 v[48:51], v[134:137], v[162:165], v[48:51]
	v_mfma_f32_16x16x32_bf16 v[52:55], v[142:145], v[162:165], v[52:55]
	v_mfma_f32_16x16x32_bf16 v[56:59], v[134:137], v[170:173], v[56:59]
	v_mfma_f32_16x16x32_bf16 v[60:63], v[142:145], v[170:173], v[60:63]
	s_setprio 0
	s_barrier
	s_mov_b32 m0, s91
	v_lshl_add_u64 v[64:65], v[64:65], 0, s[54:55]
	s_add_u32 s10, s4, 0x200380
	global_load_lds_dwordx4 v[64:65], off
	v_lshl_add_u64 v[64:65], v[66:67], 0, s[54:55]
	s_mov_b32 m0, s90
	s_addc_u32 s11, s5, 0
	global_load_lds_dwordx4 v[64:65], off
	s_mov_b32 m0, s92
	s_nop 0
	global_load_lds_dwordx4 v156, s[10:11]
	s_mov_b32 m0, s93
	s_nop 0
	global_load_lds_dwordx4 v158, s[10:11]
	ds_read2_b32 v[64:65], v128 offset1:1
	s_mov_b32 m0, s71
	s_waitcnt lgkmcnt(0)
	global_load_lds_dwordx4 v64, s[52:53]
	s_mov_b32 m0, s72
	s_nop 0
	global_load_lds_dwordx4 v65, s[52:53]
	s_waitcnt vmcnt(8)
	s_waitcnt lgkmcnt(0)
	s_barrier
	s_barrier
	s_and_b64 vcc, exec, s[2:3]
	s_cbranch_vccnz .LBB0_2159
	s_and_saveexec_b64 s[10:11], s[0:1]
	s_cbranch_execz .LBB0_2158
	s_lshl_b64 s[12:13], s[8:9], 2
	s_add_u32 s12, s94, s12
	v_readlane_b32 s14, v253, 2
	s_mov_b32 s36, s94
	s_addc_u32 s13, s14, s13
	s_mov_b32 s94, 0x400001
	s_branch .LBB0_2151

.LBB0_2159:
	ds_read_b128 v[64:67], v195
	ds_read_b128 v[70:73], v195 offset:1024
	ds_read_b128 v[74:77], v195 offset:2048
	ds_read_b128 v[78:81], v195 offset:3072
	ds_read_b128 v[82:85], v194
	ds_read_b128 v[86:89], v194 offset:1024
	ds_read_b128 v[90:93], v194 offset:2048
	ds_read_b128 v[94:97], v194 offset:3072
	ds_read_b128 v[98:101], v184
	ds_read_b128 v[102:105], v184 offset:1024
	ds_read_b128 v[106:109], v184 offset:2048
	ds_read_b128 v[110:113], v184 offset:3072
	ds_read_b128 v[114:117], v184 offset:4096
	ds_read_b128 v[118:121], v184 offset:5120
	ds_read2_b32 v[126:127], v128 offset0:2 offset1:3
	ds_read_b128 v[122:125], v184 offset:6144
	ds_read_b128 v[130:133], v184 offset:7168
	s_mov_b32 m0, s84
	s_waitcnt lgkmcnt(0)
	global_load_lds_dwordx4 v126, s[52:53]
	s_mov_b32 m0, s85
	s_nop 0
	global_load_lds_dwordx4 v127, s[52:53]
	s_waitcnt vmcnt(8)
	s_waitcnt lgkmcnt(0)
	s_barrier
	s_setprio 1
	v_mfma_f32_16x16x32_bf16 v[0:3], v[64:67], v[98:101], v[0:3]
	v_mfma_f32_16x16x32_bf16 v[4:7], v[74:77], v[98:101], v[4:7]
	v_mfma_f32_16x16x32_bf16 v[8:11], v[64:67], v[106:109], v[8:11]
	v_mfma_f32_16x16x32_bf16 v[12:15], v[74:77], v[106:109], v[12:15]
	v_mfma_f32_16x16x32_bf16 v[16:19], v[64:67], v[114:117], v[16:19]
	v_mfma_f32_16x16x32_bf16 v[20:23], v[74:77], v[114:117], v[20:23]
	v_mfma_f32_16x16x32_bf16 v[24:27], v[64:67], v[122:125], v[24:27]
	v_mfma_f32_16x16x32_bf16 v[28:31], v[74:77], v[122:125], v[28:31]
	v_mfma_f32_16x16x32_bf16 v[0:3], v[70:73], v[102:105], v[0:3]
	v_mfma_f32_16x16x32_bf16 v[4:7], v[78:81], v[102:105], v[4:7]
	v_mfma_f32_16x16x32_bf16 v[8:11], v[70:73], v[110:113], v[8:11]
	v_mfma_f32_16x16x32_bf16 v[12:15], v[78:81], v[110:113], v[12:15]
	v_mfma_f32_16x16x32_bf16 v[16:19], v[70:73], v[118:121], v[16:19]
	v_mfma_f32_16x16x32_bf16 v[20:23], v[78:81], v[118:121], v[20:23]
	v_mfma_f32_16x16x32_bf16 v[24:27], v[70:73], v[130:133], v[24:27]
	v_mfma_f32_16x16x32_bf16 v[28:31], v[78:81], v[130:133], v[28:31]
	s_setprio 0
	s_setprio 1
	v_mfma_f32_16x16x32_bf16 v[32:35], v[82:85], v[98:101], v[32:35]
	v_mfma_f32_16x16x32_bf16 v[36:39], v[90:93], v[98:101], v[36:39]
	v_mfma_f32_16x16x32_bf16 v[40:43], v[82:85], v[106:109], v[40:43]
	v_mfma_f32_16x16x32_bf16 v[44:47], v[90:93], v[106:109], v[44:47]
	v_mfma_f32_16x16x32_bf16 v[48:51], v[82:85], v[114:117], v[48:51]
	v_mfma_f32_16x16x32_bf16 v[52:55], v[90:93], v[114:117], v[52:55]
	v_mfma_f32_16x16x32_bf16 v[56:59], v[82:85], v[122:125], v[56:59]
	v_mfma_f32_16x16x32_bf16 v[60:63], v[90:93], v[122:125], v[60:63]
	v_mfma_f32_16x16x32_bf16 v[32:35], v[86:89], v[102:105], v[32:35]
	v_mfma_f32_16x16x32_bf16 v[36:39], v[94:97], v[102:105], v[36:39]
	v_mfma_f32_16x16x32_bf16 v[40:43], v[86:89], v[110:113], v[40:43]
	v_mfma_f32_16x16x32_bf16 v[44:47], v[94:97], v[110:113], v[44:47]
	v_mfma_f32_16x16x32_bf16 v[48:51], v[86:89], v[118:121], v[48:51]
	v_mfma_f32_16x16x32_bf16 v[52:55], v[94:97], v[118:121], v[52:55]
	v_mfma_f32_16x16x32_bf16 v[56:59], v[86:89], v[130:133], v[56:59]
	v_mfma_f32_16x16x32_bf16 v[60:63], v[94:97], v[130:133], v[60:63]
	s_setprio 0
	s_barrier
	s_mov_b32 m0, s86
	v_lshl_add_u64 v[150:151], s[56:57], 0, v[156:157]
	s_add_u32 s10, s56, 0x200000
	global_load_lds_dwordx4 v[150:151], off
	v_lshl_add_u64 v[178:179], s[56:57], 0, v[158:159]
	s_mov_b32 m0, s87
	s_addc_u32 s11, s57, 0
	global_load_lds_dwordx4 v[178:179], off
	s_mov_b32 m0, s88
	v_lshl_add_u32 v129, s59, 2, v155
	global_load_lds_dwordx4 v156, s[10:11]
	s_mov_b32 m0, s89
	s_nop 0
	global_load_lds_dwordx4 v158, s[10:11]
	ds_read2_b32 v[64:65], v129 offset1:1
	s_mov_b32 m0, s67
	s_waitcnt lgkmcnt(0)
	global_load_lds_dwordx4 v64, s[26:27]
	s_mov_b32 m0, s68
	s_nop 0
	global_load_lds_dwordx4 v65, s[26:27]
	s_waitcnt vmcnt(8)
	s_waitcnt lgkmcnt(0)
	s_barrier
	s_barrier
	ds_read_b128 v[64:67], v68
	ds_read_b128 v[70:73], v68 offset:1024
	ds_read_b128 v[80:83], v68 offset:2048
	ds_read_b128 v[84:87], v68 offset:3072
	ds_read_b128 v[130:133], v69
	ds_read_b128 v[134:137], v69 offset:1024
	ds_read_b128 v[138:141], v69 offset:2048
	ds_read_b128 v[142:145], v69 offset:3072
	ds_read_b128 v[96:99], v184 offset:32768
	ds_read_b128 v[100:103], v184 offset:33792
	ds_read_b128 v[146:149], v184 offset:34816
	ds_read_b128 v[162:165], v184 offset:35840
	ds_read_b128 v[166:169], v184 offset:36864
	ds_read_b128 v[170:173], v184 offset:37888
	ds_read2_b32 v[68:69], v129 offset0:2 offset1:3
	ds_read_b128 v[174:177], v184 offset:38912
	ds_read_b128 v[196:199], v184 offset:39936
	s_mov_b32 m0, s69
	s_waitcnt lgkmcnt(0)
	global_load_lds_dwordx4 v68, s[26:27]
	s_mov_b32 m0, s70
	s_nop 0
	global_load_lds_dwordx4 v69, s[26:27]
	s_waitcnt vmcnt(8)
	s_waitcnt lgkmcnt(0)
	s_barrier
	s_setprio 1
	v_mfma_f32_16x16x32_bf16 v[0:3], v[64:67], v[96:99], v[0:3]
	v_mfma_f32_16x16x32_bf16 v[124:127], v[70:73], v[100:103], v[0:3]
	v_mfma_f32_16x16x32_bf16 v[0:3], v[80:83], v[96:99], v[4:7]
	v_mfma_f32_16x16x32_bf16 v[120:123], v[84:87], v[100:103], v[0:3]
	v_mfma_f32_16x16x32_bf16 v[0:3], v[64:67], v[146:149], v[8:11]
	v_mfma_f32_16x16x32_bf16 v[108:111], v[70:73], v[162:165], v[0:3]
	v_mfma_f32_16x16x32_bf16 v[0:3], v[80:83], v[146:149], v[12:15]
	v_mfma_f32_16x16x32_bf16 v[104:107], v[84:87], v[162:165], v[0:3]
	v_mfma_f32_16x16x32_bf16 v[0:3], v[64:67], v[166:169], v[16:19]
	v_mfma_f32_16x16x32_bf16 v[92:95], v[70:73], v[170:173], v[0:3]
	v_mfma_f32_16x16x32_bf16 v[0:3], v[80:83], v[166:169], v[20:23]
	v_mfma_f32_16x16x32_bf16 v[88:91], v[84:87], v[170:173], v[0:3]
	v_mfma_f32_16x16x32_bf16 v[0:3], v[64:67], v[174:177], v[24:27]
	v_mfma_f32_16x16x32_bf16 v[76:79], v[70:73], v[196:199], v[0:3]
	v_mfma_f32_16x16x32_bf16 v[0:3], v[80:83], v[174:177], v[28:31]
	v_mfma_f32_16x16x32_bf16 v[72:75], v[84:87], v[196:199], v[0:3]
	s_setprio 0
	s_setprio 1
	v_mfma_f32_16x16x32_bf16 v[0:3], v[130:133], v[96:99], v[32:35]
	v_mfma_f32_16x16x32_bf16 v[116:119], v[134:137], v[100:103], v[0:3]
	v_mfma_f32_16x16x32_bf16 v[0:3], v[138:141], v[96:99], v[36:39]
	v_mfma_f32_16x16x32_bf16 v[112:115], v[142:145], v[100:103], v[0:3]
	v_mfma_f32_16x16x32_bf16 v[0:3], v[130:133], v[146:149], v[40:43]
	v_mfma_f32_16x16x32_bf16 v[100:103], v[134:137], v[162:165], v[0:3]
	v_mfma_f32_16x16x32_bf16 v[0:3], v[138:141], v[146:149], v[44:47]
	v_mfma_f32_16x16x32_bf16 v[96:99], v[142:145], v[162:165], v[0:3]
	v_mfma_f32_16x16x32_bf16 v[0:3], v[130:133], v[166:169], v[48:51]
	v_mfma_f32_16x16x32_bf16 v[84:87], v[134:137], v[170:173], v[0:3]
	v_mfma_f32_16x16x32_bf16 v[0:3], v[138:141], v[166:169], v[52:55]
	v_mfma_f32_16x16x32_bf16 v[80:83], v[142:145], v[170:173], v[0:3]
	v_mfma_f32_16x16x32_bf16 v[0:3], v[130:133], v[174:177], v[56:59]
	v_mfma_f32_16x16x32_bf16 v[68:71], v[134:137], v[196:199], v[0:3]
	v_mfma_f32_16x16x32_bf16 v[0:3], v[138:141], v[174:177], v[60:63]
	v_mfma_f32_16x16x32_bf16 v[64:67], v[142:145], v[196:199], v[0:3]
	s_setprio 0
	s_barrier
	s_mov_b32 m0, s91
	s_nop 3
	v_lshl_add_u64 v[0:1], v[150:151], 0, s[20:21]
	s_add_u32 s10, s56, 0x200080
	global_load_lds_dwordx4 v[0:1], off
	v_lshl_add_u64 v[0:1], v[178:179], 0, s[20:21]
	s_mov_b32 m0, s90
	s_addc_u32 s11, s57, 0
	global_load_lds_dwordx4 v[0:1], off
	s_mov_b32 m0, s92
	s_nop 0
	global_load_lds_dwordx4 v156, s[10:11]
	s_mov_b32 m0, s93
	s_nop 0
	global_load_lds_dwordx4 v158, s[10:11]
	ds_read2_b32 v[0:1], v129 offset1:1
	s_mov_b32 m0, s71
	s_waitcnt lgkmcnt(0)
	global_load_lds_dwordx4 v0, s[22:23]
	s_mov_b32 m0, s72
	s_nop 0
	global_load_lds_dwordx4 v1, s[22:23]
	s_waitcnt vmcnt(8)
	s_waitcnt lgkmcnt(0)
	s_barrier
	s_barrier
	s_mov_b64 s[10:11], 0

.LBB0_2174:
	s_lshl_b32 s85, s84, 7
	s_add_u32 s14, s26, s85
	ds_read_b128 v[130:133], v195
	ds_read_b128 v[134:137], v195 offset:1024
	ds_read_b128 v[138:141], v195 offset:2048
	ds_read_b128 v[142:145], v195 offset:3072
	ds_read_b128 v[146:149], v194
	ds_read_b128 v[162:165], v194 offset:1024
	ds_read_b128 v[166:169], v194 offset:2048
	ds_read_b128 v[170:173], v194 offset:3072
	s_addc_u32 s15, s27, 0
	s_add_u32 s86, s14, 0x100
	s_addc_u32 s87, s15, 0
	s_and_b64 s[12:13], s[10:11], exec
	s_cselect_b32 s13, s27, s87
	s_cselect_b32 s12, s26, s86
	s_add_u32 s85, s4, s85
	s_addc_u32 s86, s5, 0
	s_add_u32 s85, s85, 0x100
	s_addc_u32 s86, s86, 0
	s_and_b64 s[10:11], s[10:11], exec
	s_cselect_b32 s10, s56, s85
	s_cselect_b32 s11, s57, s86
	s_cselect_b32 s85, s59, s17
	ds_read_b128 v[174:177], v184
	ds_read_b128 v[196:199], v184 offset:1024
	ds_read_b128 v[200:203], v184 offset:2048
	ds_read_b128 v[204:207], v184 offset:3072
	ds_read2_b32 v[150:151], v128 offset0:2 offset1:3
	ds_read_b128 v[208:211], v184 offset:4096
	ds_read_b128 v[212:215], v184 offset:5120
	ds_read_b128 v[216:219], v184 offset:6144
	ds_read_b128 v[220:223], v184 offset:7168
	s_waitcnt lgkmcnt(0)
	v_mov_b32_e32 v160, v150
	v_lshl_add_u64 v[178:179], s[14:15], 0, v[160:161]
	v_mov_b32_e32 v160, v151
	v_lshl_add_u64 v[178:179], v[178:179], 0, s[20:21]
	s_add_i32 m0, s67, 0xc000
	v_lshl_add_u64 v[150:151], s[14:15], 0, v[160:161]
	global_load_lds_dwordx4 v[178:179], off
	v_lshl_add_u64 v[150:151], v[150:151], 0, s[20:21]
	s_add_i32 m0, s67, 0xe000
	s_nop 0
	global_load_lds_dwordx4 v[150:151], off
	s_waitcnt vmcnt(8)
	s_waitcnt lgkmcnt(0)
	s_barrier
	s_setprio 1
	v_mfma_f32_16x16x32_bf16 v[124:127], v[130:133], v[174:177], v[124:127]
	v_mfma_f32_16x16x32_bf16 v[120:123], v[138:141], v[174:177], v[120:123]
	v_mfma_f32_16x16x32_bf16 v[108:111], v[130:133], v[200:203], v[108:111]
	v_mfma_f32_16x16x32_bf16 v[104:107], v[138:141], v[200:203], v[104:107]
	v_mfma_f32_16x16x32_bf16 v[92:95], v[130:133], v[208:211], v[92:95]
	v_mfma_f32_16x16x32_bf16 v[88:91], v[138:141], v[208:211], v[88:91]
	v_mfma_f32_16x16x32_bf16 v[76:79], v[130:133], v[216:219], v[76:79]
	v_mfma_f32_16x16x32_bf16 v[72:75], v[138:141], v[216:219], v[72:75]
	v_mfma_f32_16x16x32_bf16 v[124:127], v[134:137], v[196:199], v[124:127]
	v_mfma_f32_16x16x32_bf16 v[120:123], v[142:145], v[196:199], v[120:123]
	v_mfma_f32_16x16x32_bf16 v[108:111], v[134:137], v[204:207], v[108:111]
	v_mfma_f32_16x16x32_bf16 v[104:107], v[142:145], v[204:207], v[104:107]
	v_mfma_f32_16x16x32_bf16 v[92:95], v[134:137], v[212:215], v[92:95]
	v_mfma_f32_16x16x32_bf16 v[88:91], v[142:145], v[212:215], v[88:91]
	v_mfma_f32_16x16x32_bf16 v[76:79], v[134:137], v[220:223], v[76:79]
	v_mfma_f32_16x16x32_bf16 v[72:75], v[142:145], v[220:223], v[72:75]
	s_setprio 0
	s_setprio 1
	v_mfma_f32_16x16x32_bf16 v[116:119], v[146:149], v[174:177], v[116:119]
	v_mfma_f32_16x16x32_bf16 v[112:115], v[166:169], v[174:177], v[112:115]
	v_mfma_f32_16x16x32_bf16 v[100:103], v[146:149], v[200:203], v[100:103]
	v_mfma_f32_16x16x32_bf16 v[96:99], v[166:169], v[200:203], v[96:99]
	v_mfma_f32_16x16x32_bf16 v[84:87], v[146:149], v[208:211], v[84:87]
	v_mfma_f32_16x16x32_bf16 v[80:83], v[166:169], v[208:211], v[80:83]
	v_mfma_f32_16x16x32_bf16 v[68:71], v[146:149], v[216:219], v[68:71]
	v_mfma_f32_16x16x32_bf16 v[64:67], v[166:169], v[216:219], v[64:67]
	v_mfma_f32_16x16x32_bf16 v[116:119], v[162:165], v[196:199], v[116:119]
	v_mfma_f32_16x16x32_bf16 v[112:115], v[170:173], v[196:199], v[112:115]
	v_mfma_f32_16x16x32_bf16 v[100:103], v[162:165], v[204:207], v[100:103]
	v_mfma_f32_16x16x32_bf16 v[96:99], v[170:173], v[204:207], v[96:99]
	v_mfma_f32_16x16x32_bf16 v[84:87], v[162:165], v[212:215], v[84:87]
	v_mfma_f32_16x16x32_bf16 v[80:83], v[170:173], v[212:215], v[80:83]
	v_mfma_f32_16x16x32_bf16 v[68:71], v[162:165], v[220:223], v[68:71]
	v_mfma_f32_16x16x32_bf16 v[64:67], v[170:173], v[220:223], v[64:67]
	s_setprio 0
	s_barrier
	s_add_i32 s14, s75, s66
	v_lshl_add_u64 v[150:151], s[10:11], 0, v[156:157]
	s_mov_b32 m0, s14
	ds_read_b128 v[174:177], v184 offset:16384
	ds_read_b128 v[196:199], v184 offset:17408
	ds_read_b128 v[200:203], v184 offset:18432
	ds_read_b128 v[204:207], v184 offset:19456
	ds_read_b128 v[208:211], v184 offset:20480
	ds_read_b128 v[212:215], v184 offset:21504
	ds_read_b128 v[216:219], v184 offset:22528
	ds_read_b128 v[220:223], v184 offset:23552
	global_load_lds_dwordx4 v[150:151], off
	s_add_i32 m0, s14, 0x2000
	s_add_u32 s14, s10, 0x200000
	v_lshl_add_u64 v[178:179], s[10:11], 0, v[158:159]
	s_addc_u32 s15, s11, 0
	s_add_i32 s86, s74, s66
	global_load_lds_dwordx4 v[178:179], off
	s_mov_b32 m0, s86
	v_lshl_add_u32 v129, s85, 2, v155
	global_load_lds_dwordx4 v156, s[14:15]
	s_add_i32 m0, s86, 0x2000
	s_nop 0
	global_load_lds_dwordx4 v158, s[14:15]
	ds_read2_b32 v[224:225], v129 offset1:1
	s_mov_b32 m0, s67
	s_waitcnt lgkmcnt(0)
	global_load_lds_dwordx4 v224, s[12:13]
	s_mov_b32 m0, s68
	s_nop 0
	global_load_lds_dwordx4 v225, s[12:13]
	s_waitcnt vmcnt(8)
	s_waitcnt lgkmcnt(0)
	s_barrier
	s_setprio 1
	v_mfma_f32_16x16x32_bf16 v[56:59], v[130:133], v[174:177], v[56:59]
	v_mfma_f32_16x16x32_bf16 v[60:63], v[138:141], v[174:177], v[60:63]
	v_mfma_f32_16x16x32_bf16 v[44:47], v[130:133], v[200:203], v[44:47]
	v_mfma_f32_16x16x32_bf16 v[40:43], v[138:141], v[200:203], v[40:43]
	v_mfma_f32_16x16x32_bf16 v[28:31], v[130:133], v[208:211], v[28:31]
	v_mfma_f32_16x16x32_bf16 v[24:27], v[138:141], v[208:211], v[24:27]
	v_mfma_f32_16x16x32_bf16 v[12:15], v[130:133], v[216:219], v[12:15]
	v_mfma_f32_16x16x32_bf16 v[8:11], v[138:141], v[216:219], v[8:11]
	v_mfma_f32_16x16x32_bf16 v[56:59], v[134:137], v[196:199], v[56:59]
	v_mfma_f32_16x16x32_bf16 v[60:63], v[142:145], v[196:199], v[60:63]
	v_mfma_f32_16x16x32_bf16 v[44:47], v[134:137], v[204:207], v[44:47]
	v_mfma_f32_16x16x32_bf16 v[40:43], v[142:145], v[204:207], v[40:43]
	v_mfma_f32_16x16x32_bf16 v[28:31], v[134:137], v[212:215], v[28:31]
	v_mfma_f32_16x16x32_bf16 v[24:27], v[142:145], v[212:215], v[24:27]
	v_mfma_f32_16x16x32_bf16 v[12:15], v[134:137], v[220:223], v[12:15]
	v_mfma_f32_16x16x32_bf16 v[8:11], v[142:145], v[220:223], v[8:11]
	s_setprio 0
	s_setprio 1
	v_mfma_f32_16x16x32_bf16 v[52:55], v[146:149], v[174:177], v[52:55]
	v_mfma_f32_16x16x32_bf16 v[48:51], v[166:169], v[174:177], v[48:51]
	v_mfma_f32_16x16x32_bf16 v[36:39], v[146:149], v[200:203], v[36:39]
	v_mfma_f32_16x16x32_bf16 v[32:35], v[166:169], v[200:203], v[32:35]
	v_mfma_f32_16x16x32_bf16 v[20:23], v[146:149], v[208:211], v[20:23]
	v_mfma_f32_16x16x32_bf16 v[16:19], v[166:169], v[208:211], v[16:19]
	v_mfma_f32_16x16x32_bf16 v[4:7], v[146:149], v[216:219], v[4:7]
	v_mfma_f32_16x16x32_bf16 v[0:3], v[166:169], v[216:219], v[0:3]
	v_mfma_f32_16x16x32_bf16 v[52:55], v[162:165], v[196:199], v[52:55]
	v_mfma_f32_16x16x32_bf16 v[48:51], v[170:173], v[196:199], v[48:51]
	v_mfma_f32_16x16x32_bf16 v[36:39], v[162:165], v[204:207], v[36:39]
	v_mfma_f32_16x16x32_bf16 v[32:35], v[170:173], v[204:207], v[32:35]
	v_mfma_f32_16x16x32_bf16 v[20:23], v[162:165], v[212:215], v[20:23]
	v_mfma_f32_16x16x32_bf16 v[16:19], v[170:173], v[212:215], v[16:19]
	v_mfma_f32_16x16x32_bf16 v[4:7], v[162:165], v[220:223], v[4:7]
	v_mfma_f32_16x16x32_bf16 v[0:3], v[170:173], v[220:223], v[0:3]
	s_setprio 0
	s_barrier
	s_add_i32 s14, 0, 0x18000
	s_add_i32 s15, 0, 0x1c000
	v_add_u32_e32 v142, s14, v181
	v_add_u32_e32 v160, s15, v181
	ds_read_b128 v[130:133], v142
	ds_read_b128 v[134:137], v142 offset:1024
	ds_read_b128 v[138:141], v142 offset:2048
	ds_read_b128 v[142:145], v142 offset:3072
	ds_read_b128 v[146:149], v160
	ds_read_b128 v[162:165], v160 offset:1024
	ds_read_b128 v[166:169], v160 offset:2048
	ds_read_b128 v[170:173], v160 offset:3072
	ds_read_b128 v[174:177], v184 offset:32768
	ds_read_b128 v[196:199], v184 offset:33792
	ds_read_b128 v[200:203], v184 offset:34816
	ds_read_b128 v[204:207], v184 offset:35840
	ds_read_b128 v[208:211], v184 offset:36864
	ds_read_b128 v[212:215], v184 offset:37888
	ds_read2_b32 v[224:225], v129 offset0:2 offset1:3
	ds_read_b128 v[216:219], v184 offset:38912
	ds_read_b128 v[220:223], v184 offset:39936
	s_mov_b32 m0, s69
	s_waitcnt lgkmcnt(0)
	global_load_lds_dwordx4 v224, s[12:13]
	s_mov_b32 m0, s70
	s_nop 0
	global_load_lds_dwordx4 v225, s[12:13]
	s_waitcnt vmcnt(8)
	s_waitcnt lgkmcnt(0)
	s_barrier
	s_setprio 1
	v_mfma_f32_16x16x32_bf16 v[124:127], v[130:133], v[174:177], v[124:127]
	v_mfma_f32_16x16x32_bf16 v[120:123], v[138:141], v[174:177], v[120:123]
	v_mfma_f32_16x16x32_bf16 v[108:111], v[130:133], v[200:203], v[108:111]
	v_mfma_f32_16x16x32_bf16 v[104:107], v[138:141], v[200:203], v[104:107]
	v_mfma_f32_16x16x32_bf16 v[92:95], v[130:133], v[208:211], v[92:95]
	v_mfma_f32_16x16x32_bf16 v[88:91], v[138:141], v[208:211], v[88:91]
	v_mfma_f32_16x16x32_bf16 v[76:79], v[130:133], v[216:219], v[76:79]
	v_mfma_f32_16x16x32_bf16 v[72:75], v[138:141], v[216:219], v[72:75]
	v_mfma_f32_16x16x32_bf16 v[124:127], v[134:137], v[196:199], v[124:127]
	v_mfma_f32_16x16x32_bf16 v[120:123], v[142:145], v[196:199], v[120:123]
	v_mfma_f32_16x16x32_bf16 v[108:111], v[134:137], v[204:207], v[108:111]
	v_mfma_f32_16x16x32_bf16 v[104:107], v[142:145], v[204:207], v[104:107]
	v_mfma_f32_16x16x32_bf16 v[92:95], v[134:137], v[212:215], v[92:95]
	v_mfma_f32_16x16x32_bf16 v[88:91], v[142:145], v[212:215], v[88:91]
	v_mfma_f32_16x16x32_bf16 v[76:79], v[134:137], v[220:223], v[76:79]
	v_mfma_f32_16x16x32_bf16 v[72:75], v[142:145], v[220:223], v[72:75]
	s_setprio 0
	s_setprio 1
	v_mfma_f32_16x16x32_bf16 v[116:119], v[146:149], v[174:177], v[116:119]
	v_mfma_f32_16x16x32_bf16 v[112:115], v[166:169], v[174:177], v[112:115]
	v_mfma_f32_16x16x32_bf16 v[100:103], v[146:149], v[200:203], v[100:103]
	v_mfma_f32_16x16x32_bf16 v[96:99], v[166:169], v[200:203], v[96:99]
	v_mfma_f32_16x16x32_bf16 v[84:87], v[146:149], v[208:211], v[84:87]
	v_mfma_f32_16x16x32_bf16 v[80:83], v[166:169], v[208:211], v[80:83]
	v_mfma_f32_16x16x32_bf16 v[68:71], v[146:149], v[216:219], v[68:71]
	v_mfma_f32_16x16x32_bf16 v[64:67], v[166:169], v[216:219], v[64:67]
	v_mfma_f32_16x16x32_bf16 v[116:119], v[162:165], v[196:199], v[116:119]
	v_mfma_f32_16x16x32_bf16 v[112:115], v[170:173], v[196:199], v[112:115]
	v_mfma_f32_16x16x32_bf16 v[100:103], v[162:165], v[204:207], v[100:103]
	v_mfma_f32_16x16x32_bf16 v[96:99], v[170:173], v[204:207], v[96:99]
	v_mfma_f32_16x16x32_bf16 v[84:87], v[162:165], v[212:215], v[84:87]
	v_mfma_f32_16x16x32_bf16 v[80:83], v[170:173], v[212:215], v[80:83]
	v_mfma_f32_16x16x32_bf16 v[68:71], v[162:165], v[220:223], v[68:71]
	v_mfma_f32_16x16x32_bf16 v[64:67], v[170:173], v[220:223], v[64:67]
	s_setprio 0
	s_barrier
	s_add_i32 s14, s14, s66
	v_lshl_add_u64 v[150:151], v[150:151], 0, s[20:21]
	s_mov_b32 m0, s14
	ds_read_b128 v[174:177], v184 offset:49152
	ds_read_b128 v[196:199], v184 offset:50176
	ds_read_b128 v[200:203], v184 offset:51200
	ds_read_b128 v[204:207], v184 offset:52224
	ds_read_b128 v[208:211], v184 offset:53248
	ds_read_b128 v[212:215], v184 offset:54272
	ds_read_b128 v[216:219], v184 offset:55296
	ds_read_b128 v[220:223], v184 offset:56320
	global_load_lds_dwordx4 v[150:151], off
	s_add_i32 m0, s14, 0x2000
	s_add_u32 s10, s10, 0x200080
	v_lshl_add_u64 v[150:151], v[178:179], 0, s[20:21]
	s_addc_u32 s11, s11, 0
	s_add_i32 s14, s15, s66
	global_load_lds_dwordx4 v[150:151], off
	s_mov_b32 m0, s14
	s_nop 0
	global_load_lds_dwordx4 v156, s[10:11]
	s_add_i32 m0, s14, 0x2000
	s_nop 0
	global_load_lds_dwordx4 v158, s[10:11]
	ds_read2_b32 v[150:151], v129 offset1:1
	s_mov_b32 m0, s71
	s_waitcnt lgkmcnt(0)
	v_mov_b32_e32 v160, v150
	v_lshl_add_u64 v[178:179], s[12:13], 0, v[160:161]
	v_mov_b32_e32 v160, v151
	v_lshl_add_u64 v[178:179], v[178:179], 0, s[20:21]
	v_lshl_add_u64 v[150:151], s[12:13], 0, v[160:161]
	global_load_lds_dwordx4 v[178:179], off
	v_lshl_add_u64 v[150:151], v[150:151], 0, s[20:21]
	s_mov_b32 m0, s72
	s_nop 0
	global_load_lds_dwordx4 v[150:151], off
	s_waitcnt vmcnt(8)
	s_waitcnt lgkmcnt(0)
	s_barrier
	s_setprio 1
	v_mfma_f32_16x16x32_bf16 v[56:59], v[130:133], v[174:177], v[56:59]
	v_mfma_f32_16x16x32_bf16 v[60:63], v[138:141], v[174:177], v[60:63]
	v_mfma_f32_16x16x32_bf16 v[44:47], v[130:133], v[200:203], v[44:47]
	v_mfma_f32_16x16x32_bf16 v[40:43], v[138:141], v[200:203], v[40:43]
	v_mfma_f32_16x16x32_bf16 v[28:31], v[130:133], v[208:211], v[28:31]
	v_mfma_f32_16x16x32_bf16 v[24:27], v[138:141], v[208:211], v[24:27]
	v_mfma_f32_16x16x32_bf16 v[12:15], v[130:133], v[216:219], v[12:15]
	v_mfma_f32_16x16x32_bf16 v[8:11], v[138:141], v[216:219], v[8:11]
	v_mfma_f32_16x16x32_bf16 v[56:59], v[134:137], v[196:199], v[56:59]
	v_mfma_f32_16x16x32_bf16 v[60:63], v[142:145], v[196:199], v[60:63]
	v_mfma_f32_16x16x32_bf16 v[44:47], v[134:137], v[204:207], v[44:47]
	v_mfma_f32_16x16x32_bf16 v[40:43], v[142:145], v[204:207], v[40:43]
	v_mfma_f32_16x16x32_bf16 v[28:31], v[134:137], v[212:215], v[28:31]
	v_mfma_f32_16x16x32_bf16 v[24:27], v[142:145], v[212:215], v[24:27]
	v_mfma_f32_16x16x32_bf16 v[12:15], v[134:137], v[220:223], v[12:15]
	v_mfma_f32_16x16x32_bf16 v[8:11], v[142:145], v[220:223], v[8:11]
	s_setprio 0
	s_setprio 1
	v_mfma_f32_16x16x32_bf16 v[52:55], v[146:149], v[174:177], v[52:55]
	v_mfma_f32_16x16x32_bf16 v[48:51], v[166:169], v[174:177], v[48:51]
	v_mfma_f32_16x16x32_bf16 v[36:39], v[146:149], v[200:203], v[36:39]
	v_mfma_f32_16x16x32_bf16 v[32:35], v[166:169], v[200:203], v[32:35]
	v_mfma_f32_16x16x32_bf16 v[20:23], v[146:149], v[208:211], v[20:23]
	v_mfma_f32_16x16x32_bf16 v[16:19], v[166:169], v[208:211], v[16:19]
	v_mfma_f32_16x16x32_bf16 v[4:7], v[146:149], v[216:219], v[4:7]
	v_mfma_f32_16x16x32_bf16 v[0:3], v[166:169], v[216:219], v[0:3]
	v_mfma_f32_16x16x32_bf16 v[52:55], v[162:165], v[196:199], v[52:55]
	v_mfma_f32_16x16x32_bf16 v[48:51], v[170:173], v[196:199], v[48:51]
	v_mfma_f32_16x16x32_bf16 v[36:39], v[162:165], v[204:207], v[36:39]
	v_mfma_f32_16x16x32_bf16 v[32:35], v[170:173], v[204:207], v[32:35]
	v_mfma_f32_16x16x32_bf16 v[20:23], v[162:165], v[212:215], v[20:23]
	v_mfma_f32_16x16x32_bf16 v[16:19], v[170:173], v[212:215], v[16:19]
	v_mfma_f32_16x16x32_bf16 v[4:7], v[162:165], v[220:223], v[4:7]
	v_mfma_f32_16x16x32_bf16 v[0:3], v[170:173], v[220:223], v[0:3]
	s_setprio 0
	s_barrier
	s_add_i32 s10, s84, 2
	s_cmp_gt_u32 s84, 5
	s_cbranch_scc1 .LBB0_2176
	s_mov_b32 s84, s10
	s_branch .LBB0_2162
